# cross-row butterflies (xor 16 / 32 sums) by v_permlane16/32_swap instead of ds_bpermute in P4, P7, P13 epilogues
# baseline (speedup 1.0000x reference)
; #define LAS __attribute__((address_space(3)))
; __device__ __forceinline__ float wave_max(float v) {
; #pragma unroll
;     for (int o = 1; o < 64; o <<= 1) v = fmaxf(v, __shfl_xor(v, o));
;     return v;
; }
; __device__ __forceinline__ void p3_side_tables(const Params& P, LAS unsigned char* lds, int tid, int lane, int wave, int sb, int nsb) {
;     ...
;         float mx = 0.f, sq = 0.f;
; #pragma unroll
;         for (int j = 0; j < 4; ++j)
; #pragma unroll
;             for (int i = 0; i < 4; ++i) { mx = fmaxf(mx, fabsf(v[j][i])); sq += v[j][i] * v[j][i]; }
;         mx = wave_max(mx);
;         unsigned w0 = 0u, w1 = 0u; float sc;
;         {
;             sc = mx > 0.f ? mx * (1.0f / 6.0f) : 1.0f; const float inv = 1.0f / sc;
;             w0 = __builtin_amdgcn_cvt_scalef32_pk_fp4_f32(w0, v[0][0] * inv, v[0][1] * inv, 1.0f, 0); w0 = __builtin_amdgcn_cvt_scalef32_pk_fp4_f32(w0, v[0][2] * inv, v[0][3] * inv, 1.0f, 1);
;             w0 = __builtin_amdgcn_cvt_scalef32_pk_fp4_f32(w0, v[1][0] * inv, v[1][1] * inv, 1.0f, 2); w0 = __builtin_amdgcn_cvt_scalef32_pk_fp4_f32(w0, v[1][2] * inv, v[1][3] * inv, 1.0f, 3);
;             w1 = __builtin_amdgcn_cvt_scalef32_pk_fp4_f32(w1, v[2][0] * inv, v[2][1] * inv, 1.0f, 0); w1 = __builtin_amdgcn_cvt_scalef32_pk_fp4_f32(w1, v[2][2] * inv, v[2][3] * inv, 1.0f, 1);
;             w1 = __builtin_amdgcn_cvt_scalef32_pk_fp4_f32(w1, v[3][0] * inv, v[3][1] * inv, 1.0f, 2); w1 = __builtin_amdgcn_cvt_scalef32_pk_fp4_f32(w1, v[3][2] * inv, v[3][3] * inv, 1.0f, 3);
;         }
;         unsigned* dst = (unsigned*)(ws + (tb_ ? WS_V4 : WS_U4)) + (size_t)(lane >> 5) * 524288 + (size_t)e * 32 + (lane & 31);
;         if (tb_) {
;             LAS unsigned char* sb = (LAS unsigned char*)scr; const int l5 = lane & 31, s0 = (lane >> 5) * 128, bp = 32 * (l5 & 3) + (l5 >> 2);
;             asm volatile("s_waitcnt lgkmcnt(0)" ::: "memory");
; #pragma unroll
;             for (int b = 0; b < 4; ++b) { sb[s0 + bp + 8 * b] = (unsigned char)(w0 >> (8 * b)); sb[256 + s0 + bp + 8 * b] = (unsigned char)(w1 >> (8 * b)); }
;             asm volatile("s_waitcnt lgkmcnt(0)" ::: "memory");
;             w0 = *(LAS unsigned*)(sb + 4 * lane); w1 = *(LAS unsigned*)(sb + 256 + 4 * lane);
.LBB0_576:
	v_max3_f32 v86, |v42|, 0, |v43|
	v_max3_f32 v86, v86, |v44|, |v45|
	v_max3_f32 v86, v86, |v34|, |v35|
	v_max3_f32 v86, v86, |v36|, |v37|
	v_max3_f32 v86, v86, |v46|, |v47|
	v_max3_f32 v86, v86, |v48|, |v49|
	v_max3_f32 v86, v86, |v38|, |v39|
	v_max3_f32 v86, v86, |v40|, |v41|
	ds_bpermute_b32 v87, v88, v86
	s_waitcnt lgkmcnt(0)
	v_max_f32_e32 v87, v87, v87
	v_max_f32_e32 v86, v86, v87
	ds_bpermute_b32 v87, v89, v86
	s_waitcnt lgkmcnt(0)
	v_max_f32_e32 v87, v87, v87
	v_max_f32_e32 v86, v86, v87
	ds_bpermute_b32 v87, v90, v86
	s_waitcnt lgkmcnt(0)
	v_max_f32_e32 v87, v87, v87
	v_max_f32_e32 v86, v86, v87
	ds_bpermute_b32 v87, v91, v86
	s_waitcnt lgkmcnt(0)
	v_max_f32_e32 v87, v87, v87
	v_max_f32_e32 v86, v86, v87
	v_mov_b32_e32 v87, v86
	s_nop 1
	v_permlane16_swap_b32_e32 v87, v86
	s_waitcnt lgkmcnt(0)
	v_max_f32_e32 v87, v87, v87
	v_max_f32_e32 v96, v86, v87
	v_mov_b32_e32 v97, v96
	s_nop 1
	v_permlane32_swap_b32_e32 v97, v96
	v_mov_b32_e32 v86, 0
	v_mov_b32_e32 v87, 0
	s_waitcnt lgkmcnt(0)
	v_max_f32_e32 v97, v97, v97
	v_max_f32_e32 v96, v96, v97
	v_mul_f32_e32 v97, 0x3e2aaaab, v96
	v_cmp_lt_f32_e32 vcc, 0, v96
	s_nop 1
	v_cndmask_b32_e32 v96, 1.0, v97, vcc
	v_div_scale_f32 v97, s[24:25], v96, v96, 1.0
	v_rcp_f32_e32 v98, v97
	v_div_scale_f32 v99, vcc, 1.0, v96, 1.0
	v_fma_f32 v100, -v97, v98, 1.0
	v_fmac_f32_e32 v98, v100, v98
	v_mul_f32_e32 v100, v99, v98
	v_fma_f32 v101, -v97, v100, v99
	v_fmac_f32_e32 v100, v101, v98
	v_fma_f32 v97, -v97, v100, v99
	v_div_fmas_f32 v97, v97, v98, v100
	v_div_fixup_f32 v97, v97, v96, 1.0
	v_mul_f32_e32 v42, v42, v97
	v_mul_f32_e32 v43, v43, v97
	v_mul_f32_e32 v46, v46, v97
	v_mul_f32_e32 v47, v47, v97
	v_mul_f32_e32 v44, v44, v97
	v_mul_f32_e32 v45, v45, v97
	v_mul_f32_e32 v48, v48, v97
	v_mul_f32_e32 v49, v49, v97
	v_cvt_scalef32_pk_fp4_f32 v86, v42, v43, 1.0
	v_cvt_scalef32_pk_fp4_f32 v87, v46, v47, 1.0
	v_mul_f32_e32 v34, v34, v97
	v_mul_f32_e32 v35, v35, v97
	v_mul_f32_e32 v38, v38, v97
	v_mul_f32_e32 v39, v39, v97
	v_cvt_scalef32_pk_fp4_f32 v86, v44, v45, 1.0 op_sel:[0,0,1,0]
	v_cvt_scalef32_pk_fp4_f32 v87, v48, v49, 1.0 op_sel:[0,0,1,0]
	v_mul_f32_e32 v36, v36, v97
	v_mul_f32_e32 v37, v37, v97
	v_mul_f32_e32 v40, v40, v97
	v_mul_f32_e32 v41, v41, v97
	v_cvt_scalef32_pk_fp4_f32 v86, v34, v35, 1.0 op_sel:[0,0,0,1]
	v_cvt_scalef32_pk_fp4_f32 v87, v38, v39, 1.0 op_sel:[0,0,0,1]
	v_cvt_scalef32_pk_fp4_f32 v86, v36, v37, 1.0 op_sel:[0,0,1,1]
	s_andn2_b64 vcc, exec, s[6:7]
	v_cvt_scalef32_pk_fp4_f32 v87, v40, v41, 1.0 op_sel:[0,0,1,1]
	s_cbranch_vccnz .LBB0_578
	v_lshrrev_b32_e32 v34, 8, v86
	s_waitcnt lgkmcnt(0)
	ds_write_b8 v94, v86
	ds_write_b8 v94, v87 offset:256
	ds_write_b8 v94, v34 offset:8
	v_lshrrev_b32_e32 v34, 8, v87
	ds_write_b8 v94, v34 offset:264
	ds_write_b8_d16_hi v94, v86 offset:16
	ds_write_b8_d16_hi v94, v87 offset:272
	v_lshrrev_b32_e32 v34, 24, v86
	ds_write_b8 v94, v34 offset:24
	v_lshrrev_b32_e32 v34, 24, v87
	ds_write_b8 v94, v34 offset:280
	s_waitcnt lgkmcnt(0)
	ds_read2st64_b32 v[86:87], v95 offset1:1
	s_waitcnt lgkmcnt(0)

; #define LAS __attribute__((address_space(3)))
; __device__ __forceinline__ unsigned pk2(float lo, float hi) { return f2bf(lo) | (f2bf(hi) << 16); }
; __device__ __forceinline__ void p4_mlstm_out(const Params& P, LAS unsigned char* lds, int tid, int lane, int wave, int vb) {
;     ...
;               const float Mt = sm[64 + t]; float p[4], ps = 0.f;
; #pragma unroll
;               for (int k = 0; k < 4; ++k) { const int s = 16 * sb + 4 * g + k; p[k] = (s <= t) ? acc[k] * __expf(sm[s] - Mt) : 0.f; ps += p[k]; }
;               v2u o; o.x = pk2(p[0], p[1]); o.y = pk2(p[2], p[3]); *(LAS v2u*)(PT + t * 72 + 16 * sb + 4 * g) = o;
;               ps += __shfl_xor(ps, 16); ps += __shfl_xor(ps, 32);
;               if (g == 0) sm[320 + sb * 64 + t] = ps; }
.LBB0_830:
	s_or_b64 exec, exec, s[92:93]
	v_add_f32_e32 v46, 0, v74
	v_add_f32_e32 v46, v46, v68
	v_and_b32_e32 v71, 64, v72
	v_add_f32_e32 v70, v46, v73
	v_xor_b32_e32 v46, 16, v72
	v_add_u32_e32 v71, 64, v71
	v_cmp_lt_i32_e32 vcc, v46, v71
	v_xor_b32_e32 v75, 32, v72
	v_add_f32_e32 v70, v70, v69
	v_cndmask_b32_e32 v46, v72, v46, vcc
	v_cmp_lt_i32_e32 vcc, v75, v71
	v_lshlrev_b32_e32 v46, 2, v46
	s_nop 0
	v_cndmask_b32_e32 v71, v72, v75, vcc
	v_and_b32_sdwa v72, v74, v245 dst_sel:DWORD dst_unused:UNUSED_PAD src0_sel:WORD_1 src1_sel:DWORD
	v_add3_u32 v72, v74, v72, s66
	v_mov_b32_e32 v74, v70
	s_nop 1
	v_permlane16_swap_b32_e32 v74, v70
	v_lshlrev_b32_e32 v248, 2, v71
	v_and_b32_sdwa v71, v73, v245 dst_sel:DWORD dst_unused:UNUSED_PAD src0_sel:WORD_1 src1_sel:DWORD
	v_add3_u32 v71, v73, v71, s66
	v_and_b32_sdwa v73, v69, v245 dst_sel:DWORD dst_unused:UNUSED_PAD src0_sel:WORD_1 src1_sel:DWORD
	v_and_b32_sdwa v75, v68, v245 dst_sel:DWORD dst_unused:UNUSED_PAD src0_sel:WORD_1 src1_sel:DWORD
	v_add3_u32 v69, v69, v73, s66
	v_add3_u32 v73, v68, v75, s66
	s_waitcnt lgkmcnt(0)
	v_add_f32_e32 v68, v70, v74
	v_and_b32_e32 v75, 0xffff0000, v69
	v_mov_b32_e32 v69, v68
	s_nop 1
	v_permlane32_swap_b32_e32 v69, v68
	v_and_b32_e32 v70, 0xffff0000, v73
	v_or_b32_sdwa v71, v75, v71 dst_sel:DWORD dst_unused:UNUSED_PAD src0_sel:DWORD src1_sel:WORD_1
	v_or_b32_sdwa v70, v70, v72 dst_sel:DWORD dst_unused:UNUSED_PAD src0_sel:DWORD src1_sel:WORD_1
	ds_write_b64 v247, v[70:71]
	s_and_saveexec_b64 s[92:93], s[14:15]
	s_cbranch_execz .LBB0_832
	s_waitcnt lgkmcnt(1)
	v_add_f32_e32 v68, v68, v69
	ds_write_b32 v177, v68 offset:1280

; #define LAS __attribute__((address_space(3)))
; __device__ __forceinline__ unsigned pk2(float lo, float hi) { return f2bf(lo) | (f2bf(hi) << 16); }
; __device__ __forceinline__ void p4_mlstm_out(const Params& P, LAS unsigned char* lds, int tid, int lane, int wave, int vb) {
;     ...
;               const float Mt = sm[64 + t]; float p[4], ps = 0.f;
; #pragma unroll
;               for (int k = 0; k < 4; ++k) { const int s = 16 * sb + 4 * g + k; p[k] = (s <= t) ? acc[k] * __expf(sm[s] - Mt) : 0.f; ps += p[k]; }
;               v2u o; o.x = pk2(p[0], p[1]); o.y = pk2(p[2], p[3]); *(LAS v2u*)(PT + t * 72 + 16 * sb + 4 * g) = o;
;               ps += __shfl_xor(ps, 16); ps += __shfl_xor(ps, 32);
;               if (g == 0) sm[320 + sb * 64 + t] = ps; }
.LBB0_840:
	s_or_b64 exec, exec, s[92:93]
	v_add_f32_e32 v54, 0, v57
	v_add_f32_e32 v54, v54, v52
	v_add_f32_e32 v54, v54, v56
	v_add_f32_e32 v54, v54, v53
	v_and_b32_sdwa v58, v57, v245 dst_sel:DWORD dst_unused:UNUSED_PAD src0_sel:WORD_1 src1_sel:DWORD
	v_add3_u32 v57, v57, v58, s66
	v_mov_b32_e32 v58, v54
	s_nop 1
	v_permlane16_swap_b32_e32 v58, v54
	v_and_b32_sdwa v55, v56, v245 dst_sel:DWORD dst_unused:UNUSED_PAD src0_sel:WORD_1 src1_sel:DWORD
	v_add3_u32 v55, v56, v55, s66
	v_and_b32_sdwa v56, v53, v245 dst_sel:DWORD dst_unused:UNUSED_PAD src0_sel:WORD_1 src1_sel:DWORD
	v_and_b32_sdwa v59, v52, v245 dst_sel:DWORD dst_unused:UNUSED_PAD src0_sel:WORD_1 src1_sel:DWORD
	v_add3_u32 v53, v53, v56, s66
	v_add3_u32 v56, v52, v59, s66
	s_waitcnt lgkmcnt(0)
	v_add_f32_e32 v52, v54, v58
	v_and_b32_e32 v59, 0xffff0000, v53
	v_mov_b32_e32 v53, v52
	s_nop 1
	v_permlane32_swap_b32_e32 v53, v52
	v_and_b32_e32 v54, 0xffff0000, v56
	v_or_b32_sdwa v55, v59, v55 dst_sel:DWORD dst_unused:UNUSED_PAD src0_sel:DWORD src1_sel:WORD_1
	v_or_b32_sdwa v54, v54, v57 dst_sel:DWORD dst_unused:UNUSED_PAD src0_sel:DWORD src1_sel:WORD_1
	ds_write_b64 v247, v[54:55] offset:2304
	s_and_saveexec_b64 s[92:93], s[14:15]
	s_cbranch_execz .LBB0_842
	s_waitcnt lgkmcnt(1)
	v_add_f32_e32 v52, v52, v53
	ds_write_b32 v177, v52 offset:1344

; __device__ __forceinline__ void p4_mlstm_out(const Params& P, LAS unsigned char* lds, int tid, int lane, int wave, int vb) {
;     ...
;         for (int tb = 0; tb < 4; ++tb) { const int t = 16 * tb + r; const float wi = sm[128 + t]; float s2 = 0.f;
; #pragma unroll
;             for (int k = 0; k < 4; ++k) { ai[tb][k] = wi * ac[tb][k] + ai[tb][k]; s2 += ai[tb][k] * ai[tb][k]; }
;             s2 += __shfl_xor(s2, 16); s2 += __shfl_xor(s2, 32);
;             if (g == 0) sm[576 + wave * 64 + t] = s2; }
.LBB0_892:
	s_nop 2
	ds_read_b32 v86, v182 offset:512
	v_mov_b32_e32 v84, v56
	v_mov_b32_e32 v85, v58
	v_mov_b32_e32 v88, v52
	v_mov_b32_e32 v89, v54
	v_mov_b32_e32 v58, v57
	v_mov_b32_e32 v54, v53
	s_waitcnt lgkmcnt(0)
	v_pk_fma_f32 v[84:85], v[84:85], v[86:87], v[88:89] op_sel_hi:[1,0,1]
	v_pk_fma_f32 v[88:89], v[58:59], v[86:87], v[54:55] op_sel_hi:[1,0,1]
	v_pk_mul_f32 v[90:91], v[84:85], v[84:85]
	v_pk_mul_f32 v[52:53], v[88:89], v[88:89]
	s_nop 0
	v_add_f32_e32 v52, v90, v52
	v_add_f32_e32 v52, v91, v52
	v_add_f32_e32 v52, v53, v52
	v_mov_b32_e32 v53, v52
	s_nop 1
	v_permlane16_swap_b32_e32 v53, v52
	s_waitcnt lgkmcnt(0)
	v_add_f32_e32 v52, v52, v53
	ds_bpermute_b32 v53, v248, v52
	s_and_saveexec_b64 s[56:57], s[14:15]
	s_cbranch_execz .LBB0_894
	s_waitcnt lgkmcnt(0)
	v_add_f32_e32 v52, v52, v53
	ds_write_b32 v192, v52 offset:2304
.LBB0_894:
	s_or_b64 exec, exec, s[56:57]
	ds_read_b32 v52, v185 offset:512
	v_mov_b32_e32 v54, v64
	v_mov_b32_e32 v55, v66
	v_mov_b32_e32 v56, v60
	v_mov_b32_e32 v57, v62
	v_mov_b32_e32 v66, v65
	v_mov_b32_e32 v62, v61
	s_waitcnt lgkmcnt(0)
	v_pk_fma_f32 v[86:87], v[54:55], v[52:53], v[56:57] op_sel_hi:[1,0,1]
	v_pk_fma_f32 v[60:61], v[66:67], v[52:53], v[62:63] op_sel_hi:[1,0,1]
	v_pk_mul_f32 v[54:55], v[86:87], v[86:87]
	v_pk_mul_f32 v[52:53], v[60:61], v[60:61]
	s_nop 0
	v_add_f32_e32 v52, v54, v52
	v_add_f32_e32 v52, v55, v52
	v_add_f32_e32 v52, v53, v52
	v_mov_b32_e32 v53, v52
	s_nop 1
	v_permlane16_swap_b32_e32 v53, v52
	s_waitcnt lgkmcnt(0)
	v_add_f32_e32 v52, v52, v53
	ds_bpermute_b32 v53, v248, v52
	s_and_saveexec_b64 s[56:57], s[14:15]
	s_cbranch_execz .LBB0_896
	s_waitcnt lgkmcnt(0)
	v_add_f32_e32 v52, v52, v53
	ds_write_b32 v192, v52 offset:2368
.LBB0_896:
	s_or_b64 exec, exec, s[56:57]
	ds_read_b32 v52, v188 offset:512
	v_mov_b32_e32 v54, v80
	v_mov_b32_e32 v55, v82
	v_mov_b32_e32 v56, v76
	v_mov_b32_e32 v57, v78
	v_mov_b32_e32 v82, v81
	v_mov_b32_e32 v78, v77
	s_waitcnt lgkmcnt(0)
	v_pk_fma_f32 v[56:57], v[54:55], v[52:53], v[56:57] op_sel_hi:[1,0,1]
	v_pk_fma_f32 v[58:59], v[82:83], v[52:53], v[78:79] op_sel_hi:[1,0,1]
	v_pk_mul_f32 v[54:55], v[56:57], v[56:57]
	v_pk_mul_f32 v[52:53], v[58:59], v[58:59]
	s_nop 0
	v_add_f32_e32 v52, v54, v52
	v_add_f32_e32 v52, v55, v52
	v_add_f32_e32 v52, v53, v52
	v_mov_b32_e32 v53, v52
	s_nop 1
	v_permlane16_swap_b32_e32 v53, v52
	s_waitcnt lgkmcnt(0)
	v_add_f32_e32 v52, v52, v53
	v_mov_b32_e32 v53, v52
	s_nop 1
	v_permlane32_swap_b32_e32 v53, v52
	s_and_saveexec_b64 s[56:57], s[14:15]
	s_cbranch_execz .LBB0_898
	s_waitcnt lgkmcnt(0)
	v_add_f32_e32 v52, v52, v53
	ds_write_b32 v192, v52 offset:2432
.LBB0_898:
	s_or_b64 exec, exec, s[56:57]
	ds_read_b32 v54, v191 offset:512
	v_mov_b32_e32 v52, v72
	s_waitcnt lgkmcnt(1)
	v_mov_b32_e32 v53, v74
	v_mov_b32_e32 v62, v68
	v_mov_b32_e32 v63, v70
	v_mov_b32_e32 v74, v73
	v_mov_b32_e32 v70, v69
	s_waitcnt lgkmcnt(0)
	v_pk_fma_f32 v[52:53], v[52:53], v[54:55], v[62:63] op_sel_hi:[1,0,1]
	v_pk_fma_f32 v[54:55], v[74:75], v[54:55], v[70:71] op_sel_hi:[1,0,1]
	v_pk_mul_f32 v[62:63], v[52:53], v[52:53]
	v_pk_mul_f32 v[64:65], v[54:55], v[54:55]
	s_nop 0
	v_add_f32_e32 v62, v62, v64
	v_add_f32_e32 v62, v63, v62
	v_add_f32_e32 v62, v65, v62
	v_mov_b32_e32 v46, v62
	s_nop 1
	v_permlane16_swap_b32_e32 v46, v62
	s_waitcnt lgkmcnt(0)
	v_add_f32_e32 v46, v62, v46
	v_mov_b32_e32 v62, v46
	s_nop 1
	v_permlane32_swap_b32_e32 v62, v46
	s_and_saveexec_b64 s[56:57], s[14:15]
	s_cbranch_execz .LBB0_900
	s_waitcnt lgkmcnt(0)
	v_add_f32_e32 v46, v46, v62
	ds_write_b32 v193, v46 offset:2304

; #define PG8_RLD(k) do { const float* p_ = rbase + (size_t)(((k) >> 2) * HALF + ((k) & 3) * 16) * 1024; rg[k][0] = *(const f32x4*)p_; rg[k][1] = *(const f32x4*)(p_ + 4); rg[k][2] = *(const f32x4*)(p_ + 32); rg[k][3] = *(const f32x4*)(p_ + 36); } while (0)
;     __device__ __forceinline__ void operator()(f32x4 (&acc)[2][2][4][2], const Unit& u, int wr, int wc, int fr, int fq) const {
;         const float* rbase = res + (size_t)(u.pm * BM + wr * 64 + fr) * 1024 + u.pn * BM + wc * 64 + 8 * fq;
;         f32x4 rg[8][4];
;     ...
;         PG8_RLD(0); PG8_RLD(1);
; #pragma unroll
;         for (int k = 0; k < 8; ++k) { const int ai = k >> 2, m = k & 3;
;             if (k + 2 < 8) PG8_RLD(k + 2);
;             acc[ai][0][m][0] += rg[k][0]; acc[ai][0][m][1] += rg[k][1]; acc[ai][1][m][0] += rg[k][2]; acc[ai][1][m][1] += rg[k][3];
;             asm volatile("" : "+v"(acc[ai][0][m][0]), "+v"(acc[ai][0][m][1]), "+v"(acc[ai][1][m][0]), "+v"(acc[ai][1][m][1]) :: "memory"); }
.LBB0_1074:
	s_lshl_b32 s58, s92, 8
	s_load_dwordx2 s[0:1], s[94:95], 0x0
	s_add_i32 s58, s58, s77
	v_or_b32_e32 v186, s58, v1
	v_ashrrev_i32_e32 v187, 31, v186
	v_lshlrev_b64 v[130:131], 12, v[186:187]
	s_lshl_b32 s56, s20, 8
	s_waitcnt lgkmcnt(0)
	v_lshl_add_u64 v[130:131], s[0:1], 0, v[130:131]
	s_ashr_i32 s57, s56, 31
	v_lshl_add_u64 v[130:131], s[56:57], 2, v[130:131]
	s_lshl_b32 s20, s79, 2
	v_lshl_add_u64 v[130:131], v[130:131], 0, s[20:21]
	v_mov_b32_e32 v185, v175
	v_lshl_add_u64 v[188:189], v[130:131], 0, v[184:185]
	s_mov_b64 s[0:1], 0x10000
	v_lshl_add_u64 v[134:135], v[188:189], 0, s[0:1]
	s_mov_b32 s0, 0x10000
	global_load_dwordx4 v[130:133], v[188:189], off offset:16
	global_load_dwordx4 v[150:153], v[188:189], off
	global_load_dwordx4 v[154:157], v[188:189], off offset:144
	global_load_dwordx4 v[158:161], v[188:189], off offset:128
	v_add_co_u32_e32 v136, vcc, s0, v188
	s_mov_b64 s[0:1], 0x10080
	s_nop 0
	v_addc_co_u32_e32 v137, vcc, 0, v189, vcc
	global_load_dwordx4 v[198:201], v[136:137], off
	global_load_dwordx4 v[202:205], v[134:135], off offset:16
	v_lshl_add_u64 v[134:135], v[188:189], 0, s[0:1]
	global_load_dwordx4 v[206:209], v[136:137], off offset:128
	global_load_dwordx4 v[212:215], v[134:135], off offset:16
	s_mov_b64 s[0:1], 0x20000
	v_lshl_add_u64 v[134:135], v[188:189], 0, s[0:1]
	s_mov_b32 s0, 0x20000
	v_add_co_u32_e32 v142, vcc, s0, v188
	s_mov_b64 s[0:1], 0x20080
	s_nop 0
	v_addc_co_u32_e32 v143, vcc, 0, v189, vcc
	v_lshl_add_u64 v[144:145], v[188:189], 0, s[0:1]
	s_mov_b64 s[0:1], 0x30000
	global_load_dwordx4 v[138:141], v[142:143], off
	s_nop 0
	global_load_dwordx4 v[134:137], v[134:135], off offset:16
	s_nop 0
	global_load_dwordx4 v[146:149], v[142:143], off offset:128
	s_nop 0
	global_load_dwordx4 v[142:145], v[144:145], off offset:16
	s_or_b32 s56, s56, s79
	s_ashr_i32 s57, s56, 31
	s_waitcnt vmcnt(0)
	v_pk_add_f32 v[132:133], v[124:125], v[132:133]
	v_pk_add_f32 v[128:129], v[128:129], v[152:153]
	v_pk_add_f32 v[126:127], v[126:127], v[150:151]
	v_pk_add_f32 v[130:131], v[122:123], v[130:131]
	v_pk_add_f32 v[120:121], v[120:121], v[160:161]
	v_pk_add_f32 v[118:119], v[118:119], v[158:159]
	v_pk_add_f32 v[124:125], v[116:117], v[156:157]
	v_pk_add_f32 v[122:123], v[114:115], v[154:155]
	v_add_co_u32_e32 v116, vcc, s84, v188
	v_lshl_add_u64 v[114:115], v[188:189], 0, s[0:1]
	s_nop 0
	v_addc_co_u32_e32 v117, vcc, 0, v189, vcc
	global_load_dwordx4 v[154:157], v[116:117], off
	global_load_dwordx4 v[150:153], v[114:115], off offset:16
	v_lshl_add_u64 v[114:115], v[188:189], 0, s[36:37]
	global_load_dwordx4 v[162:165], v[116:117], off offset:128
	global_load_dwordx4 v[158:161], v[114:115], off offset:16
	v_pk_add_f32 v[60:61], v[60:61], v[200:201]
	v_pk_add_f32 v[58:59], v[58:59], v[198:199]
	v_pk_add_f32 v[64:65], v[64:65], v[204:205]
	v_pk_add_f32 v[62:63], v[62:63], v[202:203]
	v_pk_add_f32 v[52:53], v[52:53], v[208:209]
	v_pk_add_f32 v[50:51], v[50:51], v[206:207]
	v_pk_add_f32 v[56:57], v[56:57], v[214:215]
	v_pk_add_f32 v[54:55], v[54:55], v[212:213]
	v_add_co_u32_e32 v116, vcc, s85, v188
	v_lshl_add_u64 v[114:115], v[188:189], 0, s[38:39]
	s_nop 0
	v_addc_co_u32_e32 v117, vcc, 0, v189, vcc
	global_load_dwordx4 v[198:201], v[116:117], off
	global_load_dwordx4 v[202:205], v[114:115], off offset:16
	v_lshl_add_u64 v[114:115], v[188:189], 0, s[40:41]
	global_load_dwordx4 v[206:209], v[116:117], off offset:128
	global_load_dwordx4 v[212:215], v[114:115], off offset:16
	v_pk_add_f32 v[106:107], v[106:107], v[138:139]
	v_add_co_u32_e32 v138, vcc, s86, v188
	v_pk_add_f32 v[108:109], v[108:109], v[140:141]
	s_nop 0
	v_addc_co_u32_e32 v139, vcc, 0, v189, vcc
	v_pk_add_f32 v[112:113], v[112:113], v[136:137]
	v_pk_add_f32 v[110:111], v[110:111], v[134:135]
	v_pk_add_f32 v[92:93], v[92:93], v[148:149]
	v_pk_add_f32 v[90:91], v[90:91], v[146:147]
	v_pk_add_f32 v[96:97], v[96:97], v[144:145]
	v_pk_add_f32 v[94:95], v[94:95], v[142:143]
	v_lshl_add_u64 v[114:115], v[188:189], 0, s[42:43]
	v_lshl_add_u64 v[140:141], v[188:189], 0, s[44:45]
	global_load_dwordx4 v[134:137], v[138:139], off
	s_nop 0
	global_load_dwordx4 v[114:117], v[114:115], off offset:16
	s_nop 0
	global_load_dwordx4 v[142:145], v[138:139], off offset:128
	s_nop 0
	global_load_dwordx4 v[138:141], v[140:141], off offset:16
	v_lshl_add_u64 v[146:147], v[188:189], 0, s[46:47]
	s_movk_i32 s0, 0x4000
	s_waitcnt vmcnt(11)
	v_pk_add_f32 v[98:99], v[98:99], v[154:155]
	v_add_co_u32_e32 v154, vcc, s87, v188
	v_pk_add_f32 v[100:101], v[100:101], v[156:157]
	s_waitcnt vmcnt(10)
	v_pk_add_f32 v[104:105], v[104:105], v[152:153]
	v_pk_add_f32 v[102:103], v[102:103], v[150:151]
	s_waitcnt vmcnt(9)
	v_pk_add_f32 v[76:77], v[76:77], v[164:165]
	v_pk_add_f32 v[74:75], v[74:75], v[162:163]
	s_waitcnt vmcnt(8)
	v_pk_add_f32 v[80:81], v[80:81], v[160:161]
	v_pk_add_f32 v[78:79], v[78:79], v[158:159]
	v_addc_co_u32_e32 v155, vcc, 0, v189, vcc
	v_lshl_add_u64 v[156:157], v[188:189], 0, s[48:49]
	global_load_dwordx4 v[150:153], v[154:155], off
	s_nop 0
	global_load_dwordx4 v[146:149], v[146:147], off offset:16
	s_nop 0
	global_load_dwordx4 v[158:161], v[154:155], off offset:128
	s_nop 0
	global_load_dwordx4 v[154:157], v[156:157], off offset:16
	s_waitcnt vmcnt(11)
	v_pk_add_f32 v[84:85], v[84:85], v[200:201]
	v_pk_add_f32 v[82:83], v[82:83], v[198:199]
	s_waitcnt vmcnt(10)
	v_pk_add_f32 v[88:89], v[88:89], v[204:205]
	v_pk_add_f32 v[86:87], v[86:87], v[202:203]
	s_waitcnt vmcnt(9)
	v_pk_add_f32 v[68:69], v[68:69], v[208:209]
	v_pk_add_f32 v[66:67], v[66:67], v[206:207]
	s_waitcnt vmcnt(8)
; __device__ __forceinline__ u32x4 pack8(const f32x4& v0, const f32x4& v1) { u32x4 w; w.x = cvt_pk_bf16(v0[0], v0[1]); w.y = cvt_pk_bf16(v0[2], v0[3]); w.z = cvt_pk_bf16(v1[0], v1[1]); w.w = cvt_pk_bf16(v1[2], v1[3]); return w; }
; __device__ __forceinline__ u32x4 xor8_16B(u32x4 v) { u32x4 r; r.x = (unsigned)__shfl_xor((int)v.x, 8); r.y = (unsigned)__shfl_xor((int)v.y, 8); r.z = (unsigned)__shfl_xor((int)v.z, 8); r.w = (unsigned)__shfl_xor((int)v.w, 8); return r; }
; __device__ __forceinline__ void store_rows_bf16(bf16_t* O, size_t ldc, int r0, int c0, int fr, int fq, u32x4 w0, u32x4 w1) {
;     const bool h = fr & 8; const u32x4 recv = xor8_16B(h ? w0 : w1);
;     const u32x4 d1 = h ? recv : w0, d2 = h ? w1 : recv;
;     const int lane = fr + 16 * fq, src = ((lane >> 3) + 8 * ((lane >> 2) & 1) + 16 * (lane & 3)) * 4;
;     const u32x4 e1 = bperm_16B(src, d1), e2 = bperm_16B(src, d2);
;     bf16_t* p = O + (size_t)(r0 + (lane >> 3)) * ldc + c0 + 8 * (lane & 7);
;     *(u32x4*)p = e1; *(u32x4*)(p + 8 * ldc) = e2;
;     __device__ __forceinline__ void operator()(f32x4 (&acc)[2][2][4][2], const Unit& u, int wr, int wc, int fr, int fq) const {
;     ...
;         for (int k = 0; k < 8; ++k) { const int ai = k >> 2, m = k & 3;
;             if (k + 2 < 8) PG8_RLD(k + 2);
;             acc[ai][0][m][0] += rg[k][0]; acc[ai][0][m][1] += rg[k][1]; acc[ai][1][m][0] += rg[k][2]; acc[ai][1][m][1] += rg[k][3];
;             asm volatile("" : "+v"(acc[ai][0][m][0]), "+v"(acc[ai][0][m][1]), "+v"(acc[ai][1][m][0]), "+v"(acc[ai][1][m][1]) :: "memory"); }
;     ...
; #pragma unroll
;         for (int ai = 0; ai < 2; ++ai)
; #pragma unroll
;             for (int m = 0; m < 4; ++m) { const int row = u.pm * BM + wr * 64 + fr + ai * HALF + m * 16; float s = 0.f; u32x4 wx[2];
; #pragma unroll
;                 for (int bj = 0; bj < 2; ++bj) { const f32x4 v0 = acc[ai][bj][m][0], v1 = acc[ai][bj][m][1];
;                     s += (v0[0] * v0[0] + v0[1] * v0[1]) + (v0[2] * v0[2] + v0[3] * v0[3]) + (v1[0] * v1[0] + v1[1] * v1[1]) + (v1[2] * v1[2] + v1[3] * v1[3]);
;                     wx[bj] = pack8(v0, v1); }
;                 store_rows_bf16(xb, 1024, u.pm * BM + wr * 64 + ai * HALF + m * 16, u.pn * BM + wc * 64, fr, fq, wx[0], wx[1]);
;                 s += __shfl_xor(s, 16); s += __shfl_xor(s, 32);
;                 if (fq == 0) atomicAdd(ssq + row, s);
	v_pk_add_f32 v[72:73], v[72:73], v[214:215]
	v_pk_add_f32 v[70:71], v[70:71], v[212:213]
	v_add_co_u32_e32 v202, vcc, s88, v188
	v_lshl_add_u64 v[198:199], v[188:189], 0, s[50:51]
	s_nop 0
	v_addc_co_u32_e32 v203, vcc, 0, v189, vcc
	global_load_dwordx4 v[162:165], v[202:203], off
	s_nop 0
	global_load_dwordx4 v[198:201], v[198:199], off offset:16
	v_lshl_add_u64 v[188:189], v[188:189], 0, s[52:53]
	global_load_dwordx4 v[202:205], v[202:203], off offset:128
	s_nop 0
	global_load_dwordx4 v[206:209], v[188:189], off offset:16
	s_waitcnt vmcnt(11)
	v_pk_add_f32 v[48:49], v[48:49], v[136:137]
	s_waitcnt vmcnt(10)
	v_pk_add_f32 v[116:117], v[44:45], v[116:117]
	v_pk_add_f32 v[114:115], v[42:43], v[114:115]
	s_waitcnt vmcnt(8)
	v_pk_add_f32 v[44:45], v[36:37], v[140:141]
	v_pk_add_f32 v[42:43], v[34:35], v[138:139]
	v_pk_add_f32 v[46:47], v[46:47], v[134:135]
	v_pk_add_f32 v[40:41], v[40:41], v[144:145]
	v_pk_add_f32 v[38:39], v[38:39], v[142:143]
	s_waitcnt vmcnt(7)
	v_pk_add_f32 v[32:33], v[32:33], v[152:153]
	s_waitcnt vmcnt(6)
	v_pk_add_f32 v[36:37], v[28:29], v[148:149]
	v_pk_add_f32 v[34:35], v[26:27], v[146:147]
	s_waitcnt vmcnt(4)
	v_pk_add_f32 v[28:29], v[20:21], v[156:157]
	v_pk_add_f32 v[26:27], v[18:19], v[154:155]
	v_pk_add_f32 v[30:31], v[30:31], v[150:151]
	v_pk_add_f32 v[24:25], v[24:25], v[160:161]
	v_pk_add_f32 v[22:23], v[22:23], v[158:159]
	s_waitcnt vmcnt(3)
	v_pk_add_f32 v[16:17], v[16:17], v[164:165]
	s_waitcnt vmcnt(2)
	v_pk_add_f32 v[20:21], v[8:9], v[200:201]
	v_pk_add_f32 v[18:19], v[6:7], v[198:199]
	s_waitcnt vmcnt(1)
	v_pk_add_f32 v[8:9], v[12:13], v[204:205]
	v_pk_add_f32 v[6:7], v[10:11], v[202:203]
	v_mul_f32_e32 v11, v127, v127
	v_mul_f32_e32 v12, v129, v129
	v_fmac_f32_e32 v11, v126, v126
	v_fmac_f32_e32 v12, v128, v128
	v_add_f32_e32 v11, v11, v12
	v_mul_f32_e32 v12, v131, v131
	v_fmac_f32_e32 v12, v130, v130
	v_add_f32_e32 v11, v12, v11
	v_mul_f32_e32 v12, v133, v133
	v_pk_add_f32 v[14:15], v[14:15], v[162:163]
	s_waitcnt vmcnt(0)
	v_pk_add_f32 v[4:5], v[4:5], v[208:209]
	v_pk_add_f32 v[2:3], v[2:3], v[206:207]
	v_fmac_f32_e32 v12, v132, v132
	v_add_f32_e32 v11, v12, v11
	v_cvt_pk_bf16_f32 v13, v126, v127
	v_cvt_pk_bf16_f32 v126, v128, v129
	v_mul_f32_e32 v12, v119, v119
	v_mul_f32_e32 v129, v121, v121
	v_fmac_f32_e32 v12, v118, v118
	v_fmac_f32_e32 v129, v120, v120
	v_add_f32_e32 v12, v12, v129
	v_mul_f32_e32 v129, v123, v123
	v_fmac_f32_e32 v129, v122, v122
	v_add_f32_e32 v12, v129, v12
	v_mul_f32_e32 v129, v125, v125
	v_fmac_f32_e32 v129, v124, v124
	v_add_f32_e32 v12, v129, v12
	v_and_b32_e32 v129, 64, v196
	v_cvt_pk_bf16_f32 v127, v130, v131
	v_cvt_pk_bf16_f32 v128, v132, v133
	v_add_f32_e32 v12, v11, v12
	v_cvt_pk_bf16_f32 v11, v118, v119
	v_xor_b32_e32 v118, 8, v196
	v_add_u32_e32 v130, 64, v129
	v_cmp_lt_i32_e32 vcc, v118, v130
	v_cvt_pk_bf16_f32 v119, v120, v121
	v_cvt_pk_bf16_f32 v120, v122, v123
	v_cvt_pk_bf16_f32 v121, v124, v125
	v_cndmask_b32_e64 v125, v13, v11, s[4:5]
	v_cndmask_b32_e64 v122, v128, v121, s[4:5]
	v_cndmask_b32_e32 v118, v196, v118, vcc
	v_cndmask_b32_e64 v123, v127, v120, s[4:5]
	v_cndmask_b32_e64 v124, v126, v119, s[4:5]
	v_lshlrev_b32_e32 v118, 2, v118
	v_mov_b32_dpp v125, v125 row_ror:8 row_mask:0xf bank_mask:0xf
	v_mov_b32_dpp v124, v124 row_ror:8 row_mask:0xf bank_mask:0xf
	v_mov_b32_dpp v123, v123 row_ror:8 row_mask:0xf bank_mask:0xf
	v_mov_b32_dpp v122, v122 row_ror:8 row_mask:0xf bank_mask:0xf
	v_or_b32_e32 v10, s58, v191
	s_waitcnt lgkmcnt(0)
	v_cndmask_b32_e64 v13, v125, v13, s[4:5]
	s_waitcnt lgkmcnt(0)
	v_cndmask_b32_e64 v126, v124, v126, s[4:5]
	s_waitcnt lgkmcnt(0)
	v_cndmask_b32_e64 v127, v123, v127, s[4:5]
	s_waitcnt lgkmcnt(0)
	v_cndmask_b32_e64 v128, v122, v128, s[4:5]
	v_cndmask_b32_e64 v11, v11, v125, s[4:5]
	v_cndmask_b32_e64 v129, v121, v122, s[4:5]
	v_cndmask_b32_e64 v131, v120, v123, s[4:5]
	v_cndmask_b32_e64 v119, v119, v124, s[4:5]
	ds_bpermute_b32 v120, v192, v13
	ds_bpermute_b32 v121, v192, v126
	ds_bpermute_b32 v122, v192, v127
	ds_bpermute_b32 v123, v192, v128
	ds_bpermute_b32 v124, v192, v11
	v_ashrrev_i32_e32 v11, 31, v10
	ds_bpermute_b32 v127, v192, v129
	v_lshlrev_b64 v[128:129], 11, v[10:11]
	v_lshl_add_u64 v[128:129], s[24:25], 0, v[128:129]
	v_lshl_add_u64 v[128:129], s[56:57], 1, v[128:129]
	v_lshl_add_u64 v[128:129], v[128:129], 0, v[174:175]
	s_waitcnt lgkmcnt(2)
	global_store_dwordx4 v[128:129], v[120:123], off
	v_xor_b32_e32 v11, 16, v196
	ds_bpermute_b32 v125, v192, v119
	v_add_co_u32_e32 v120, vcc, s0, v128
	ds_bpermute_b32 v126, v192, v131
	s_nop 0
	v_addc_co_u32_e32 v121, vcc, 0, v129, vcc
	v_cmp_lt_i32_e32 vcc, v11, v130
	s_waitcnt lgkmcnt(0)
	global_store_dwordx4 v[120:121], v[124:127], off
	v_cndmask_b32_e32 v11, v196, v11, vcc
	v_lshlrev_b32_e32 v11, 2, v11
	v_mov_b32_e32 v13, v12
	s_nop 1
	v_permlane16_swap_b32_e32 v13, v12
	s_waitcnt lgkmcnt(0)
	v_add_f32_e32 v120, v12, v13
	v_xor_b32_e32 v12, 32, v196
	v_cmp_lt_i32_e32 vcc, v12, v130
	s_nop 1
	v_cndmask_b32_e32 v12, v196, v12, vcc
	v_lshlrev_b32_e32 v119, 2, v12
	v_mov_b32_e32 v121, v120
	s_nop 1
	v_permlane32_swap_b32_e32 v121, v120
	v_lshl_add_u64 v[12:13], v[186:187], 2, s[26:27]
	s_and_saveexec_b64 s[58:59], s[6:7]
	s_cbranch_execz .LBB0_1076
	s_waitcnt lgkmcnt(0)
	v_add_f32_e32 v120, v120, v121
	global_atomic_add_f32 v[12:13], v120, off
; __device__ __forceinline__ u32x4 pack8(const f32x4& v0, const f32x4& v1) { u32x4 w; w.x = cvt_pk_bf16(v0[0], v0[1]); w.y = cvt_pk_bf16(v0[2], v0[3]); w.z = cvt_pk_bf16(v1[0], v1[1]); w.w = cvt_pk_bf16(v1[2], v1[3]); return w; }
; __device__ __forceinline__ u32x4 xor8_16B(u32x4 v) { u32x4 r; r.x = (unsigned)__shfl_xor((int)v.x, 8); r.y = (unsigned)__shfl_xor((int)v.y, 8); r.z = (unsigned)__shfl_xor((int)v.z, 8); r.w = (unsigned)__shfl_xor((int)v.w, 8); return r; }
; __device__ __forceinline__ u32x4 bperm_16B(int src_byte, u32x4 v) { u32x4 r; r.x = (unsigned)__builtin_amdgcn_ds_bpermute(src_byte, (int)v.x); r.y = (unsigned)__builtin_amdgcn_ds_bpermute(src_byte, (int)v.y); r.z = (unsigned)__builtin_amdgcn_ds_bpermute(src_byte, (int)v.z); r.w = (unsigned)__builtin_amdgcn_ds_bpermute(src_byte, (int)v.w); return r; }
; __device__ __forceinline__ void store_rows_bf16(bf16_t* O, size_t ldc, int r0, int c0, int fr, int fq, u32x4 w0, u32x4 w1) {
;     const bool h = fr & 8; const u32x4 recv = xor8_16B(h ? w0 : w1);
;     const u32x4 d1 = h ? recv : w0, d2 = h ? w1 : recv;
;     const int lane = fr + 16 * fq, src = ((lane >> 3) + 8 * ((lane >> 2) & 1) + 16 * (lane & 3)) * 4;
;     const u32x4 e1 = bperm_16B(src, d1), e2 = bperm_16B(src, d2);
;     bf16_t* p = O + (size_t)(r0 + (lane >> 3)) * ldc + c0 + 8 * (lane & 7);
;     *(u32x4*)p = e1; *(u32x4*)(p + 8 * ldc) = e2;
;     __device__ __forceinline__ void operator()(f32x4 (&acc)[2][2][4][2], const Unit& u, int wr, int wc, int fr, int fq) const {
;     ...
;             for (int m = 0; m < 4; ++m) { const int row = u.pm * BM + wr * 64 + fr + ai * HALF + m * 16; float s = 0.f; u32x4 wx[2];
; #pragma unroll
;                 for (int bj = 0; bj < 2; ++bj) { const f32x4 v0 = acc[ai][bj][m][0], v1 = acc[ai][bj][m][1];
;                     s += (v0[0] * v0[0] + v0[1] * v0[1]) + (v0[2] * v0[2] + v0[3] * v0[3]) + (v1[0] * v1[0] + v1[1] * v1[1]) + (v1[2] * v1[2] + v1[3] * v1[3]);
;                     wx[bj] = pack8(v0, v1); }
;                 store_rows_bf16(xb, 1024, u.pm * BM + wr * 64 + ai * HALF + m * 16, u.pn * BM + wc * 64, fr, fq, wx[0], wx[1]);
;                 s += __shfl_xor(s, 16); s += __shfl_xor(s, 32);
;                 if (fq == 0) atomicAdd(ssq + row, s);
.LBB0_1076:
	s_or_b64 exec, exec, s[58:59]
	v_mul_f32_e32 v120, v59, v59
	s_waitcnt lgkmcnt(0)
	v_mul_f32_e32 v121, v61, v61
	v_fmac_f32_e32 v120, v58, v58
	v_fmac_f32_e32 v121, v60, v60
	v_add_f32_e32 v120, v120, v121
	v_mul_f32_e32 v121, v63, v63
	v_fmac_f32_e32 v121, v62, v62
	v_cvt_pk_bf16_f32 v58, v58, v59
	v_cvt_pk_bf16_f32 v59, v60, v61
	v_cvt_pk_bf16_f32 v60, v62, v63
	v_mul_f32_e32 v62, v51, v51
	v_mul_f32_e32 v63, v53, v53
	v_fmac_f32_e32 v62, v50, v50
	v_fmac_f32_e32 v63, v52, v52
	v_add_f32_e32 v62, v62, v63
	v_mul_f32_e32 v63, v55, v55
	v_fmac_f32_e32 v63, v54, v54
	v_cvt_pk_bf16_f32 v61, v64, v65
	v_add_f32_e32 v62, v63, v62
	v_mul_f32_e32 v63, v57, v57
	v_cvt_pk_bf16_f32 v50, v50, v51
	v_cvt_pk_bf16_f32 v51, v52, v53
	v_cvt_pk_bf16_f32 v52, v54, v55
	v_cvt_pk_bf16_f32 v53, v56, v57
	v_fmac_f32_e32 v63, v56, v56
	v_cndmask_b32_e64 v57, v58, v50, s[4:5]
	v_cndmask_b32_e64 v54, v61, v53, s[4:5]
	v_cndmask_b32_e64 v55, v60, v52, s[4:5]
	v_cndmask_b32_e64 v56, v59, v51, s[4:5]
	v_mov_b32_dpp v57, v57 row_ror:8 row_mask:0xf bank_mask:0xf
	v_mov_b32_dpp v54, v54 row_ror:8 row_mask:0xf bank_mask:0xf
	v_mov_b32_dpp v55, v55 row_ror:8 row_mask:0xf bank_mask:0xf
	v_mov_b32_dpp v56, v56 row_ror:8 row_mask:0xf bank_mask:0xf
	v_add_f32_e32 v120, v121, v120
	v_mul_f32_e32 v121, v65, v65
	v_fmac_f32_e32 v121, v64, v64
	v_add_f32_e32 v120, v121, v120
	v_add_f32_e32 v62, v63, v62
	s_waitcnt lgkmcnt(0)
	v_cndmask_b32_e64 v58, v57, v58, s[4:5]
	v_add_f32_e32 v62, v120, v62
	s_waitcnt lgkmcnt(0)
	v_cndmask_b32_e64 v61, v54, v61, s[4:5]
	s_waitcnt lgkmcnt(0)
	v_cndmask_b32_e64 v60, v55, v60, s[4:5]
	s_waitcnt lgkmcnt(0)
	v_cndmask_b32_e64 v59, v56, v59, s[4:5]
	v_cndmask_b32_e64 v63, v53, v54, s[4:5]
	v_cndmask_b32_e64 v54, v50, v57, s[4:5]
	ds_bpermute_b32 v50, v192, v58
	v_or_b32_e32 v58, 16, v10
	v_cndmask_b32_e64 v64, v52, v55, s[4:5]
	v_cndmask_b32_e64 v55, v51, v56, s[4:5]
	ds_bpermute_b32 v51, v192, v59
	ds_bpermute_b32 v52, v192, v60
	ds_bpermute_b32 v53, v192, v61
	v_ashrrev_i32_e32 v59, 31, v58
	v_mov_b32_e32 v60, v62
	s_nop 1
	v_permlane16_swap_b32_e32 v60, v62
	v_lshlrev_b64 v[58:59], 11, v[58:59]
	v_lshl_add_u64 v[58:59], s[24:25], 0, v[58:59]
	v_lshl_add_u64 v[58:59], s[56:57], 1, v[58:59]
	v_lshl_add_u64 v[58:59], v[58:59], 0, v[174:175]
	s_waitcnt lgkmcnt(0)
	global_store_dwordx4 v[58:59], v[50:53], off
	ds_bpermute_b32 v54, v192, v54
	ds_bpermute_b32 v55, v192, v55
	s_waitcnt lgkmcnt(2)
	v_add_f32_e32 v50, v62, v60
	ds_bpermute_b32 v56, v192, v64
	ds_bpermute_b32 v57, v192, v63
	v_mov_b32_e32 v51, v50
	s_nop 1
	v_permlane32_swap_b32_e32 v51, v50
	v_add_co_u32_e32 v52, vcc, 0x4000, v58
	s_nop 1
	v_addc_co_u32_e32 v53, vcc, 0, v59, vcc
	s_waitcnt lgkmcnt(0)
	global_store_dwordx4 v[52:53], v[54:57], off
	s_and_saveexec_b64 s[58:59], s[6:7]
	s_cbranch_execz .LBB0_1078
	s_waitcnt lgkmcnt(0)
	v_add_f32_e32 v50, v50, v51
	global_atomic_add_f32 v[12:13], v50, off offset:64
.LBB0_1078:
	s_or_b64 exec, exec, s[58:59]
	v_mul_f32_e32 v50, v107, v107
	s_waitcnt lgkmcnt(0)
	v_mul_f32_e32 v51, v109, v109
	v_mul_f32_e32 v55, v91, v91
	v_mul_f32_e32 v56, v93, v93
	v_fmac_f32_e32 v50, v106, v106
	v_fmac_f32_e32 v51, v108, v108
	v_fmac_f32_e32 v55, v90, v90
	v_fmac_f32_e32 v56, v92, v92
	v_add_f32_e32 v50, v50, v51
	v_mul_f32_e32 v51, v111, v111
	v_add_f32_e32 v55, v55, v56
	v_mul_f32_e32 v56, v95, v95
	v_fmac_f32_e32 v51, v110, v110
	v_fmac_f32_e32 v56, v94, v94
	v_add_f32_e32 v50, v51, v50
	v_mul_f32_e32 v51, v113, v113
	v_add_f32_e32 v55, v56, v55
	v_mul_f32_e32 v56, v97, v97
	v_fmac_f32_e32 v51, v112, v112
	v_fmac_f32_e32 v56, v96, v96
	v_add_f32_e32 v50, v51, v50
	v_cvt_pk_bf16_f32 v51, v106, v107
	v_cvt_pk_bf16_f32 v52, v108, v109
	v_cvt_pk_bf16_f32 v53, v110, v111
	v_cvt_pk_bf16_f32 v54, v112, v113
	v_add_f32_e32 v55, v56, v55
	v_cvt_pk_bf16_f32 v56, v90, v91
	v_cvt_pk_bf16_f32 v57, v92, v93
	v_cvt_pk_bf16_f32 v58, v94, v95
	v_cvt_pk_bf16_f32 v59, v96, v97
	v_add_f32_e32 v64, v50, v55
	v_cndmask_b32_e64 v60, v54, v59, s[4:5]
	v_cndmask_b32_e64 v61, v53, v58, s[4:5]
	v_cndmask_b32_e64 v62, v52, v57, s[4:5]
	v_cndmask_b32_e64 v63, v51, v56, s[4:5]
	v_mov_b32_dpp v60, v60 row_ror:8 row_mask:0xf bank_mask:0xf
	v_mov_b32_dpp v61, v61 row_ror:8 row_mask:0xf bank_mask:0xf
	v_mov_b32_dpp v62, v62 row_ror:8 row_mask:0xf bank_mask:0xf
	v_mov_b32_dpp v63, v63 row_ror:8 row_mask:0xf bank_mask:0xf
	s_waitcnt lgkmcnt(0)
	v_cndmask_b32_e64 v54, v60, v54, s[4:5]
	s_waitcnt lgkmcnt(0)
	v_cndmask_b32_e64 v53, v61, v53, s[4:5]
	s_waitcnt lgkmcnt(0)
	v_cndmask_b32_e64 v52, v62, v52, s[4:5]
	v_cndmask_b32_e64 v58, v58, v61, s[4:5]
	s_waitcnt lgkmcnt(0)
	v_cndmask_b32_e64 v56, v56, v63, s[4:5]
	v_cndmask_b32_e64 v50, v63, v51, s[4:5]
	v_cndmask_b32_e64 v59, v59, v60, s[4:5]
	ds_bpermute_b32 v51, v192, v52
	ds_bpermute_b32 v52, v192, v53
	ds_bpermute_b32 v53, v192, v54
	ds_bpermute_b32 v54, v192, v56
	ds_bpermute_b32 v56, v192, v58
	v_or_b32_e32 v58, 32, v10
	v_cndmask_b32_e64 v55, v57, v62, s[4:5]
	ds_bpermute_b32 v50, v192, v50
	ds_bpermute_b32 v57, v192, v59
	v_ashrrev_i32_e32 v59, 31, v58
	v_mov_b32_e32 v60, v64
	s_nop 1
	v_permlane16_swap_b32_e32 v60, v64
	v_lshlrev_b64 v[58:59], 11, v[58:59]
	v_lshl_add_u64 v[58:59], s[24:25], 0, v[58:59]
	v_lshl_add_u64 v[58:59], s[56:57], 1, v[58:59]
	v_lshl_add_u64 v[58:59], v[58:59], 0, v[174:175]
	s_waitcnt lgkmcnt(1)
	global_store_dwordx4 v[58:59], v[50:53], off
	ds_bpermute_b32 v55, v192, v55
	s_waitcnt lgkmcnt(1)
	v_add_f32_e32 v50, v64, v60
	v_mov_b32_e32 v51, v50
	s_nop 1
	v_permlane32_swap_b32_e32 v51, v50
	v_add_co_u32_e32 v52, vcc, 0x4000, v58
	s_nop 1
	v_addc_co_u32_e32 v53, vcc, 0, v59, vcc
	s_waitcnt lgkmcnt(0)
	global_store_dwordx4 v[52:53], v[54:57], off
	s_and_saveexec_b64 s[58:59], s[6:7]
	s_cbranch_execz .LBB0_1080
	s_waitcnt lgkmcnt(0)
	v_add_f32_e32 v50, v50, v51
	global_atomic_add_f32 v[12:13], v50, off offset:128
; __device__ __forceinline__ u32x4 pack8(const f32x4& v0, const f32x4& v1) { u32x4 w; w.x = cvt_pk_bf16(v0[0], v0[1]); w.y = cvt_pk_bf16(v0[2], v0[3]); w.z = cvt_pk_bf16(v1[0], v1[1]); w.w = cvt_pk_bf16(v1[2], v1[3]); return w; }
; __device__ __forceinline__ u32x4 xor8_16B(u32x4 v) { u32x4 r; r.x = (unsigned)__shfl_xor((int)v.x, 8); r.y = (unsigned)__shfl_xor((int)v.y, 8); r.z = (unsigned)__shfl_xor((int)v.z, 8); r.w = (unsigned)__shfl_xor((int)v.w, 8); return r; }
; __device__ __forceinline__ u32x4 bperm_16B(int src_byte, u32x4 v) { u32x4 r; r.x = (unsigned)__builtin_amdgcn_ds_bpermute(src_byte, (int)v.x); r.y = (unsigned)__builtin_amdgcn_ds_bpermute(src_byte, (int)v.y); r.z = (unsigned)__builtin_amdgcn_ds_bpermute(src_byte, (int)v.z); r.w = (unsigned)__builtin_amdgcn_ds_bpermute(src_byte, (int)v.w); return r; }
; __device__ __forceinline__ void store_rows_bf16(bf16_t* O, size_t ldc, int r0, int c0, int fr, int fq, u32x4 w0, u32x4 w1) {
;     const bool h = fr & 8; const u32x4 recv = xor8_16B(h ? w0 : w1);
;     const u32x4 d1 = h ? recv : w0, d2 = h ? w1 : recv;
;     const int lane = fr + 16 * fq, src = ((lane >> 3) + 8 * ((lane >> 2) & 1) + 16 * (lane & 3)) * 4;
;     const u32x4 e1 = bperm_16B(src, d1), e2 = bperm_16B(src, d2);
;     bf16_t* p = O + (size_t)(r0 + (lane >> 3)) * ldc + c0 + 8 * (lane & 7);
;     *(u32x4*)p = e1; *(u32x4*)(p + 8 * ldc) = e2;
;     __device__ __forceinline__ void operator()(f32x4 (&acc)[2][2][4][2], const Unit& u, int wr, int wc, int fr, int fq) const {
;     ...
;             for (int m = 0; m < 4; ++m) { const int row = u.pm * BM + wr * 64 + fr + ai * HALF + m * 16; float s = 0.f; u32x4 wx[2];
; #pragma unroll
;                 for (int bj = 0; bj < 2; ++bj) { const f32x4 v0 = acc[ai][bj][m][0], v1 = acc[ai][bj][m][1];
;                     s += (v0[0] * v0[0] + v0[1] * v0[1]) + (v0[2] * v0[2] + v0[3] * v0[3]) + (v1[0] * v1[0] + v1[1] * v1[1]) + (v1[2] * v1[2] + v1[3] * v1[3]);
;                     wx[bj] = pack8(v0, v1); }
;                 store_rows_bf16(xb, 1024, u.pm * BM + wr * 64 + ai * HALF + m * 16, u.pn * BM + wc * 64, fr, fq, wx[0], wx[1]);
;                 s += __shfl_xor(s, 16); s += __shfl_xor(s, 32);
;                 if (fq == 0) atomicAdd(ssq + row, s);
.LBB0_1080:
	s_or_b64 exec, exec, s[58:59]
	v_mul_f32_e32 v50, v99, v99
	s_waitcnt lgkmcnt(0)
	v_mul_f32_e32 v51, v101, v101
	v_mul_f32_e32 v55, v75, v75
	v_mul_f32_e32 v56, v77, v77
	v_fmac_f32_e32 v50, v98, v98
	v_fmac_f32_e32 v51, v100, v100
	v_fmac_f32_e32 v55, v74, v74
	v_fmac_f32_e32 v56, v76, v76
	v_add_f32_e32 v50, v50, v51
	v_mul_f32_e32 v51, v103, v103
	v_add_f32_e32 v55, v55, v56
	v_mul_f32_e32 v56, v79, v79
	v_fmac_f32_e32 v51, v102, v102
	v_fmac_f32_e32 v56, v78, v78
	v_add_f32_e32 v50, v51, v50
	v_mul_f32_e32 v51, v105, v105
	v_add_f32_e32 v55, v56, v55
	v_mul_f32_e32 v56, v81, v81
	v_fmac_f32_e32 v51, v104, v104
	v_fmac_f32_e32 v56, v80, v80
	v_add_f32_e32 v50, v51, v50
	v_cvt_pk_bf16_f32 v51, v98, v99
	v_cvt_pk_bf16_f32 v52, v100, v101
	v_cvt_pk_bf16_f32 v53, v102, v103
	v_cvt_pk_bf16_f32 v54, v104, v105
	v_add_f32_e32 v55, v56, v55
	v_cvt_pk_bf16_f32 v56, v74, v75
	v_cvt_pk_bf16_f32 v57, v76, v77
	v_cvt_pk_bf16_f32 v58, v78, v79
	v_cvt_pk_bf16_f32 v59, v80, v81
	v_add_f32_e32 v64, v50, v55
	v_cndmask_b32_e64 v60, v54, v59, s[4:5]
	v_cndmask_b32_e64 v61, v53, v58, s[4:5]
	v_cndmask_b32_e64 v62, v52, v57, s[4:5]
	v_cndmask_b32_e64 v63, v51, v56, s[4:5]
	v_mov_b32_dpp v60, v60 row_ror:8 row_mask:0xf bank_mask:0xf
	v_mov_b32_dpp v61, v61 row_ror:8 row_mask:0xf bank_mask:0xf
	v_mov_b32_dpp v62, v62 row_ror:8 row_mask:0xf bank_mask:0xf
	v_mov_b32_dpp v63, v63 row_ror:8 row_mask:0xf bank_mask:0xf
	s_waitcnt lgkmcnt(0)
	v_cndmask_b32_e64 v54, v60, v54, s[4:5]
	s_waitcnt lgkmcnt(0)
	v_cndmask_b32_e64 v53, v61, v53, s[4:5]
	s_waitcnt lgkmcnt(0)
	v_cndmask_b32_e64 v52, v62, v52, s[4:5]
	v_cndmask_b32_e64 v58, v58, v61, s[4:5]
	s_waitcnt lgkmcnt(0)
	v_cndmask_b32_e64 v56, v56, v63, s[4:5]
	v_cndmask_b32_e64 v50, v63, v51, s[4:5]
	v_cndmask_b32_e64 v59, v59, v60, s[4:5]
	ds_bpermute_b32 v51, v192, v52
	ds_bpermute_b32 v52, v192, v53
	ds_bpermute_b32 v53, v192, v54
	ds_bpermute_b32 v54, v192, v56
	ds_bpermute_b32 v56, v192, v58
	v_or_b32_e32 v58, 48, v10
	v_cndmask_b32_e64 v55, v57, v62, s[4:5]
	ds_bpermute_b32 v50, v192, v50
	ds_bpermute_b32 v57, v192, v59
	v_ashrrev_i32_e32 v59, 31, v58
	v_mov_b32_e32 v60, v64
	s_nop 1
	v_permlane16_swap_b32_e32 v60, v64
	v_lshlrev_b64 v[58:59], 11, v[58:59]
	v_lshl_add_u64 v[58:59], s[24:25], 0, v[58:59]
	v_lshl_add_u64 v[58:59], s[56:57], 1, v[58:59]
	v_lshl_add_u64 v[58:59], v[58:59], 0, v[174:175]
	s_waitcnt lgkmcnt(1)
	global_store_dwordx4 v[58:59], v[50:53], off
	ds_bpermute_b32 v55, v192, v55
	s_waitcnt lgkmcnt(1)
	v_add_f32_e32 v50, v64, v60
	v_mov_b32_e32 v51, v50
	s_nop 1
	v_permlane32_swap_b32_e32 v51, v50
	v_add_co_u32_e32 v52, vcc, 0x4000, v58
	s_nop 1
	v_addc_co_u32_e32 v53, vcc, 0, v59, vcc
	s_waitcnt lgkmcnt(0)
	global_store_dwordx4 v[52:53], v[54:57], off
	s_and_saveexec_b64 s[58:59], s[6:7]
	s_cbranch_execz .LBB0_1082
	s_waitcnt lgkmcnt(0)
	v_add_f32_e32 v50, v50, v51
	global_atomic_add_f32 v[12:13], v50, off offset:192
.LBB0_1082:
	s_or_b64 exec, exec, s[58:59]
	v_mul_f32_e32 v50, v83, v83
	s_waitcnt lgkmcnt(0)
	v_mul_f32_e32 v51, v85, v85
	v_mul_f32_e32 v55, v67, v67
	v_mul_f32_e32 v56, v69, v69
	v_fmac_f32_e32 v50, v82, v82
	v_fmac_f32_e32 v51, v84, v84
	v_fmac_f32_e32 v55, v66, v66
	v_fmac_f32_e32 v56, v68, v68
	v_add_f32_e32 v50, v50, v51
	v_mul_f32_e32 v51, v87, v87
	v_add_f32_e32 v55, v55, v56
	v_mul_f32_e32 v56, v71, v71
	v_fmac_f32_e32 v51, v86, v86
	v_fmac_f32_e32 v56, v70, v70
	v_add_f32_e32 v50, v51, v50
	v_mul_f32_e32 v51, v89, v89
	v_add_f32_e32 v55, v56, v55
	v_mul_f32_e32 v56, v73, v73
	v_fmac_f32_e32 v51, v88, v88
	v_fmac_f32_e32 v56, v72, v72
	v_add_f32_e32 v50, v51, v50
	v_cvt_pk_bf16_f32 v51, v82, v83
	v_cvt_pk_bf16_f32 v52, v84, v85
	v_cvt_pk_bf16_f32 v53, v86, v87
	v_cvt_pk_bf16_f32 v54, v88, v89
	v_add_f32_e32 v55, v56, v55
	v_cvt_pk_bf16_f32 v56, v66, v67
	v_cvt_pk_bf16_f32 v57, v68, v69
	v_cvt_pk_bf16_f32 v59, v70, v71
	v_cvt_pk_bf16_f32 v60, v72, v73
	v_add_u32_e32 v58, 0x80, v10
	v_cndmask_b32_e64 v61, v54, v60, s[4:5]
	v_cndmask_b32_e64 v62, v53, v59, s[4:5]
	v_cndmask_b32_e64 v63, v52, v57, s[4:5]
	v_cndmask_b32_e64 v64, v51, v56, s[4:5]
	v_mov_b32_dpp v61, v61 row_ror:8 row_mask:0xf bank_mask:0xf
	v_mov_b32_dpp v62, v62 row_ror:8 row_mask:0xf bank_mask:0xf
	v_mov_b32_dpp v63, v63 row_ror:8 row_mask:0xf bank_mask:0xf
	v_mov_b32_dpp v64, v64 row_ror:8 row_mask:0xf bank_mask:0xf
	v_add_f32_e32 v65, v50, v55
	s_waitcnt lgkmcnt(0)
	v_cndmask_b32_e64 v54, v61, v54, s[4:5]
	s_waitcnt lgkmcnt(0)
	v_cndmask_b32_e64 v53, v62, v53, s[4:5]
	s_waitcnt lgkmcnt(0)
	v_cndmask_b32_e64 v52, v63, v52, s[4:5]
	s_waitcnt lgkmcnt(0)
	v_cndmask_b32_e64 v50, v64, v51, s[4:5]
	v_cndmask_b32_e64 v60, v60, v61, s[4:5]
	v_cndmask_b32_e64 v59, v59, v62, s[4:5]
	v_cndmask_b32_e64 v56, v56, v64, s[4:5]
	v_cndmask_b32_e64 v55, v57, v63, s[4:5]
	ds_bpermute_b32 v50, v192, v50
	ds_bpermute_b32 v51, v192, v52
	ds_bpermute_b32 v52, v192, v53
	ds_bpermute_b32 v53, v192, v54
	ds_bpermute_b32 v54, v192, v56
	ds_bpermute_b32 v56, v192, v59
	ds_bpermute_b32 v57, v192, v60
	v_ashrrev_i32_e32 v59, 31, v58
	v_mov_b32_e32 v60, v65
	s_nop 1
	v_permlane16_swap_b32_e32 v60, v65
	v_lshlrev_b64 v[58:59], 11, v[58:59]
	v_lshl_add_u64 v[58:59], s[24:25], 0, v[58:59]
	v_lshl_add_u64 v[58:59], s[56:57], 1, v[58:59]
	v_lshl_add_u64 v[58:59], v[58:59], 0, v[174:175]
	s_waitcnt lgkmcnt(3)
	global_store_dwordx4 v[58:59], v[50:53], off
	ds_bpermute_b32 v55, v192, v55
	s_waitcnt lgkmcnt(1)
	v_add_f32_e32 v50, v65, v60
	v_mov_b32_e32 v51, v50
	s_nop 1
	v_permlane32_swap_b32_e32 v51, v50
	v_add_co_u32_e32 v52, vcc, 0x4000, v58
	s_nop 1
	v_addc_co_u32_e32 v53, vcc, 0, v59, vcc
	s_waitcnt lgkmcnt(0)
	global_store_dwordx4 v[52:53], v[54:57], off
	s_and_saveexec_b64 s[58:59], s[6:7]
	s_cbranch_execz .LBB0_1084
	s_waitcnt lgkmcnt(0)
	v_add_f32_e32 v50, v50, v51
	global_atomic_add_f32 v[12:13], v50, off offset:512
; __device__ __forceinline__ u32x4 pack8(const f32x4& v0, const f32x4& v1) { u32x4 w; w.x = cvt_pk_bf16(v0[0], v0[1]); w.y = cvt_pk_bf16(v0[2], v0[3]); w.z = cvt_pk_bf16(v1[0], v1[1]); w.w = cvt_pk_bf16(v1[2], v1[3]); return w; }
; __device__ __forceinline__ u32x4 xor8_16B(u32x4 v) { u32x4 r; r.x = (unsigned)__shfl_xor((int)v.x, 8); r.y = (unsigned)__shfl_xor((int)v.y, 8); r.z = (unsigned)__shfl_xor((int)v.z, 8); r.w = (unsigned)__shfl_xor((int)v.w, 8); return r; }
; __device__ __forceinline__ u32x4 bperm_16B(int src_byte, u32x4 v) { u32x4 r; r.x = (unsigned)__builtin_amdgcn_ds_bpermute(src_byte, (int)v.x); r.y = (unsigned)__builtin_amdgcn_ds_bpermute(src_byte, (int)v.y); r.z = (unsigned)__builtin_amdgcn_ds_bpermute(src_byte, (int)v.z); r.w = (unsigned)__builtin_amdgcn_ds_bpermute(src_byte, (int)v.w); return r; }
; __device__ __forceinline__ void store_rows_bf16(bf16_t* O, size_t ldc, int r0, int c0, int fr, int fq, u32x4 w0, u32x4 w1) {
;     const bool h = fr & 8; const u32x4 recv = xor8_16B(h ? w0 : w1);
;     const u32x4 d1 = h ? recv : w0, d2 = h ? w1 : recv;
;     const int lane = fr + 16 * fq, src = ((lane >> 3) + 8 * ((lane >> 2) & 1) + 16 * (lane & 3)) * 4;
;     const u32x4 e1 = bperm_16B(src, d1), e2 = bperm_16B(src, d2);
;     bf16_t* p = O + (size_t)(r0 + (lane >> 3)) * ldc + c0 + 8 * (lane & 7);
;     *(u32x4*)p = e1; *(u32x4*)(p + 8 * ldc) = e2;
;     __device__ __forceinline__ void operator()(f32x4 (&acc)[2][2][4][2], const Unit& u, int wr, int wc, int fr, int fq) const {
;     ...
;             for (int m = 0; m < 4; ++m) { const int row = u.pm * BM + wr * 64 + fr + ai * HALF + m * 16; float s = 0.f; u32x4 wx[2];
; #pragma unroll
;                 for (int bj = 0; bj < 2; ++bj) { const f32x4 v0 = acc[ai][bj][m][0], v1 = acc[ai][bj][m][1];
;                     s += (v0[0] * v0[0] + v0[1] * v0[1]) + (v0[2] * v0[2] + v0[3] * v0[3]) + (v1[0] * v1[0] + v1[1] * v1[1]) + (v1[2] * v1[2] + v1[3] * v1[3]);
;                     wx[bj] = pack8(v0, v1); }
;                 store_rows_bf16(xb, 1024, u.pm * BM + wr * 64 + ai * HALF + m * 16, u.pn * BM + wc * 64, fr, fq, wx[0], wx[1]);
;                 s += __shfl_xor(s, 16); s += __shfl_xor(s, 32);
;                 if (fq == 0) atomicAdd(ssq + row, s);
.LBB0_1084:
	s_or_b64 exec, exec, s[58:59]
	v_mul_f32_e32 v50, v47, v47
	s_waitcnt lgkmcnt(0)
	v_mul_f32_e32 v51, v49, v49
	v_fmac_f32_e32 v50, v46, v46
	v_fmac_f32_e32 v51, v48, v48
	v_add_f32_e32 v50, v50, v51
	v_mul_f32_e32 v51, v115, v115
	v_fmac_f32_e32 v51, v114, v114
	v_add_f32_e32 v50, v51, v50
	v_mul_f32_e32 v51, v117, v117
	v_fmac_f32_e32 v51, v116, v116
	v_add_f32_e32 v50, v51, v50
	v_mul_f32_e32 v51, v39, v39
	v_mul_f32_e32 v52, v41, v41
	v_fmac_f32_e32 v51, v38, v38
	v_fmac_f32_e32 v52, v40, v40
	v_add_f32_e32 v51, v51, v52
	v_mul_f32_e32 v52, v43, v43
	v_fmac_f32_e32 v52, v42, v42
	v_cvt_pk_bf16_f32 v46, v46, v47
	v_cvt_pk_bf16_f32 v47, v48, v49
	v_cvt_pk_bf16_f32 v48, v114, v115
	v_cvt_pk_bf16_f32 v49, v116, v117
	v_add_f32_e32 v51, v52, v51
	v_mul_f32_e32 v52, v45, v45
	v_cvt_pk_bf16_f32 v38, v38, v39
	v_cvt_pk_bf16_f32 v39, v40, v41
	v_cvt_pk_bf16_f32 v40, v42, v43
	v_cvt_pk_bf16_f32 v41, v44, v45
	v_fmac_f32_e32 v52, v44, v44
	v_cndmask_b32_e64 v45, v46, v38, s[4:5]
	v_cndmask_b32_e64 v42, v49, v41, s[4:5]
	v_cndmask_b32_e64 v43, v48, v40, s[4:5]
	v_cndmask_b32_e64 v44, v47, v39, s[4:5]
	v_mov_b32_dpp v45, v45 row_ror:8 row_mask:0xf bank_mask:0xf
	v_mov_b32_dpp v42, v42 row_ror:8 row_mask:0xf bank_mask:0xf
	v_mov_b32_dpp v43, v43 row_ror:8 row_mask:0xf bank_mask:0xf
	v_mov_b32_dpp v44, v44 row_ror:8 row_mask:0xf bank_mask:0xf
	v_add_f32_e32 v51, v52, v51
	s_waitcnt lgkmcnt(0)
	v_cndmask_b32_e64 v46, v45, v46, s[4:5]
	v_add_f32_e32 v50, v50, v51
	s_waitcnt lgkmcnt(0)
	v_cndmask_b32_e64 v49, v42, v49, s[4:5]
	s_waitcnt lgkmcnt(0)
	v_cndmask_b32_e64 v48, v43, v48, s[4:5]
	s_waitcnt lgkmcnt(0)
	v_cndmask_b32_e64 v47, v44, v47, s[4:5]
	v_cndmask_b32_e64 v51, v41, v42, s[4:5]
	v_cndmask_b32_e64 v42, v38, v45, s[4:5]
	ds_bpermute_b32 v38, v192, v46
	v_add_u32_e32 v46, 0x90, v10
	v_cndmask_b32_e64 v52, v40, v43, s[4:5]
	v_cndmask_b32_e64 v43, v39, v44, s[4:5]
	ds_bpermute_b32 v39, v192, v47
	ds_bpermute_b32 v40, v192, v48
	ds_bpermute_b32 v41, v192, v49
	v_ashrrev_i32_e32 v47, 31, v46
	v_mov_b32_e32 v48, v50
	s_nop 1
	v_permlane16_swap_b32_e32 v48, v50
	v_lshlrev_b64 v[46:47], 11, v[46:47]
	v_lshl_add_u64 v[46:47], s[24:25], 0, v[46:47]
	v_lshl_add_u64 v[46:47], s[56:57], 1, v[46:47]
	v_lshl_add_u64 v[46:47], v[46:47], 0, v[174:175]
	s_waitcnt lgkmcnt(0)
	global_store_dwordx4 v[46:47], v[38:41], off
	ds_bpermute_b32 v42, v192, v42
	ds_bpermute_b32 v43, v192, v43
	s_waitcnt lgkmcnt(2)
	v_add_f32_e32 v38, v50, v48
	ds_bpermute_b32 v44, v192, v52
	ds_bpermute_b32 v45, v192, v51
	v_mov_b32_e32 v39, v38
	s_nop 1
	v_permlane32_swap_b32_e32 v39, v38
	v_add_co_u32_e32 v40, vcc, 0x4000, v46
	s_nop 1
	v_addc_co_u32_e32 v41, vcc, 0, v47, vcc
	s_waitcnt lgkmcnt(0)
	global_store_dwordx4 v[40:41], v[42:45], off
	s_and_saveexec_b64 s[58:59], s[6:7]
	s_cbranch_execz .LBB0_1086
	s_waitcnt lgkmcnt(0)
	v_add_f32_e32 v38, v38, v39
	global_atomic_add_f32 v[12:13], v38, off offset:576
; __device__ __forceinline__ u32x4 pack8(const f32x4& v0, const f32x4& v1) { u32x4 w; w.x = cvt_pk_bf16(v0[0], v0[1]); w.y = cvt_pk_bf16(v0[2], v0[3]); w.z = cvt_pk_bf16(v1[0], v1[1]); w.w = cvt_pk_bf16(v1[2], v1[3]); return w; }
; __device__ __forceinline__ u32x4 xor8_16B(u32x4 v) { u32x4 r; r.x = (unsigned)__shfl_xor((int)v.x, 8); r.y = (unsigned)__shfl_xor((int)v.y, 8); r.z = (unsigned)__shfl_xor((int)v.z, 8); r.w = (unsigned)__shfl_xor((int)v.w, 8); return r; }
; __device__ __forceinline__ u32x4 bperm_16B(int src_byte, u32x4 v) { u32x4 r; r.x = (unsigned)__builtin_amdgcn_ds_bpermute(src_byte, (int)v.x); r.y = (unsigned)__builtin_amdgcn_ds_bpermute(src_byte, (int)v.y); r.z = (unsigned)__builtin_amdgcn_ds_bpermute(src_byte, (int)v.z); r.w = (unsigned)__builtin_amdgcn_ds_bpermute(src_byte, (int)v.w); return r; }
; __device__ __forceinline__ void store_rows_bf16(bf16_t* O, size_t ldc, int r0, int c0, int fr, int fq, u32x4 w0, u32x4 w1) {
;     const bool h = fr & 8; const u32x4 recv = xor8_16B(h ? w0 : w1);
;     const u32x4 d1 = h ? recv : w0, d2 = h ? w1 : recv;
;     const int lane = fr + 16 * fq, src = ((lane >> 3) + 8 * ((lane >> 2) & 1) + 16 * (lane & 3)) * 4;
;     const u32x4 e1 = bperm_16B(src, d1), e2 = bperm_16B(src, d2);
;     bf16_t* p = O + (size_t)(r0 + (lane >> 3)) * ldc + c0 + 8 * (lane & 7);
;     *(u32x4*)p = e1; *(u32x4*)(p + 8 * ldc) = e2;
;     __device__ __forceinline__ void operator()(f32x4 (&acc)[2][2][4][2], const Unit& u, int wr, int wc, int fr, int fq) const {
;     ...
;             for (int m = 0; m < 4; ++m) { const int row = u.pm * BM + wr * 64 + fr + ai * HALF + m * 16; float s = 0.f; u32x4 wx[2];
; #pragma unroll
;                 for (int bj = 0; bj < 2; ++bj) { const f32x4 v0 = acc[ai][bj][m][0], v1 = acc[ai][bj][m][1];
;                     s += (v0[0] * v0[0] + v0[1] * v0[1]) + (v0[2] * v0[2] + v0[3] * v0[3]) + (v1[0] * v1[0] + v1[1] * v1[1]) + (v1[2] * v1[2] + v1[3] * v1[3]);
;                     wx[bj] = pack8(v0, v1); }
;                 store_rows_bf16(xb, 1024, u.pm * BM + wr * 64 + ai * HALF + m * 16, u.pn * BM + wc * 64, fr, fq, wx[0], wx[1]);
;                 s += __shfl_xor(s, 16); s += __shfl_xor(s, 32);
;                 if (fq == 0) atomicAdd(ssq + row, s);
.LBB0_1086:
	s_or_b64 exec, exec, s[58:59]
	v_mul_f32_e32 v38, v31, v31
	s_waitcnt lgkmcnt(0)
	v_mul_f32_e32 v39, v33, v33
	v_fmac_f32_e32 v38, v30, v30
	v_fmac_f32_e32 v39, v32, v32
	v_add_f32_e32 v38, v38, v39
	v_mul_f32_e32 v39, v35, v35
	v_fmac_f32_e32 v39, v34, v34
	v_cvt_pk_bf16_f32 v30, v30, v31
	v_cvt_pk_bf16_f32 v31, v32, v33
	v_cvt_pk_bf16_f32 v32, v34, v35
	v_mul_f32_e32 v34, v23, v23
	v_mul_f32_e32 v35, v25, v25
	v_fmac_f32_e32 v34, v22, v22
	v_fmac_f32_e32 v35, v24, v24
	v_add_f32_e32 v34, v34, v35
	v_mul_f32_e32 v35, v27, v27
	v_fmac_f32_e32 v35, v26, v26
	v_cvt_pk_bf16_f32 v33, v36, v37
	v_add_f32_e32 v34, v35, v34
	v_mul_f32_e32 v35, v29, v29
	v_cvt_pk_bf16_f32 v22, v22, v23
	v_cvt_pk_bf16_f32 v23, v24, v25
	v_cvt_pk_bf16_f32 v24, v26, v27
	v_cvt_pk_bf16_f32 v25, v28, v29
	v_fmac_f32_e32 v35, v28, v28
	v_cndmask_b32_e64 v29, v30, v22, s[4:5]
	v_cndmask_b32_e64 v26, v33, v25, s[4:5]
	v_cndmask_b32_e64 v27, v32, v24, s[4:5]
	v_cndmask_b32_e64 v28, v31, v23, s[4:5]
	v_mov_b32_dpp v29, v29 row_ror:8 row_mask:0xf bank_mask:0xf
	v_mov_b32_dpp v26, v26 row_ror:8 row_mask:0xf bank_mask:0xf
	v_mov_b32_dpp v27, v27 row_ror:8 row_mask:0xf bank_mask:0xf
	v_mov_b32_dpp v28, v28 row_ror:8 row_mask:0xf bank_mask:0xf
	v_add_f32_e32 v38, v39, v38
	v_mul_f32_e32 v39, v37, v37
	v_fmac_f32_e32 v39, v36, v36
	v_add_f32_e32 v38, v39, v38
	v_add_f32_e32 v34, v35, v34
	s_waitcnt lgkmcnt(0)
	v_cndmask_b32_e64 v30, v29, v30, s[4:5]
	v_add_f32_e32 v34, v38, v34
	s_waitcnt lgkmcnt(0)
	v_cndmask_b32_e64 v33, v26, v33, s[4:5]
	s_waitcnt lgkmcnt(0)
	v_cndmask_b32_e64 v32, v27, v32, s[4:5]
	s_waitcnt lgkmcnt(0)
	v_cndmask_b32_e64 v31, v28, v31, s[4:5]
	v_cndmask_b32_e64 v35, v25, v26, s[4:5]
	v_cndmask_b32_e64 v26, v22, v29, s[4:5]
	ds_bpermute_b32 v22, v192, v30
	v_add_u32_e32 v30, 0xa0, v10
	v_cndmask_b32_e64 v36, v24, v27, s[4:5]
	v_cndmask_b32_e64 v27, v23, v28, s[4:5]
	ds_bpermute_b32 v23, v192, v31
	ds_bpermute_b32 v24, v192, v32
	ds_bpermute_b32 v25, v192, v33
	v_ashrrev_i32_e32 v31, 31, v30
	v_mov_b32_e32 v32, v34
	s_nop 1
	v_permlane16_swap_b32_e32 v32, v34
	v_lshlrev_b64 v[30:31], 11, v[30:31]
	v_lshl_add_u64 v[30:31], s[24:25], 0, v[30:31]
	v_lshl_add_u64 v[30:31], s[56:57], 1, v[30:31]
	v_lshl_add_u64 v[30:31], v[30:31], 0, v[174:175]
	s_waitcnt lgkmcnt(0)
	global_store_dwordx4 v[30:31], v[22:25], off
	ds_bpermute_b32 v26, v192, v26
	ds_bpermute_b32 v27, v192, v27
	s_waitcnt lgkmcnt(2)
	v_add_f32_e32 v22, v34, v32
	ds_bpermute_b32 v28, v192, v36
	ds_bpermute_b32 v29, v192, v35
	v_mov_b32_e32 v23, v22
	s_nop 1
	v_permlane32_swap_b32_e32 v23, v22
	v_add_co_u32_e32 v24, vcc, 0x4000, v30
	s_nop 1
	v_addc_co_u32_e32 v25, vcc, 0, v31, vcc
	s_waitcnt lgkmcnt(0)
	global_store_dwordx4 v[24:25], v[26:29], off
	s_and_saveexec_b64 s[58:59], s[6:7]
	s_cbranch_execz .LBB0_1088
	s_waitcnt lgkmcnt(0)
	v_add_f32_e32 v22, v22, v23
	global_atomic_add_f32 v[12:13], v22, off offset:640
.LBB0_1088:
	s_or_b64 exec, exec, s[58:59]
	v_mul_f32_e32 v22, v15, v15
	s_waitcnt lgkmcnt(0)
	v_mul_f32_e32 v23, v17, v17
	v_fmac_f32_e32 v22, v14, v14
	v_fmac_f32_e32 v23, v16, v16
	v_add_f32_e32 v22, v22, v23
	v_mul_f32_e32 v23, v19, v19
	v_fmac_f32_e32 v23, v18, v18
	v_cvt_pk_bf16_f32 v14, v14, v15
	v_cvt_pk_bf16_f32 v15, v16, v17
	v_cvt_pk_bf16_f32 v16, v18, v19
	v_mul_f32_e32 v18, v7, v7
	v_mul_f32_e32 v19, v9, v9
	v_fmac_f32_e32 v18, v6, v6
	v_fmac_f32_e32 v19, v8, v8
	v_add_f32_e32 v18, v18, v19
	v_mul_f32_e32 v19, v3, v3
	v_fmac_f32_e32 v19, v2, v2
	v_cvt_pk_bf16_f32 v17, v20, v21
	v_add_f32_e32 v18, v19, v18
	v_mul_f32_e32 v19, v5, v5
	v_cvt_pk_bf16_f32 v6, v6, v7
	v_cvt_pk_bf16_f32 v7, v8, v9
	v_fmac_f32_e32 v19, v4, v4
	v_cndmask_b32_e64 v9, v14, v6, s[4:5]
	v_cvt_pk_bf16_f32 v2, v2, v3
	v_cvt_pk_bf16_f32 v3, v4, v5
	v_cndmask_b32_e64 v8, v15, v7, s[4:5]
	v_cndmask_b32_e64 v4, v17, v3, s[4:5]
	v_cndmask_b32_e64 v5, v16, v2, s[4:5]
	v_mov_b32_dpp v9, v9 row_ror:8 row_mask:0xf bank_mask:0xf
	v_mov_b32_dpp v4, v4 row_ror:8 row_mask:0xf bank_mask:0xf
	v_mov_b32_dpp v5, v5 row_ror:8 row_mask:0xf bank_mask:0xf
	v_mov_b32_dpp v8, v8 row_ror:8 row_mask:0xf bank_mask:0xf
	v_add_f32_e32 v22, v23, v22
	v_mul_f32_e32 v23, v21, v21
	v_fmac_f32_e32 v23, v20, v20
	v_add_f32_e32 v22, v23, v22
	v_add_f32_e32 v18, v19, v18
	s_waitcnt lgkmcnt(0)
	v_cndmask_b32_e64 v14, v9, v14, s[4:5]
	v_add_f32_e32 v18, v22, v18
	s_waitcnt lgkmcnt(0)
	v_cndmask_b32_e64 v17, v4, v17, s[4:5]
	s_waitcnt lgkmcnt(0)
	v_cndmask_b32_e64 v16, v5, v16, s[4:5]
	s_waitcnt lgkmcnt(0)
	v_cndmask_b32_e64 v15, v8, v15, s[4:5]
	v_cndmask_b32_e64 v20, v2, v5, s[4:5]
	ds_bpermute_b32 v2, v192, v14
	v_add_u32_e32 v14, 0xb0, v10
	v_cndmask_b32_e64 v19, v3, v4, s[4:5]
	ds_bpermute_b32 v3, v192, v15
	ds_bpermute_b32 v4, v192, v16
	ds_bpermute_b32 v5, v192, v17
	v_ashrrev_i32_e32 v15, 31, v14
	v_mov_b32_e32 v16, v18
	s_nop 1
	v_permlane16_swap_b32_e32 v16, v18
	v_lshlrev_b64 v[14:15], 11, v[14:15]
	v_lshl_add_u64 v[14:15], s[24:25], 0, v[14:15]
	v_lshl_add_u64 v[14:15], s[56:57], 1, v[14:15]
	v_lshl_add_u64 v[10:11], v[14:15], 0, v[174:175]
	v_cndmask_b32_e64 v7, v7, v8, s[4:5]
	v_cndmask_b32_e64 v6, v6, v9, s[4:5]
	s_waitcnt lgkmcnt(0)
	global_store_dwordx4 v[10:11], v[2:5], off
	ds_bpermute_b32 v6, v192, v6
	ds_bpermute_b32 v7, v192, v7
	s_waitcnt lgkmcnt(2)
	v_add_f32_e32 v2, v18, v16
	ds_bpermute_b32 v8, v192, v20
	ds_bpermute_b32 v9, v192, v19
	v_mov_b32_e32 v3, v2
	s_nop 1
	v_permlane32_swap_b32_e32 v3, v2
	v_add_co_u32_e32 v4, vcc, 0x4000, v10
	s_nop 1
	v_addc_co_u32_e32 v5, vcc, 0, v11, vcc
	s_waitcnt lgkmcnt(0)
	global_store_dwordx4 v[4:5], v[6:9], off
	s_and_saveexec_b64 s[56:57], s[6:7]
	s_cbranch_execz .LBB0_1090
	s_waitcnt lgkmcnt(0)
	v_add_f32_e32 v2, v2, v3
	global_atomic_add_f32 v[12:13], v2, off offset:704

; __device__ __forceinline__ void p10_topk(const Params& P, LAS unsigned char* lds, int tid, int lane, int wave, int vb) {
;     ...
;         const float f1_0 = ord2f(R[0][0] & ~0x7f); const float f1_1 = ord2f(R[0][1] & ~0x7f); const float f1_2 = ord2f(R[0][2] & ~0x7f); const float f1_3 = ord2f(R[0][3] & ~0x7f); const float f1_4 = ord2f(R[0][4] & ~0x7f); const float f1_5 = ord2f(R[0][5] & ~0x7f); const float f1_6 = ord2f(R[0][6] & ~0x7f); const float f1_7 = ord2f(R[0][7] & ~0x7f); const float f1_8 = ord2f(R[0][8] & ~0x7f); const float f1_9 = ord2f(R[0][9] & ~0x7f); const float f1_10 = ord2f(R[0][10] & ~0x7f); const float f1_11 = ord2f(R[0][11] & ~0x7f); const float f1_12 = ord2f(R[0][12] & ~0x7f); const float f1_13 = ord2f(R[0][13] & ~0x7f); const float f1_14 = ord2f(R[0][14] & ~0x7f); const float f1_15 = ord2f(R[0][15] & ~0x7f);
;         const float f2_0 = ord2f(R[1][0] & ~0x7f); const float f2_1 = ord2f(R[1][1] & ~0x7f); const float f2_2 = ord2f(R[1][2] & ~0x7f); const float f2_3 = ord2f(R[1][3] & ~0x7f); const float f2_4 = ord2f(R[1][4] & ~0x7f); const float f2_5 = ord2f(R[1][5] & ~0x7f); const float f2_6 = ord2f(R[1][6] & ~0x7f); const float f2_7 = ord2f(R[1][7] & ~0x7f); const float f2_8 = ord2f(R[1][8] & ~0x7f); const float f2_9 = ord2f(R[1][9] & ~0x7f); const float f2_10 = ord2f(R[1][10] & ~0x7f); const float f2_11 = ord2f(R[1][11] & ~0x7f); const float f2_12 = ord2f(R[1][12] & ~0x7f); const float f2_13 = ord2f(R[1][13] & ~0x7f); const float f2_14 = ord2f(R[1][14] & ~0x7f); const float f2_15 = ord2f(R[1][15] & ~0x7f);
;         int C[16];
;         { const bool g0 = g == 0, g1 = g == 1, g2 = g == 2;
;           { const float fa = g0 ? f1_0 : (g1 ? f1_1 : (g2 ? f1_3 : f1_8)), fb = g0 ? f2_0 : (g1 ? f2_0 : (g2 ? f2_0 : f2_0)); const int ab = g0 ? 0 : (g1 ? 16 : (g2 ? 48 : 128)); int key = (f2ord(fa + fb) & ~0xff) | ab; C[0] = key; }
;           { const float fa = g0 ? f1_0 : (g1 ? f1_1 : (g2 ? f1_3 : f1_9)), fb = g0 ? f2_1 : (g1 ? f2_1 : (g2 ? f2_1 : f2_0)); const int ab = g0 ? 1 : (g1 ? 17 : (g2 ? 49 : 144)); int key = (f2ord(fa + fb) & ~0xff) | ab; C[1] = key; }
;           { const float fa = g0 ? f1_0 : (g1 ? f1_1 : (g2 ? f1_3 : f1_10)), fb = g0 ? f2_2 : (g1 ? f2_2 : (g2 ? f2_2 : f2_0)); const int ab = g0 ? 2 : (g1 ? 18 : (g2 ? 50 : 160)); int key = (f2ord(fa + fb) & ~0xff) | ab; C[2] = key; }
.LBB0_1252:
	s_or_b64 exec, exec, s[90:91]
	v_and_b32_e32 v176, 0xffffff80, v165
	v_ashrrev_i32_e32 v165, 31, v165
	v_bitop3_b32 v165, v165, v176, s67 bitop3:0x6c
	v_and_b32_e32 v176, 0xffffff80, v162
	v_ashrrev_i32_e32 v162, 31, v162
	v_bitop3_b32 v162, v162, v176, s67 bitop3:0x6c
	v_and_b32_e32 v176, 0xffffff80, v175
	v_ashrrev_i32_e32 v175, 31, v175
	v_bitop3_b32 v175, v175, v176, s67 bitop3:0x6c
	v_and_b32_e32 v176, 0xffffff80, v174
	v_ashrrev_i32_e32 v174, 31, v174
	v_bitop3_b32 v174, v174, v176, s67 bitop3:0x6c
	v_and_b32_e32 v176, 0xffffff80, v172
	v_ashrrev_i32_e32 v172, 31, v172
	v_bitop3_b32 v172, v172, v176, s67 bitop3:0x6c
	v_and_b32_e32 v176, 0xffffff80, v173
	v_ashrrev_i32_e32 v173, 31, v173
	v_bitop3_b32 v173, v173, v176, s67 bitop3:0x6c
	v_and_b32_e32 v176, 0xffffff80, v171
	v_ashrrev_i32_e32 v171, 31, v171
	v_bitop3_b32 v171, v171, v176, s67 bitop3:0x6c
	v_and_b32_e32 v176, 0xffffff80, v168
	v_ashrrev_i32_e32 v168, 31, v168
	v_bitop3_b32 v168, v168, v176, s67 bitop3:0x6c
	v_and_b32_e32 v176, 0xffffff80, v170
	v_ashrrev_i32_e32 v170, 31, v170
	v_bitop3_b32 v170, v170, v176, s67 bitop3:0x6c
	v_and_b32_e32 v176, 0xffffff80, v167
	v_ashrrev_i32_e32 v167, 31, v167
	v_bitop3_b32 v167, v167, v176, s67 bitop3:0x6c
	v_and_b32_e32 v176, 0xffffff80, v169
	v_ashrrev_i32_e32 v169, 31, v169
	v_bitop3_b32 v169, v169, v176, s67 bitop3:0x6c
	v_and_b32_e32 v176, 0xffffff80, v166
	v_ashrrev_i32_e32 v166, 31, v166
	v_bitop3_b32 v166, v166, v176, s67 bitop3:0x6c
	v_and_b32_e32 v176, 0xffffff80, v164
	v_ashrrev_i32_e32 v164, 31, v164
	v_bitop3_b32 v164, v164, v176, s67 bitop3:0x6c
	v_and_b32_e32 v176, 0xffffff80, v163
	v_ashrrev_i32_e32 v163, 31, v163
	v_bitop3_b32 v163, v163, v176, s67 bitop3:0x6c
	v_and_b32_e32 v176, 0xffffff80, v161
	v_ashrrev_i32_e32 v161, 31, v161
	v_bitop3_b32 v161, v161, v176, s67 bitop3:0x6c
	v_and_b32_e32 v176, 0xffffff80, v160
	v_ashrrev_i32_e32 v160, 31, v160
	v_bitop3_b32 v160, v160, v176, s67 bitop3:0x6c
	v_and_b32_e32 v176, 0xffffff80, v61
	v_ashrrev_i32_e32 v61, 31, v61
	v_bitop3_b32 v61, v61, v176, s67 bitop3:0x6c
	v_and_b32_e32 v176, 0xffffff80, v60
	v_ashrrev_i32_e32 v60, 31, v60
	v_bitop3_b32 v60, v60, v176, s67 bitop3:0x6c
	v_and_b32_e32 v176, 0xffffff80, v59
	v_ashrrev_i32_e32 v59, 31, v59
	v_bitop3_b32 v59, v59, v176, s67 bitop3:0x6c
	v_and_b32_e32 v176, 0xffffff80, v58
	v_ashrrev_i32_e32 v58, 31, v58
	v_bitop3_b32 v58, v58, v176, s67 bitop3:0x6c
	v_and_b32_e32 v176, 0xffffff80, v57
	v_ashrrev_i32_e32 v57, 31, v57
	v_bitop3_b32 v57, v57, v176, s67 bitop3:0x6c
	v_and_b32_e32 v176, 0xffffff80, v56
	v_ashrrev_i32_e32 v56, 31, v56
	v_bitop3_b32 v56, v56, v176, s67 bitop3:0x6c
	v_and_b32_e32 v176, 0xffffff80, v55
	v_ashrrev_i32_e32 v55, 31, v55
	v_bitop3_b32 v55, v55, v176, s67 bitop3:0x6c
	v_and_b32_e32 v176, 0xffffff80, v54
	v_ashrrev_i32_e32 v54, 31, v54
	v_bitop3_b32 v54, v54, v176, s67 bitop3:0x6c
	v_and_b32_e32 v176, 0xffffff80, v53
	v_ashrrev_i32_e32 v53, 31, v53
	v_bitop3_b32 v53, v53, v176, s67 bitop3:0x6c
	v_and_b32_e32 v176, 0xffffff80, v52
	v_ashrrev_i32_e32 v52, 31, v52
	v_bitop3_b32 v52, v52, v176, s67 bitop3:0x6c
	v_and_b32_e32 v176, 0xffffff80, v51
	v_ashrrev_i32_e32 v51, 31, v51
	v_bitop3_b32 v51, v51, v176, s67 bitop3:0x6c
	v_and_b32_e32 v176, 0xffffff80, v50
	v_ashrrev_i32_e32 v50, 31, v50
	v_bitop3_b32 v50, v50, v176, s67 bitop3:0x6c
	v_and_b32_e32 v176, 0xffffff80, v49
	v_ashrrev_i32_e32 v49, 31, v49
	v_bitop3_b32 v49, v49, v176, s67 bitop3:0x6c
	v_and_b32_e32 v176, 0xffffff80, v48
	v_ashrrev_i32_e32 v48, 31, v48
	v_bitop3_b32 v48, v48, v176, s67 bitop3:0x6c
	v_and_b32_e32 v176, 0xffffff80, v47
	v_ashrrev_i32_e32 v47, 31, v47
	v_bitop3_b32 v47, v47, v176, s67 bitop3:0x6c
	v_and_b32_e32 v176, 0xffffff80, v46
	v_ashrrev_i32_e32 v46, 31, v46
	v_bitop3_b32 v46, v46, v176, s67 bitop3:0x6c
	v_cndmask_b32_e64 v176, v170, v174, s[2:3]
	v_cndmask_b32_e64 v176, v176, v162, s[4:5]
	v_cndmask_b32_e64 v176, v176, v165, s[6:7]
	v_add_f32_e32 v176, v176, v61
	v_ashrrev_i32_e32 v177, 31, v176
	v_and_b32_e32 v177, 0x7fffff00, v177
	v_and_b32_e32 v176, 0xffffff00, v176
	v_bitop3_b32 v176, v177, v109, v176 bitop3:0xde
	v_cndmask_b32_e64 v177, v167, v174, s[2:3]
	v_cndmask_b32_e64 v178, v61, v60, s[2:3]
	v_cndmask_b32_e64 v167, v167, v171, s[2:3]
	v_cndmask_b32_e64 v177, v177, v162, s[4:5]
	v_cndmask_b32_e64 v179, v178, v60, s[8:9]
	v_cndmask_b32_e64 v167, v167, v175, s[4:5]
	v_cndmask_b32_e64 v60, v61, v60, s[4:5]
	v_cndmask_b32_e64 v177, v177, v165, s[6:7]
	v_cndmask_b32_e64 v167, v167, v165, s[6:7]
	v_cndmask_b32_e64 v52, v60, v52, s[6:7]
	v_add_f32_e32 v177, v177, v179
	v_add_f32_e32 v52, v167, v52
	v_ashrrev_i32_e32 v179, 31, v177
	v_ashrrev_i32_e32 v60, 31, v52
	v_and_b32_e32 v179, 0x7fffff00, v179
	v_and_b32_e32 v177, 0xffffff00, v177
	v_and_b32_e32 v60, 0x7fffff00, v60
	v_and_b32_e32 v52, 0xffffff00, v52
	v_bitop3_b32 v177, v179, v110, v177 bitop3:0xde
	v_cndmask_b32_e64 v179, v169, v174, s[2:3]
	v_cndmask_b32_e64 v180, v61, v59, s[2:3]
	v_bitop3_b32 v52, v60, v118, v52 bitop3:0xde
	v_cndmask_b32_e64 v60, v169, v171, s[2:3]
	v_cndmask_b32_e64 v179, v179, v162, s[4:5]
	v_cndmask_b32_e64 v181, v180, v59, s[8:9]
	v_cndmask_b32_e64 v60, v60, v175, s[4:5]
	v_cndmask_b32_e64 v59, v178, v59, s[4:5]
	v_cndmask_b32_e64 v179, v179, v165, s[6:7]
	v_cndmask_b32_e64 v60, v60, v165, s[6:7]
	v_cndmask_b32_e64 v51, v59, v51, s[6:7]
	v_add_f32_e32 v179, v179, v181
	v_add_f32_e32 v51, v60, v51
	v_ashrrev_i32_e32 v181, 31, v179
	v_ashrrev_i32_e32 v59, 31, v51
	v_and_b32_e32 v181, 0x7fffff00, v181
	v_and_b32_e32 v179, 0xffffff00, v179
	v_and_b32_e32 v59, 0x7fffff00, v59
	v_and_b32_e32 v51, 0xffffff00, v51
; __device__ __forceinline__ void p10_topk(const Params& P, LAS unsigned char* lds, int tid, int lane, int wave, int vb) {
;     ...
;           { const float fa = g0 ? f1_0 : (g1 ? f1_2 : (g2 ? f1_5 : f1_8)), fb = g0 ? f2_8 : (g1 ? f2_0 : (g2 ? f2_1 : f2_0)); const int ab = g0 ? 8 : (g1 ? 32 : (g2 ? 81 : 128)); int key = (f2ord(fa + fb) & ~0xff) | ab; key = (g0 || g1 || g2) ? key : (int)0x80000000; C[8] = key; }
;           { const float fa = g0 ? f1_0 : (g1 ? f1_2 : (g2 ? f1_6 : f1_9)), fb = g0 ? f2_9 : (g1 ? f2_1 : (g2 ? f2_0 : f2_0)); const int ab = g0 ? 9 : (g1 ? 33 : (g2 ? 96 : 144)); int key = (f2ord(fa + fb) & ~0xff) | ab; key = (g0 || g1 || g2) ? key : (int)0x80000000; C[9] = key; }
;           { const float fa = g0 ? f1_0 : (g1 ? f1_2 : (g2 ? f1_6 : f1_10)), fb = g0 ? f2_10 : (g1 ? f2_2 : (g2 ? f2_1 : f2_0)); const int ab = g0 ? 10 : (g1 ? 34 : (g2 ? 97 : 160)); int key = (f2ord(fa + fb) & ~0xff) | ab; key = (g0 || g1 || g2) ? key : (int)0x80000000; C[10] = key; }
;           { const float fa = g0 ? f1_0 : (g1 ? f1_2 : (g2 ? f1_7 : f1_11)), fb = g0 ? f2_11 : (g1 ? f2_3 : (g2 ? f2_0 : f2_0)); const int ab = g0 ? 11 : (g1 ? 35 : (g2 ? 112 : 176)); int key = (f2ord(fa + fb) & ~0xff) | ab; key = (g0 || g1 || g2) ? key : (int)0x80000000; C[11] = key; }
;           { const float fa = g0 ? f1_0 : (g1 ? f1_2 : (g2 ? f1_7 : f1_12)), fb = g0 ? f2_12 : (g1 ? f2_4 : (g2 ? f2_1 : f2_0)); const int ab = g0 ? 12 : (g1 ? 36 : (g2 ? 113 : 192)); int key = (f2ord(fa + fb) & ~0xff) | ab; key = (g0 || g1 || g2) ? key : (int)0x80000000; C[12] = key; }
;           { const float fa = g0 ? f1_0 : (g1 ? f1_2 : (g2 ? f1_7 : f1_13)), fb = g0 ? f2_13 : (g1 ? f2_5 : (g2 ? f2_2 : f2_0)); const int ab = g0 ? 13 : (g1 ? 37 : (g2 ? 114 : 208)); int key = (f2ord(fa + fb) & ~0xff) | ab; key = g0 ? key : (int)0x80000000; C[13] = key; }
;           { const float fa = g0 ? f1_0 : (g1 ? f1_2 : (g2 ? f1_7 : f1_14)), fb = g0 ? f2_14 : (g1 ? f2_6 : (g2 ? f2_3 : f2_0)); const int ab = g0 ? 14 : (g1 ? 38 : (g2 ? 115 : 224)); int key = (f2ord(fa + fb) & ~0xff) | ab; key = g0 ? key : (int)0x80000000; C[14] = key; }
;           { const float fa = g0 ? f1_0 : (g1 ? f1_2 : (g2 ? f1_7 : f1_15)), fb = g0 ? f2_15 : (g1 ? f2_7 : (g2 ? f2_4 : f2_0)); const int ab = g0 ? 15 : (g1 ? 39 : (g2 ? 116 : 240)); int key = (f2ord(fa + fb) & ~0xff) | ab; key = g0 ? key : (int)0x80000000; C[15] = key; }
;         }
	v_bitop3_b32 v179, v181, v111, v179 bitop3:0xde
	v_cndmask_b32_e64 v181, v61, v58, s[2:3]
	v_bitop3_b32 v51, v59, v119, v51 bitop3:0xde
	v_cndmask_b32_e64 v59, v166, v168, s[2:3]
	v_cndmask_b32_e64 v174, v166, v174, s[2:3]
	v_cndmask_b32_e64 v182, v181, v58, s[8:9]
	v_cndmask_b32_e64 v59, v59, v175, s[4:5]
	v_cndmask_b32_e64 v58, v61, v58, s[4:5]
	v_cndmask_b32_e64 v174, v174, v162, s[4:5]
	v_cndmask_b32_e64 v59, v59, v165, s[6:7]
	v_cndmask_b32_e64 v50, v58, v50, s[6:7]
	v_cndmask_b32_e64 v174, v174, v165, s[6:7]
	v_add_f32_e32 v50, v59, v50
	v_add_f32_e32 v174, v174, v182
	v_ashrrev_i32_e32 v58, 31, v50
	v_ashrrev_i32_e32 v182, 31, v174
	v_and_b32_e32 v58, 0x7fffff00, v58
	v_and_b32_e32 v50, 0xffffff00, v50
	v_and_b32_e32 v182, 0x7fffff00, v182
	v_and_b32_e32 v174, 0xffffff00, v174
	v_bitop3_b32 v50, v58, v120, v50 bitop3:0xde
	v_cndmask_b32_e64 v58, v164, v168, s[2:3]
	v_bitop3_b32 v174, v182, v112, v174 bitop3:0xde
	v_cndmask_b32_e64 v182, v164, v172, s[2:3]
	v_cndmask_b32_e64 v58, v58, v175, s[4:5]
	v_cndmask_b32_e64 v59, v178, v57, s[4:5]
	v_cndmask_b32_e64 v182, v182, v162, s[4:5]
	v_cndmask_b32_e64 v58, v58, v165, s[6:7]
	v_cndmask_b32_e64 v49, v59, v49, s[6:7]
	v_cndmask_b32_e64 v182, v182, v165, s[6:7]
	v_cndmask_b32_e64 v183, v61, v57, s[8:9]
	v_add_f32_e32 v49, v58, v49
	v_add_f32_e32 v182, v182, v183
	v_ashrrev_i32_e32 v58, 31, v49
	v_ashrrev_i32_e32 v183, 31, v182
	v_and_b32_e32 v58, 0x7fffff00, v58
	v_and_b32_e32 v49, 0xffffff00, v49
	v_and_b32_e32 v183, 0x7fffff00, v183
	v_and_b32_e32 v182, 0xffffff00, v182
	v_bitop3_b32 v49, v58, v121, v49 bitop3:0xde
	v_cndmask_b32_e64 v58, v163, v168, s[2:3]
	v_bitop3_b32 v182, v183, v113, v182 bitop3:0xde
	v_cndmask_b32_e64 v183, v163, v172, s[2:3]
	v_cndmask_b32_e64 v184, v178, v56, s[8:9]
	v_cndmask_b32_e64 v58, v58, v175, s[4:5]
	v_cndmask_b32_e64 v56, v180, v56, s[4:5]
	v_cndmask_b32_e64 v183, v183, v162, s[4:5]
	v_cndmask_b32_e64 v58, v58, v165, s[6:7]
	v_cndmask_b32_e64 v48, v56, v48, s[6:7]
	v_cndmask_b32_e64 v183, v183, v165, s[6:7]
	v_add_f32_e32 v48, v58, v48
	v_add_f32_e32 v183, v183, v184
	v_ashrrev_i32_e32 v56, 31, v48
	v_ashrrev_i32_e32 v184, 31, v183
	v_and_b32_e32 v56, 0x7fffff00, v56
	v_and_b32_e32 v48, 0xffffff00, v48
	v_and_b32_e32 v184, 0x7fffff00, v184
	v_and_b32_e32 v183, 0xffffff00, v183
	v_cndmask_b32_e64 v172, v161, v172, s[2:3]
	v_bitop3_b32 v48, v56, 13, v48 bitop3:0xde
	v_cndmask_b32_e64 v56, v161, v168, s[2:3]
	v_bitop3_b32 v183, v184, v114, v183 bitop3:0xde
	v_cndmask_b32_e64 v172, v172, v162, s[4:5]
	v_cndmask_b32_e64 v184, v180, v55, s[8:9]
	v_cndmask_b32_e64 v56, v56, v175, s[4:5]
	v_cndmask_b32_e64 v55, v181, v55, s[4:5]
	v_cndmask_b32_e64 v172, v172, v165, s[6:7]
	v_cndmask_b32_e64 v56, v56, v165, s[6:7]
	v_cndmask_b32_e64 v47, v55, v47, s[6:7]
	v_add_f32_e32 v172, v172, v184
	v_add_f32_e32 v47, v56, v47
	v_ashrrev_i32_e32 v184, 31, v172
	v_ashrrev_i32_e32 v55, 31, v47
	v_and_b32_e32 v184, 0x7fffff00, v184
	v_and_b32_e32 v172, 0xffffff00, v172
	v_and_b32_e32 v55, 0x7fffff00, v55
	v_and_b32_e32 v47, 0xffffff00, v47
	v_bitop3_b32 v172, v184, v115, v172 bitop3:0xde
	v_cndmask_b32_e64 v184, v160, v173, s[2:3]
	v_cndmask_b32_e64 v170, v170, v173, s[2:3]
	v_bitop3_b32 v47, v55, 14, v47 bitop3:0xde
	v_cndmask_b32_e64 v55, v160, v168, s[2:3]
	v_cndmask_b32_e64 v56, v61, v57, s[2:3]
	v_cndmask_b32_e64 v162, v184, v162, s[4:5]
	v_cndmask_b32_e64 v184, v61, v54, s[8:9]
	v_cndmask_b32_e64 v170, v170, v175, s[4:5]
	v_cndmask_b32_e64 v173, v178, v61, s[4:5]
	v_cndmask_b32_e64 v55, v55, v175, s[4:5]
	v_cndmask_b32_e64 v54, v56, v54, s[4:5]
	v_cndmask_b32_e64 v170, v170, v165, s[6:7]
	v_cndmask_b32_e64 v53, v173, v53, s[6:7]
	v_cndmask_b32_e64 v55, v55, v165, s[6:7]
	v_cndmask_b32_e64 v46, v54, v46, s[6:7]
	v_cndmask_b32_e64 v162, v162, v165, s[6:7]
	v_add_f32_e32 v53, v170, v53
	v_add_f32_e32 v46, v55, v46
	v_add_f32_e32 v162, v162, v184
	v_ashrrev_i32_e32 v170, 31, v53
	v_ashrrev_i32_e32 v54, 31, v46
	v_ashrrev_i32_e32 v184, 31, v162
	v_and_b32_e32 v170, 0x7fffff00, v170
	v_and_b32_e32 v53, 0xffffff00, v53
	v_and_b32_e32 v54, 0x7fffff00, v54
	v_and_b32_e32 v46, 0xffffff00, v46
	v_and_b32_e32 v184, 0x7fffff00, v184
	v_and_b32_e32 v162, 0xffffff00, v162
	v_bitop3_b32 v53, v170, v117, v53 bitop3:0xde
	v_bitop3_b32 v46, v54, 15, v46 bitop3:0xde
	v_bitop3_b32 v162, v184, v116, v162 bitop3:0xde
	v_cndmask_b32_e64 v53, v158, v53, s[12:13]
	v_cndmask_b32_e64 v52, v158, v52, s[12:13]
	v_cndmask_b32_e64 v51, v158, v51, s[12:13]
	v_cndmask_b32_e64 v50, v158, v50, s[12:13]
	v_cndmask_b32_e64 v49, v158, v49, s[12:13]
	v_cndmask_b32_e64 v48, v158, v48, s[6:7]
	v_cndmask_b32_e64 v47, v158, v47, s[6:7]
	v_cndmask_b32_e64 v46, v158, v46, s[6:7]
	v_max_i32_e32 v54, v176, v48
	v_min_i32_e32 v48, v176, v48
	v_max_i32_e32 v55, v177, v49
	v_min_i32_e32 v49, v177, v49
	v_max_i32_e32 v56, v179, v46
	v_min_i32_e32 v46, v179, v46
	v_max_i32_e32 v57, v174, v47
	v_min_i32_e32 v47, v174, v47
	v_max_i32_e32 v58, v182, v53
	v_min_i32_e32 v53, v182, v53
	v_max_i32_e32 v59, v183, v172
	v_min_i32_e32 v60, v183, v172
	v_max_i32_e32 v61, v162, v50
	v_min_i32_e32 v50, v162, v50
	v_max_i32_e32 v160, v52, v51
	v_min_i32_e32 v51, v52, v51
	v_max_i32_e32 v52, v54, v59
	v_min_i32_e32 v54, v54, v59
	v_max_i32_e32 v59, v55, v61
	v_min_i32_e32 v55, v55, v61
	v_max_i32_e32 v61, v56, v160
	v_min_i32_e32 v56, v56, v160
	v_max_i32_e32 v160, v57, v58
	v_min_i32_e32 v57, v57, v58
	v_max_i32_e32 v58, v60, v48
	v_min_i32_e32 v48, v60, v48
	v_max_i32_e32 v60, v53, v47
	v_min_i32_e32 v47, v53, v47
	v_max_i32_e32 v53, v51, v46
	v_min_i32_e32 v46, v51, v46
	v_max_i32_e32 v51, v50, v49
	v_min_i32_e32 v49, v50, v49
; __device__ __forceinline__ void merge16_desc(int (&a)[16], const int (&b)[16]) {
; #pragma unroll
;     for (int i = 0; i < 16; ++i) a[i] = max(a[i], b[15 - i]);
; #pragma unroll
;     for (int j = 8; j > 0; j >>= 1) {
; #pragma unroll
;         for (int i = 0; i < 16; ++i) { const int l = i ^ j; if (l > i) CE_DESC(a, i, l) }
;     }
; }
; __device__ __forceinline__ void xmerge16(int (&a)[16], int mask) {
;     int b[16];
; #pragma unroll
;     for (int i = 0; i < 16; ++i) b[i] = __shfl_xor(a[i], mask);
;     merge16_desc(a, b);
; __device__ __forceinline__ void p10_topk(const Params& P, LAS unsigned char* lds, int tid, int lane, int wave, int vb) {
;     ...
;         sort16_desc(C); xmerge16(C, 16);
;         int T8[8]; const int c0x = __shfl_xor(C[0], 32);
; #pragma unroll
;         for (int i = 0; i < 8; ++i) T8[i] = max(C[i], __shfl_xor(C[15 - i], 32));
;         const float rstd1 = rsqrtf(SSQ1[row] * (1.0f / 1024.0f) + EPS);
	v_max_i32_e32 v50, v52, v59
	v_min_i32_e32 v52, v52, v59
	v_max_i32_e32 v59, v61, v160
	v_min_i32_e32 v61, v61, v160
	v_max_i32_e32 v160, v57, v54
	v_min_i32_e32 v54, v57, v54
	v_max_i32_e32 v57, v58, v60
	v_min_i32_e32 v58, v58, v60
	v_max_i32_e32 v60, v55, v56
	v_min_i32_e32 v55, v55, v56
	v_max_i32_e32 v56, v53, v51
	v_min_i32_e32 v51, v53, v51
	v_max_i32_e32 v53, v49, v48
	v_min_i32_e32 v48, v49, v48
	v_max_i32_e32 v49, v47, v46
	v_min_i32_e32 v46, v47, v46
	v_max_i32_e32 v47, v50, v59
	v_min_i32_e32 v50, v50, v59
	v_max_i32_e32 v59, v52, v61
	v_min_i32_e32 v52, v52, v61
	v_max_i32_e32 v61, v160, v56
	v_min_i32_e32 v56, v160, v56
	v_max_i32_e32 v160, v54, v51
	v_min_i32_e32 v51, v54, v51
	v_max_i32_e32 v54, v57, v60
	v_min_i32_e32 v57, v57, v60
	v_max_i32_e32 v60, v58, v55
	v_min_i32_e32 v55, v58, v55
	v_max_i32_e32 v58, v53, v49
	v_min_i32_e32 v49, v53, v49
	v_max_i32_e32 v53, v48, v46
	v_min_i32_e32 v48, v48, v46
	v_max_i32_e32 v46, v59, v50
	v_min_i32_e32 v50, v59, v50
	v_max_i32_e32 v59, v52, v58
	v_min_i32_e32 v52, v52, v58
	v_max_i32_e32 v58, v61, v54
	v_min_i32_e32 v54, v61, v54
	v_max_i32_e32 v61, v160, v57
	v_min_i32_e32 v57, v160, v57
	v_max_i32_e32 v160, v60, v56
	v_min_i32_e32 v56, v60, v56
	v_max_i32_e32 v60, v55, v51
	v_min_i32_e32 v51, v55, v51
	v_max_i32_e32 v55, v53, v49
	v_min_i32_e32 v49, v53, v49
	v_max_i32_e32 v53, v46, v58
	v_min_i32_e32 v46, v46, v58
	v_max_i32_e32 v58, v50, v54
	v_min_i32_e32 v50, v50, v54
	v_max_i32_e32 v54, v61, v160
	v_min_i32_e32 v61, v61, v160
	v_max_i32_e32 v160, v57, v56
	v_min_i32_e32 v56, v57, v56
	v_max_i32_e32 v57, v60, v55
	v_min_i32_e32 v55, v60, v55
	v_max_i32_e32 v60, v51, v49
	v_min_i32_e32 v49, v51, v49
	v_max_i32_e32 v51, v58, v46
	v_min_i32_e32 v46, v58, v46
	v_max_i32_e32 v58, v59, v50
	v_min_i32_e32 v50, v59, v50
	v_max_i32_e32 v59, v57, v52
	v_min_i32_e32 v52, v57, v52
	v_max_i32_e32 v57, v60, v55
	v_min_i32_e32 v55, v60, v55
	v_max_i32_e32 v60, v58, v54
	v_min_i32_e32 v54, v58, v54
	v_max_i32_e32 v58, v50, v61
	v_min_i32_e32 v50, v50, v61
	v_max_i32_e32 v61, v160, v59
	v_min_i32_e32 v59, v160, v59
	v_max_i32_e32 v160, v56, v52
	v_min_i32_e32 v52, v56, v52
	v_max_i32_e32 v56, v60, v46
	v_min_i32_e32 v46, v60, v46
	v_max_i32_e32 v60, v54, v58
	v_min_i32_e32 v54, v54, v58
	v_max_i32_e32 v58, v61, v50
	v_min_i32_e32 v50, v61, v50
	v_max_i32_e32 v61, v59, v160
	v_min_i32_e32 v59, v59, v160
	v_max_i32_e32 v160, v57, v52
	ds_bpermute_b32 v171, v71, v48
	ds_bpermute_b32 v172, v71, v49
	ds_bpermute_b32 v175, v71, v160
	v_min_i32_e32 v52, v57, v52
	v_max_i32_e32 v57, v54, v58
	v_min_i32_e32 v54, v54, v58
	v_max_i32_e32 v58, v50, v61
	v_min_i32_e32 v50, v50, v61
	ds_bpermute_b32 v61, v71, v47
	ds_bpermute_b32 v161, v71, v53
	ds_bpermute_b32 v164, v71, v46
	s_waitcnt lgkmcnt(5)
	v_max_i32_e32 v171, v47, v171
	s_waitcnt lgkmcnt(4)
	v_max_i32_e32 v53, v53, v172
	s_waitcnt lgkmcnt(3)
	v_max_i32_e32 v172, v46, v175
	v_lshl_add_u64 v[46:47], s[64:65], 0, v[100:101]
	global_load_dword v46, v[46:47], off
	ds_bpermute_b32 v162, v71, v51
	ds_bpermute_b32 v163, v71, v56
	ds_bpermute_b32 v165, v71, v60
	ds_bpermute_b32 v166, v71, v57
	ds_bpermute_b32 v167, v71, v54
	ds_bpermute_b32 v168, v71, v58
	ds_bpermute_b32 v169, v71, v50
	ds_bpermute_b32 v170, v71, v59
	ds_bpermute_b32 v173, v71, v55
	ds_bpermute_b32 v174, v71, v52
	s_waitcnt lgkmcnt(4)
	v_max_i32_e32 v54, v54, v168
	s_waitcnt lgkmcnt(3)
	v_max_i32_e32 v57, v57, v169
	s_waitcnt lgkmcnt(2)
	v_max_i32_e32 v60, v60, v170
	s_waitcnt lgkmcnt(1)
	v_max_i32_e32 v51, v51, v173
	s_waitcnt lgkmcnt(0)
	v_max_i32_e32 v56, v56, v174
	v_max_i32_e32 v58, v58, v167
	v_max_i32_e32 v50, v50, v166
	v_max_i32_e32 v59, v59, v165
	v_max_i32_e32 v160, v160, v164
	v_max_i32_e32 v47, v52, v163
	v_max_i32_e32 v52, v55, v162
	v_max_i32_e32 v49, v49, v161
	v_max_i32_e32 v48, v48, v61
	v_max_i32_e32 v55, v171, v58
	v_min_i32_e32 v58, v171, v58
	v_max_i32_e32 v61, v53, v50
	v_min_i32_e32 v50, v53, v50
	v_max_i32_e32 v53, v51, v59
	v_min_i32_e32 v51, v51, v59
	v_max_i32_e32 v59, v56, v160
	v_min_i32_e32 v56, v56, v160
	v_max_i32_e32 v160, v172, v47
	v_min_i32_e32 v47, v172, v47
	v_max_i32_e32 v161, v60, v52
	v_min_i32_e32 v52, v60, v52
	v_max_i32_e32 v60, v57, v49
	v_min_i32_e32 v49, v57, v49
	v_max_i32_e32 v57, v54, v48
	v_min_i32_e32 v48, v54, v48
	v_max_i32_e32 v54, v55, v160
	v_min_i32_e32 v55, v55, v160
	v_max_i32_e32 v160, v61, v161
	v_min_i32_e32 v61, v61, v161
	v_max_i32_e32 v161, v53, v60
	v_min_i32_e32 v53, v53, v60
	v_max_i32_e32 v60, v59, v57
	v_min_i32_e32 v57, v59, v57
	v_max_i32_e32 v59, v58, v47
	v_min_i32_e32 v47, v58, v47
	v_max_i32_e32 v58, v50, v52
	v_min_i32_e32 v50, v50, v52
	v_max_i32_e32 v52, v51, v49
	v_min_i32_e32 v49, v51, v49
	v_max_i32_e32 v51, v56, v48
	v_min_i32_e32 v48, v56, v48
	v_max_i32_e32 v56, v54, v161
	v_min_i32_e32 v54, v54, v161
	v_max_i32_e32 v161, v160, v60
	v_min_i32_e32 v60, v160, v60
	v_max_i32_e32 v160, v55, v53
	v_min_i32_e32 v53, v55, v53
	v_max_i32_e32 v55, v61, v57
	v_min_i32_e32 v57, v61, v57
	v_max_i32_e32 v61, v59, v52
	v_min_i32_e32 v52, v59, v52
	v_max_i32_e32 v59, v58, v51
	v_min_i32_e32 v51, v58, v51
	v_max_i32_e32 v58, v47, v49
	v_min_i32_e32 v47, v47, v49
	v_max_i32_e32 v49, v50, v48
	v_min_i32_e32 v48, v50, v48
	v_max_i32_e32 v164, v61, v59
	v_min_i32_e32 v59, v61, v59
	v_max_i32_e32 v61, v52, v51
	v_min_i32_e32 v51, v52, v51
	v_max_i32_e32 v52, v58, v49
	v_min_i32_e32 v49, v58, v49
	v_min_i32_e32 v165, v47, v48
	v_max_i32_e32 v47, v47, v48
	ds_bpermute_b32 v49, v108, v49
	ds_bpermute_b32 v58, v108, v61
	ds_bpermute_b32 v47, v108, v47
	ds_bpermute_b32 v51, v108, v51
	v_min_i32_e32 v162, v160, v55
	s_waitcnt vmcnt(0)
; __device__ __forceinline__ float ord2f(int o) { return __int_as_float(o ^ ((o >> 31) & 0x7fffffff)); }
; __device__ __forceinline__ void p10_topk(const Params& P, LAS unsigned char* lds, int tid, int lane, int wave, int vb) {
;     ...
;         for (int i = 0; i < 8; ++i) T8[i] = max(C[i], __shfl_xor(C[15 - i], 32));
;         const float rstd1 = rsqrtf(SSQ1[row] * (1.0f / 1024.0f) + EPS);
;         const float mx = ord2f(max(C[0], c0x) & ~0xff);
;         const bool outer = (g == 0) || (g == 3);
;         int oi[4]; float og[4], s4 = 0.f;
; #pragma unroll
;         for (int kk = 0; kk < 4; ++kk) {
;             const int key = outer ? T8[kk] : T8[4 + kk];
;             og[kk] = __expf((ord2f(key & ~0xff) - mx) * rstd1); s4 += og[kk];
;             const int a = (key >> 4) & 15, bq = key & 15;
;             oi[kk] = Tb[r * 32 + a] * 128 + Tb[r * 32 + 16 + bq];
;         }
;         s4 += __shfl_xor(s4, 16); s4 += __shfl_xor(s4, 32);
;         { const float inv = __builtin_amdgcn_rcpf(s4);
; #pragma unroll
;           for (int kk = 0; kk < 4; ++kk) og[kk] *= inv; }
;         { const int R0 = 8 * (2 * h + (g >> 1)) + 4 * (g & 1);
;           *(int4*)(REC + row * 768 + 4 * R0) = make_int4(oi[0], oi[1], oi[2], oi[3]); *(float4*)(GATE + row * 128 + R0) = make_float4(og[0], og[1], og[2], og[3]);
;           if (pvalid) { *(float4*)(SUR + poff) = make_float4(puv[0].x, puv[1].x, puv[2].x, puv[3].x); *(float4*)(SVR + poff) = make_float4(puv[0].y, puv[1].y, puv[2].y, puv[3].y); }
; #pragma unroll
;           for (int kk = 0; kk < 4; ++kk) puv[kk] = *(const float2*)(SUVt + 2 * oi[kk]);
;           poff = row * 128 + R0; pvalid = true; }
	v_fmamk_f32 v46, v46, 0x3a800000, v154
	v_max_i32_e32 v50, v56, v161
	v_min_i32_e32 v56, v56, v161
	v_min_i32_e32 v161, v54, v60
	s_waitcnt lgkmcnt(3)
	v_max3_i32 v49, v54, v60, v49
	s_waitcnt lgkmcnt(2)
	v_max_i32_e32 v54, v162, v58
	v_mul_f32_e32 v58, 0x4b800000, v46
	v_cmp_gt_f32_e32 vcc, s69, v46
	ds_bpermute_b32 v165, v108, v165
	ds_bpermute_b32 v52, v108, v52
	s_waitcnt lgkmcnt(3)
	v_max_i32_e32 v47, v56, v47
	s_waitcnt lgkmcnt(2)
	v_max3_i32 v51, v160, v55, v51
	ds_bpermute_b32 v55, v108, v59
	ds_bpermute_b32 v56, v108, v164
	v_cndmask_b32_e32 v46, v46, v58, vcc
	ds_bpermute_b32 v58, v108, v50
	v_rsq_f32_e32 v46, v46
	v_min_i32_e32 v163, v53, v57
	s_waitcnt lgkmcnt(4)
	v_max_i32_e32 v48, v50, v165
	s_waitcnt lgkmcnt(3)
	v_max_i32_e32 v52, v161, v52
	s_waitcnt lgkmcnt(2)
	v_max3_i32 v53, v53, v57, v55
	s_waitcnt lgkmcnt(1)
	v_max_i32_e32 v55, v163, v56
	s_waitcnt lgkmcnt(0)
	v_max_i32_e32 v50, v50, v58
	v_mul_f32_e32 v56, 0x45800000, v46
	v_cndmask_b32_e64 v48, v51, v48, s[14:15]
	v_cndmask_b32_e64 v55, v55, v52, s[14:15]
	v_and_b32_e32 v52, 0xffffff00, v50
	v_ashrrev_i32_e32 v50, 31, v50
	v_cndmask_b32_e32 v46, v46, v56, vcc
	v_and_b32_e32 v51, 0xffffff00, v48
	v_ashrrev_i32_e32 v56, 31, v48
	v_cndmask_b32_e64 v47, v54, v47, s[14:15]
	v_and_b32_e32 v50, 0x7fffffff, v50
	v_bitop3_b32 v51, v56, v51, s67 bitop3:0x6c
	v_and_b32_e32 v54, 0xffffff00, v47
	v_ashrrev_i32_e32 v57, 31, v47
	v_cndmask_b32_e64 v49, v53, v49, s[14:15]
	v_xor_b32_e32 v61, v50, v52
	v_bitop3_b32 v54, v57, v54, s67 bitop3:0x6c
	v_and_b32_e32 v53, 0xffffff00, v49
	v_ashrrev_i32_e32 v58, 31, v49
	v_ashrrev_i32_e32 v60, 31, v55
	v_sub_f32_e32 v50, v51, v61
	v_bitop3_b32 v53, v58, v53, s67 bitop3:0x6c
	v_and_b32_e32 v59, 0xffffff00, v55
	v_and_b32_e32 v60, 0x7fffffff, v60
	v_mul_f32_e32 v50, v50, v46
	v_sub_f32_e32 v51, v54, v61
	v_xor_b32_e32 v59, v60, v59
	v_mul_f32_e32 v50, 0x3fb8aa3b, v50
	v_mul_f32_e32 v51, v51, v46
	v_sub_f32_e32 v52, v53, v61
	v_exp_f32_e32 v50, v50
	v_mul_f32_e32 v51, 0x3fb8aa3b, v51
	v_mul_f32_e32 v52, v52, v46
	v_sub_f32_e32 v53, v59, v61
	v_exp_f32_e32 v51, v51
	v_mul_f32_e32 v52, 0x3fb8aa3b, v52
	v_mul_f32_e32 v46, v53, v46
	v_exp_f32_e32 v52, v52
	v_mul_f32_e32 v46, 0x3fb8aa3b, v46
	v_exp_f32_e32 v53, v46
	v_add_f32_e32 v46, 0, v50
	v_add_f32_e32 v46, v51, v46
	v_add_f32_e32 v46, v52, v46
	v_add_f32_e32 v46, v53, v46
	v_mov_b32_e32 v59, v46
	s_nop 1
	v_permlane16_swap_b32_e32 v59, v46
	v_and_b32_e32 v56, 15, v48
	v_lshrrev_b32_e32 v48, 2, v48
	v_and_b32_e32 v57, 15, v47
	v_lshrrev_b32_e32 v47, 2, v47
	s_waitcnt lgkmcnt(0)
	v_add_f32_e32 v46, v46, v59
	v_and_b32_e32 v58, 15, v49
	v_lshrrev_b32_e32 v49, 2, v49
	v_and_b32_e32 v54, 15, v55
	v_lshrrev_b32_e32 v55, 2, v55
	v_mov_b32_e32 v59, v46
	s_nop 1
	v_permlane32_swap_b32_e32 v59, v46
	v_and_b32_e32 v48, 60, v48
	v_and_b32_e32 v47, 60, v47
	v_and_b32_e32 v49, 60, v49
	v_and_b32_e32 v55, 60, v55
	v_add_u32_e32 v48, v122, v48
	v_add_u32_e32 v47, v122, v47
	v_add_u32_e32 v49, v122, v49
	v_lshl_add_u32 v58, v58, 2, v122
	v_add_u32_e32 v55, v122, v55
	v_lshl_add_u32 v56, v56, 2, v122
	v_lshl_add_u32 v57, v57, 2, v122
	v_lshl_add_u32 v54, v54, 2, v122
	ds_read_b32 v48, v48
	ds_read_b32 v60, v56 offset:64
	ds_read_b32 v47, v47
	ds_read_b32 v61, v57 offset:64
	ds_read_b32 v160, v49
	ds_read_b32 v58, v58 offset:64
	ds_read_b32 v49, v55
	ds_read_b32 v55, v54 offset:64
	s_waitcnt lgkmcnt(8)
	v_add_f32_e32 v46, v46, v59
	v_rcp_f32_e32 v54, v46
	v_lshl_add_u64 v[56:57], s[64:65], 0, v[92:93]
	v_add_co_u32_e32 v56, vcc, s71, v56
	s_waitcnt lgkmcnt(4)
	v_lshl_add_u32 v47, v47, 7, v61
	v_lshl_add_u32 v46, v48, 7, v60
	s_waitcnt lgkmcnt(0)
	v_lshl_add_u32 v49, v49, 7, v55
	v_lshl_add_u32 v48, v160, 7, v58
	v_addc_co_u32_e32 v57, vcc, 0, v57, vcc
	global_store_dwordx4 v[56:57], v[46:49], off
	v_lshl_add_u64 v[56:57], s[64:65], 0, v[96:97]
	v_pk_mul_f32 v[50:51], v[50:51], v[54:55] op_sel_hi:[1,0]
	v_pk_mul_f32 v[52:53], v[52:53], v[54:55] op_sel_hi:[1,0]
	v_add_co_u32_e32 v54, vcc, 0xa800000, v56
	s_nop 1
	v_addc_co_u32_e32 v55, vcc, 0, v57, vcc
	s_andn2_b64 vcc, exec, s[84:85]
	global_store_dwordx4 v[54:55], v[50:53], off
	s_cbranch_vccnz .LBB0_1254
	v_lshlrev_b64 v[54:55], 2, v[106:107]
	v_lshl_add_u64 v[56:57], s[26:27], 0, v[54:55]
	v_mov_b32_e32 v50, v84
	v_mov_b32_e32 v51, v2
	v_mov_b32_e32 v52, v80
	v_mov_b32_e32 v53, v4
	global_store_dwordx4 v[56:57], v[50:53], off
	v_mov_b32_e32 v2, v85
	v_mov_b32_e32 v4, v81
	v_lshl_add_u64 v[50:51], s[24:25], 0, v[54:55]
	global_store_dwordx4 v[50:51], v[2:5], off

; __device__ __forceinline__ float sigm(float x) { return __builtin_amdgcn_rcpf(1.0f + __builtin_amdgcn_exp2f(-1.4426950408889634f * x)); }
; __device__ __forceinline__ void unpack8(const u32x4& w, f32x4& v0, f32x4& v1) { v0[0] = bf_lo(w.x); v0[1] = bf_hi(w.x); v0[2] = bf_lo(w.y); v0[3] = bf_hi(w.y); v1[0] = bf_lo(w.z); v1[1] = bf_hi(w.z); v1[2] = bf_lo(w.w); v1[3] = bf_hi(w.w); }
; #define PG8_ELD(k) do { const size_t o_ = ob + (size_t)(((k) >> 2) * HALF + ((k) & 3) * 16) * 1024; eq[k][0] = *(const u32x4*)(e + o_); xq[k][0] = *(const u32x4*)(x2 + o_); eq[k][1] = *(const u32x4*)(e + o_ + 32); xq[k][1] = *(const u32x4*)(x2 + o_ + 32); } while (0)
;     __device__ __forceinline__ void run(f32x4 (&acc)[2][2][4][2], const Unit& u, int wr, int wc, int fr, int fq, PG8_LAS unsigned char* lds, int wid) const {
;         const int row0 = u.pm * BM + wr * 64 + fr;
;         float sq8[8], sv[8];
; #pragma unroll
;         for (int k = 0; k < 8; ++k) sq8[k] = ssq[row0 + (k >> 2) * HALF + (k & 3) * 16];
;         const size_t ob = (size_t)row0 * 1024 + u.pn * BM + wc * 64 + 8 * fq;
;         u32x4 eq[8][2], xq[8][2];
;     ...
;         PG8_ELD(0); PG8_ELD(1);
; #pragma unroll
;         for (int k = 0; k < 8; ++k) { const int ai = k >> 2, m = k & 3; float s = 0.f;
;             if (k + 2 < 8) PG8_ELD(k + 2);
;             const float rstd = rsqrtf(sq8[k] * (1.0f / 1024.0f) + 1e-6f);
; #pragma unroll
;             for (int bj = 0; bj < 2; ++bj) { f32x4 v0 = acc[ai][bj][m][0] * rstd, v1 = acc[ai][bj][m][1] * rstd, e0, e1, r0, r1; unpack8(eq[k][bj], e0, e1); unpack8(xq[k][bj], r0, r1);
; #pragma unroll
;                 for (int i = 0; i < 4; ++i) { v0[i] = r0[i] + sigm(v0[i]) * e0[i]; v1[i] = r1[i] + sigm(v1[i]) * e1[i]; }
.LBB0_1661:
	s_lshl_b32 s57, s76, 8
	s_add_i32 s57, s57, s92
	v_or_b32_e32 v206, s57, v195
	v_ashrrev_i32_e32 v207, 31, v206
	v_lshl_add_u64 v[0:1], v[206:207], 2, s[30:31]
	global_load_dword v30, v[0:1], off
	global_load_dword v31, v[0:1], off offset:64
	global_load_dword v232, v[0:1], off offset:128
	global_load_dword v234, v[0:1], off offset:192
	global_load_dword v233, v[0:1], off offset:512
	global_load_dword v231, v[0:1], off offset:576
	global_load_dword v229, v[0:1], off offset:640
	global_load_dword v227, v[0:1], off offset:704
	s_lshl_b32 s2, s77, 8
	v_lshlrev_b64 v[0:1], 10, v[206:207]
	s_ashr_i32 s3, s2, 31
	v_lshl_add_u64 v[0:1], v[0:1], 0, s[2:3]
	v_or_b32_e32 v0, v0, v194
	v_lshlrev_b64 v[0:1], 1, v[0:1]
	v_lshl_add_u64 v[212:213], s[28:29], 0, v[0:1]
	global_load_dwordx4 v[10:13], v[212:213], off
	v_lshl_add_u64 v[208:209], s[16:17], 0, v[0:1]
	global_load_dwordx4 v[6:9], v[208:209], off
	global_load_dwordx4 v[18:21], v[212:213], off offset:64
	global_load_dwordx4 v[14:17], v[208:209], off offset:64
	v_add_co_u32_e32 v2, vcc, s96, v212
	s_mov_b64 s[0:1], 0x8000
	s_nop 0
	v_addc_co_u32_e32 v3, vcc, 0, v213, vcc
	v_add_co_u32_e32 v4, vcc, s96, v208
	v_lshl_add_u64 v[0:1], v[212:213], 0, s[0:1]
	s_nop 0
	v_addc_co_u32_e32 v5, vcc, 0, v209, vcc
	global_load_dwordx4 v[22:25], v[2:3], off
	v_lshl_add_u64 v[2:3], v[208:209], 0, s[0:1]
	global_load_dwordx4 v[26:29], v[4:5], off
	global_load_dwordx4 v[180:183], v[0:1], off offset:64
	global_load_dwordx4 v[176:179], v[2:3], off offset:64
	v_and_b32_e32 v1, 64, v220
	v_xor_b32_e32 v0, 16, v220
	v_add_u32_e32 v1, 64, v1
	v_cmp_lt_i32_e32 vcc, v0, v1
	s_nop 1
	v_cndmask_b32_e32 v0, v220, v0, vcc
	v_lshlrev_b32_e32 v225, 2, v0
	v_xor_b32_e32 v0, 32, v220
	v_cmp_lt_i32_e32 vcc, v0, v1
	s_nop 1
	v_cndmask_b32_e32 v0, v220, v0, vcc
	v_add_co_u32_e32 v2, vcc, s88, v212
	v_lshlrev_b32_e32 v226, 2, v0
	s_nop 0
	v_addc_co_u32_e32 v3, vcc, 0, v213, vcc
	v_add_co_u32_e32 v4, vcc, s88, v208
	v_lshl_add_u64 v[0:1], v[212:213], 0, s[42:43]
	s_nop 0
	v_addc_co_u32_e32 v5, vcc, 0, v209, vcc
	global_load_dwordx4 v[168:171], v[2:3], off
	v_lshl_add_u64 v[2:3], v[208:209], 0, s[42:43]
	global_load_dwordx4 v[172:175], v[4:5], off
	global_load_dwordx4 v[156:159], v[0:1], off offset:64
	global_load_dwordx4 v[152:155], v[2:3], off offset:64
	s_waitcnt vmcnt(0)
	v_fmamk_f32 v0, v30, 0x3a800000, v221
	v_cmp_gt_f32_e32 vcc, s11, v0
	v_mul_f32_e32 v1, 0x4b800000, v0
	s_nop 0
	v_cndmask_b32_e32 v0, v0, v1, vcc
	v_rsq_f32_e32 v0, v0
	s_nop 0
	v_mul_f32_e32 v1, 0x45800000, v0
	v_cndmask_b32_e32 v30, v0, v1, vcc
	v_pk_mul_f32 v[0:1], v[164:165], v[30:31] op_sel_hi:[1,0]
	v_pk_mul_f32 v[4:5], v[160:161], v[30:31] op_sel_hi:[1,0]
	v_mul_f32_e32 v0, 0xbfb8aa3b, v0
	v_mul_f32_e32 v1, 0xbfb8aa3b, v1
	v_exp_f32_e32 v0, v0
	v_mul_f32_e32 v4, 0xbfb8aa3b, v4
	v_exp_f32_e32 v1, v1
	v_mul_f32_e32 v5, 0xbfb8aa3b, v5
	v_exp_f32_e32 v4, v4
	v_exp_f32_e32 v5, v5
	v_add_f32_e32 v0, 1.0, v0
	v_add_f32_e32 v1, 1.0, v1
	v_rcp_f32_e32 v0, v0
	v_add_f32_e32 v4, 1.0, v4
	v_rcp_f32_e32 v1, v1
	v_add_f32_e32 v5, 1.0, v5
	v_rcp_f32_e32 v4, v4
	v_rcp_f32_e32 v5, v5
	v_pk_mul_f32 v[2:3], v[166:167], v[30:31] op_sel_hi:[1,0]
	v_lshlrev_b32_e32 v160, 16, v10
	v_and_b32_e32 v161, 0xffff0000, v10
	v_lshlrev_b32_e32 v164, 16, v6
	v_and_b32_e32 v165, 0xffff0000, v6
	v_pk_mul_f32 v[162:163], v[162:163], v[30:31] op_sel_hi:[1,0]
	v_pk_fma_f32 v[0:1], v[0:1], v[160:161], v[164:165]
	v_lshlrev_b32_e32 v160, 16, v12
	v_and_b32_e32 v161, 0xffff0000, v12
	v_lshlrev_b32_e32 v164, 16, v8
	v_and_b32_e32 v165, 0xffff0000, v8
	v_mul_f32_e32 v2, 0xbfb8aa3b, v2
	v_mul_f32_e32 v3, 0xbfb8aa3b, v3
	v_pk_fma_f32 v[4:5], v[4:5], v[160:161], v[164:165]
	v_exp_f32_e32 v2, v2
	v_mul_f32_e32 v6, 0xbfb8aa3b, v162
	v_exp_f32_e32 v3, v3
	v_lshlrev_b32_e32 v160, 16, v7
	v_and_b32_e32 v161, 0xffff0000, v7
	v_mul_f32_e32 v7, 0xbfb8aa3b, v163
	v_exp_f32_e32 v6, v6
	v_exp_f32_e32 v7, v7
	v_add_f32_e32 v2, 1.0, v2
	v_add_f32_e32 v3, 1.0, v3
	v_rcp_f32_e32 v2, v2
	v_add_f32_e32 v6, 1.0, v6
	v_rcp_f32_e32 v3, v3
	v_add_f32_e32 v7, 1.0, v7
	v_rcp_f32_e32 v6, v6
	v_rcp_f32_e32 v7, v7
	v_lshlrev_b32_e32 v10, 16, v11
	v_and_b32_e32 v11, 0xffff0000, v11
	v_pk_fma_f32 v[2:3], v[2:3], v[10:11], v[160:161]
	v_lshlrev_b32_e32 v10, 16, v13
	v_and_b32_e32 v11, 0xffff0000, v13
	v_lshlrev_b32_e32 v8, 16, v9
	v_and_b32_e32 v9, 0xffff0000, v9
	v_pk_fma_f32 v[6:7], v[6:7], v[10:11], v[8:9]
	v_pk_mul_f32 v[8:9], v[148:149], v[30:31] op_sel_hi:[1,0]
	v_pk_mul_f32 v[12:13], v[144:145], v[30:31] op_sel_hi:[1,0]
	v_mul_f32_e32 v8, 0xbfb8aa3b, v8
	v_mul_f32_e32 v9, 0xbfb8aa3b, v9
	v_exp_f32_e32 v8, v8
	v_mul_f32_e32 v12, 0xbfb8aa3b, v12
	v_exp_f32_e32 v9, v9
	v_mul_f32_e32 v13, 0xbfb8aa3b, v13
	v_exp_f32_e32 v12, v12
	v_exp_f32_e32 v13, v13
	v_add_f32_e32 v8, 1.0, v8
	v_add_f32_e32 v9, 1.0, v9
	v_rcp_f32_e32 v8, v8
	v_add_f32_e32 v12, 1.0, v12
	v_rcp_f32_e32 v9, v9
	v_add_f32_e32 v13, 1.0, v13
	v_rcp_f32_e32 v12, v12
	v_rcp_f32_e32 v13, v13
	v_pk_mul_f32 v[10:11], v[150:151], v[30:31] op_sel_hi:[1,0]
	v_lshlrev_b32_e32 v144, 16, v18
	v_and_b32_e32 v145, 0xffff0000, v18
	v_lshlrev_b32_e32 v148, 16, v14
	v_and_b32_e32 v149, 0xffff0000, v14
	v_pk_mul_f32 v[146:147], v[146:147], v[30:31] op_sel_hi:[1,0]
	v_pk_fma_f32 v[8:9], v[8:9], v[144:145], v[148:149]
	v_lshlrev_b32_e32 v144, 16, v20
	v_and_b32_e32 v145, 0xffff0000, v20
	v_lshlrev_b32_e32 v148, 16, v16
	v_and_b32_e32 v149, 0xffff0000, v16
	v_mul_f32_e32 v10, 0xbfb8aa3b, v10
	v_mul_f32_e32 v11, 0xbfb8aa3b, v11
	v_pk_fma_f32 v[12:13], v[12:13], v[144:145], v[148:149]
	v_exp_f32_e32 v10, v10
	v_mul_f32_e32 v14, 0xbfb8aa3b, v146
	v_exp_f32_e32 v11, v11
; __device__ __forceinline__ float sigm(float x) { return __builtin_amdgcn_rcpf(1.0f + __builtin_amdgcn_exp2f(-1.4426950408889634f * x)); }
; __device__ __forceinline__ void unpack8(const u32x4& w, f32x4& v0, f32x4& v1) { v0[0] = bf_lo(w.x); v0[1] = bf_hi(w.x); v0[2] = bf_lo(w.y); v0[3] = bf_hi(w.y); v1[0] = bf_lo(w.z); v1[1] = bf_hi(w.z); v1[2] = bf_lo(w.w); v1[3] = bf_hi(w.w); }
; #define PG8_ELD(k) do { const size_t o_ = ob + (size_t)(((k) >> 2) * HALF + ((k) & 3) * 16) * 1024; eq[k][0] = *(const u32x4*)(e + o_); xq[k][0] = *(const u32x4*)(x2 + o_); eq[k][1] = *(const u32x4*)(e + o_ + 32); xq[k][1] = *(const u32x4*)(x2 + o_ + 32); } while (0)
;     __device__ __forceinline__ void run(f32x4 (&acc)[2][2][4][2], const Unit& u, int wr, int wc, int fr, int fq, PG8_LAS unsigned char* lds, int wid) const {
;     ...
;         for (int k = 0; k < 8; ++k) { const int ai = k >> 2, m = k & 3; float s = 0.f;
;             if (k + 2 < 8) PG8_ELD(k + 2);
;             const float rstd = rsqrtf(sq8[k] * (1.0f / 1024.0f) + 1e-6f);
; #pragma unroll
;             for (int bj = 0; bj < 2; ++bj) { f32x4 v0 = acc[ai][bj][m][0] * rstd, v1 = acc[ai][bj][m][1] * rstd, e0, e1, r0, r1; unpack8(eq[k][bj], e0, e1); unpack8(xq[k][bj], r0, r1);
; #pragma unroll
;                 for (int i = 0; i < 4; ++i) { v0[i] = r0[i] + sigm(v0[i]) * e0[i]; v1[i] = r1[i] + sigm(v1[i]) * e1[i]; }
;                 s += (v0[0] * v0[0] + v0[1] * v0[1]) + (v0[2] * v0[2] + v0[3] * v0[3]) + (v1[0] * v1[0] + v1[1] * v1[1]) + (v1[2] * v1[2] + v1[3] * v1[3]);
;                 acc[ai][bj][m][0] = v0; acc[ai][bj][m][1] = v1; }
;             s += __shfl_xor(s, 16); s += __shfl_xor(s, 32); sv[k] = s;
;             asm volatile("" : "+v"(acc[ai][0][m][0]), "+v"(acc[ai][0][m][1]), "+v"(acc[ai][1][m][0]), "+v"(acc[ai][1][m][1]), "+v"(sv[k]) :: "memory"); }
	v_lshlrev_b32_e32 v144, 16, v15
	v_and_b32_e32 v145, 0xffff0000, v15
	v_mul_f32_e32 v15, 0xbfb8aa3b, v147
	v_exp_f32_e32 v14, v14
	v_exp_f32_e32 v15, v15
	v_add_f32_e32 v10, 1.0, v10
	v_add_f32_e32 v11, 1.0, v11
	v_rcp_f32_e32 v10, v10
	v_add_f32_e32 v14, 1.0, v14
	v_rcp_f32_e32 v11, v11
	v_add_f32_e32 v15, 1.0, v15
	v_rcp_f32_e32 v14, v14
	v_rcp_f32_e32 v15, v15
	v_lshlrev_b32_e32 v18, 16, v19
	v_and_b32_e32 v19, 0xffff0000, v19
	v_pk_fma_f32 v[10:11], v[10:11], v[18:19], v[144:145]
	v_lshlrev_b32_e32 v18, 16, v21
	v_and_b32_e32 v19, 0xffff0000, v21
	v_lshlrev_b32_e32 v16, 16, v17
	v_and_b32_e32 v17, 0xffff0000, v17
	v_pk_fma_f32 v[14:15], v[14:15], v[18:19], v[16:17]
	v_pk_mul_f32 v[16:17], v[8:9], v[8:9]
	v_pk_mul_f32 v[18:19], v[10:11], v[10:11]
	v_pk_mul_f32 v[160:161], v[0:1], v[0:1]
	v_pk_mul_f32 v[162:163], v[2:3], v[2:3]
	v_add_f32_e32 v18, v18, v19
	v_add_f32_e32 v16, v16, v17
	v_pk_mul_f32 v[164:165], v[4:5], v[4:5]
	v_pk_mul_f32 v[20:21], v[12:13], v[12:13]
	v_add_f32_e32 v16, v16, v18
	v_add_f32_e32 v18, v162, v163
	v_add_f32_e32 v19, v160, v161
	v_pk_mul_f32 v[166:167], v[6:7], v[6:7]
	v_pk_mul_f32 v[144:145], v[14:15], v[14:15]
	v_add_f32_e32 v17, v20, v21
	v_add_f32_e32 v18, v19, v18
	v_add_f32_e32 v19, v164, v165
	v_add_f32_e32 v30, v144, v145
	v_add_f32_e32 v16, v17, v16
	v_add_f32_e32 v17, v166, v167
	v_add_f32_e32 v18, v19, v18
	v_add_f32_e32 v16, v30, v16
	v_add_f32_e32 v17, v17, v18
	v_add_f32_e32 v16, v17, v16
	v_mov_b32_e32 v17, v16
	s_nop 1
	v_permlane16_swap_b32_e32 v17, v16
	v_add_co_u32_e32 v18, vcc, s95, v212
	s_waitcnt lgkmcnt(0)
	v_add_f32_e32 v16, v16, v17
	v_mov_b32_e32 v17, v16
	s_nop 1
	v_permlane32_swap_b32_e32 v17, v16
	v_addc_co_u32_e32 v19, vcc, 0, v213, vcc
	v_add_co_u32_e32 v20, vcc, s95, v208
	s_waitcnt lgkmcnt(0)
	v_add_f32_e32 v228, v16, v17
	v_lshl_add_u64 v[16:17], v[212:213], 0, s[46:47]
	v_addc_co_u32_e32 v21, vcc, 0, v209, vcc
	global_load_dwordx4 v[160:163], v[18:19], off
	v_lshl_add_u64 v[18:19], v[208:209], 0, s[46:47]
	global_load_dwordx4 v[164:167], v[20:21], off
	global_load_dwordx4 v[148:151], v[16:17], off offset:64
	global_load_dwordx4 v[144:147], v[18:19], off offset:64
	v_fmamk_f32 v16, v31, 0x3a800000, v221
	v_cmp_gt_f32_e32 vcc, s11, v16
	v_mul_f32_e32 v17, 0x4b800000, v16
	s_nop 0
	v_cndmask_b32_e32 v16, v16, v17, vcc
	v_rsq_f32_e32 v16, v16
	s_nop 0
	v_mul_f32_e32 v17, 0x45800000, v16
	v_cndmask_b32_e32 v30, v16, v17, vcc
	v_pk_mul_f32 v[16:17], v[140:141], v[30:31] op_sel_hi:[1,0]
	v_pk_mul_f32 v[20:21], v[136:137], v[30:31] op_sel_hi:[1,0]
	v_mul_f32_e32 v16, 0xbfb8aa3b, v16
	v_mul_f32_e32 v17, 0xbfb8aa3b, v17
	v_exp_f32_e32 v16, v16
	v_mul_f32_e32 v20, 0xbfb8aa3b, v20
	v_exp_f32_e32 v17, v17
	v_mul_f32_e32 v21, 0xbfb8aa3b, v21
	v_exp_f32_e32 v20, v20
	v_exp_f32_e32 v21, v21
	v_add_f32_e32 v16, 1.0, v16
	v_add_f32_e32 v17, 1.0, v17
	v_rcp_f32_e32 v16, v16
	v_add_f32_e32 v20, 1.0, v20
	v_rcp_f32_e32 v17, v17
	v_add_f32_e32 v21, 1.0, v21
	v_rcp_f32_e32 v20, v20
	v_rcp_f32_e32 v21, v21
	v_pk_mul_f32 v[18:19], v[142:143], v[30:31] op_sel_hi:[1,0]
	v_lshlrev_b32_e32 v136, 16, v22
	v_and_b32_e32 v137, 0xffff0000, v22
	v_lshlrev_b32_e32 v140, 16, v26
	v_and_b32_e32 v141, 0xffff0000, v26
	v_pk_mul_f32 v[138:139], v[138:139], v[30:31] op_sel_hi:[1,0]
	v_pk_fma_f32 v[16:17], v[16:17], v[136:137], v[140:141]
	v_lshlrev_b32_e32 v136, 16, v24
	v_and_b32_e32 v137, 0xffff0000, v24
	v_lshlrev_b32_e32 v140, 16, v28
	v_and_b32_e32 v141, 0xffff0000, v28
	v_mul_f32_e32 v18, 0xbfb8aa3b, v18
	v_mul_f32_e32 v19, 0xbfb8aa3b, v19
	v_pk_fma_f32 v[20:21], v[20:21], v[136:137], v[140:141]
	v_exp_f32_e32 v18, v18
	v_mul_f32_e32 v22, 0xbfb8aa3b, v138
	v_exp_f32_e32 v19, v19
	v_lshlrev_b32_e32 v136, 16, v23
	v_and_b32_e32 v137, 0xffff0000, v23
	v_mul_f32_e32 v23, 0xbfb8aa3b, v139
	v_exp_f32_e32 v22, v22
	v_exp_f32_e32 v23, v23
	v_add_f32_e32 v18, 1.0, v18
	v_add_f32_e32 v19, 1.0, v19
	v_rcp_f32_e32 v18, v18
	v_add_f32_e32 v22, 1.0, v22
	v_rcp_f32_e32 v19, v19
	v_add_f32_e32 v23, 1.0, v23
	v_rcp_f32_e32 v22, v22
	v_rcp_f32_e32 v23, v23
	v_lshlrev_b32_e32 v26, 16, v27
	v_and_b32_e32 v27, 0xffff0000, v27
	v_pk_fma_f32 v[18:19], v[18:19], v[136:137], v[26:27]
	v_lshlrev_b32_e32 v24, 16, v25
	v_and_b32_e32 v25, 0xffff0000, v25
	v_lshlrev_b32_e32 v26, 16, v29
	v_and_b32_e32 v27, 0xffff0000, v29
	v_pk_fma_f32 v[22:23], v[22:23], v[24:25], v[26:27]
	v_pk_mul_f32 v[24:25], v[132:133], v[30:31] op_sel_hi:[1,0]
	v_pk_mul_f32 v[28:29], v[128:129], v[30:31] op_sel_hi:[1,0]
	v_mul_f32_e32 v24, 0xbfb8aa3b, v24
	v_mul_f32_e32 v25, 0xbfb8aa3b, v25
	v_exp_f32_e32 v24, v24
	v_mul_f32_e32 v28, 0xbfb8aa3b, v28
	v_exp_f32_e32 v25, v25
	v_mul_f32_e32 v29, 0xbfb8aa3b, v29
	v_exp_f32_e32 v28, v28
	v_exp_f32_e32 v29, v29
	v_add_f32_e32 v24, 1.0, v24
	v_add_f32_e32 v25, 1.0, v25
	v_rcp_f32_e32 v24, v24
	v_add_f32_e32 v28, 1.0, v28
	v_rcp_f32_e32 v25, v25
	v_add_f32_e32 v29, 1.0, v29
	v_rcp_f32_e32 v28, v28
	v_rcp_f32_e32 v29, v29
	v_pk_mul_f32 v[26:27], v[134:135], v[30:31] op_sel_hi:[1,0]
	v_pk_mul_f32 v[130:131], v[130:131], v[30:31] op_sel_hi:[1,0]
	v_lshlrev_b32_e32 v30, 16, v180
	v_and_b32_e32 v31, 0xffff0000, v180
	v_lshlrev_b32_e32 v128, 16, v176
	v_and_b32_e32 v129, 0xffff0000, v176
	v_pk_fma_f32 v[24:25], v[24:25], v[30:31], v[128:129]
	v_lshlrev_b32_e32 v30, 16, v182
	v_and_b32_e32 v31, 0xffff0000, v182
	v_lshlrev_b32_e32 v128, 16, v178
	v_and_b32_e32 v129, 0xffff0000, v178
	v_mul_f32_e32 v26, 0xbfb8aa3b, v26
	v_mul_f32_e32 v27, 0xbfb8aa3b, v27
	v_pk_fma_f32 v[28:29], v[28:29], v[30:31], v[128:129]
	v_exp_f32_e32 v26, v26
	v_mul_f32_e32 v30, 0xbfb8aa3b, v130
	v_exp_f32_e32 v27, v27
	v_mul_f32_e32 v31, 0xbfb8aa3b, v131
; __device__ __forceinline__ float sigm(float x) { return __builtin_amdgcn_rcpf(1.0f + __builtin_amdgcn_exp2f(-1.4426950408889634f * x)); }
; __device__ __forceinline__ void unpack8(const u32x4& w, f32x4& v0, f32x4& v1) { v0[0] = bf_lo(w.x); v0[1] = bf_hi(w.x); v0[2] = bf_lo(w.y); v0[3] = bf_hi(w.y); v1[0] = bf_lo(w.z); v1[1] = bf_hi(w.z); v1[2] = bf_lo(w.w); v1[3] = bf_hi(w.w); }
; #define PG8_ELD(k) do { const size_t o_ = ob + (size_t)(((k) >> 2) * HALF + ((k) & 3) * 16) * 1024; eq[k][0] = *(const u32x4*)(e + o_); xq[k][0] = *(const u32x4*)(x2 + o_); eq[k][1] = *(const u32x4*)(e + o_ + 32); xq[k][1] = *(const u32x4*)(x2 + o_ + 32); } while (0)
;     __device__ __forceinline__ void run(f32x4 (&acc)[2][2][4][2], const Unit& u, int wr, int wc, int fr, int fq, PG8_LAS unsigned char* lds, int wid) const {
;     ...
;         for (int k = 0; k < 8; ++k) { const int ai = k >> 2, m = k & 3; float s = 0.f;
;             if (k + 2 < 8) PG8_ELD(k + 2);
;             const float rstd = rsqrtf(sq8[k] * (1.0f / 1024.0f) + 1e-6f);
; #pragma unroll
;             for (int bj = 0; bj < 2; ++bj) { f32x4 v0 = acc[ai][bj][m][0] * rstd, v1 = acc[ai][bj][m][1] * rstd, e0, e1, r0, r1; unpack8(eq[k][bj], e0, e1); unpack8(xq[k][bj], r0, r1);
; #pragma unroll
;                 for (int i = 0; i < 4; ++i) { v0[i] = r0[i] + sigm(v0[i]) * e0[i]; v1[i] = r1[i] + sigm(v1[i]) * e1[i]; }
;                 s += (v0[0] * v0[0] + v0[1] * v0[1]) + (v0[2] * v0[2] + v0[3] * v0[3]) + (v1[0] * v1[0] + v1[1] * v1[1]) + (v1[2] * v1[2] + v1[3] * v1[3]);
;                 acc[ai][bj][m][0] = v0; acc[ai][bj][m][1] = v1; }
	v_exp_f32_e32 v30, v30
	v_exp_f32_e32 v31, v31
	v_add_f32_e32 v26, 1.0, v26
	v_add_f32_e32 v27, 1.0, v27
	v_rcp_f32_e32 v26, v26
	v_add_f32_e32 v30, 1.0, v30
	v_rcp_f32_e32 v27, v27
	v_add_f32_e32 v31, 1.0, v31
	v_rcp_f32_e32 v30, v30
	v_rcp_f32_e32 v31, v31
	v_lshlrev_b32_e32 v128, 16, v181
	v_and_b32_e32 v129, 0xffff0000, v181
	v_lshlrev_b32_e32 v132, 16, v177
	v_and_b32_e32 v133, 0xffff0000, v177
	v_pk_fma_f32 v[26:27], v[26:27], v[128:129], v[132:133]
	v_lshlrev_b32_e32 v128, 16, v183
	v_and_b32_e32 v129, 0xffff0000, v183
	v_lshlrev_b32_e32 v130, 16, v179
	v_and_b32_e32 v131, 0xffff0000, v179
	v_pk_fma_f32 v[30:31], v[30:31], v[128:129], v[130:131]
	v_pk_mul_f32 v[128:129], v[24:25], v[24:25]
	v_pk_mul_f32 v[130:131], v[26:27], v[26:27]
	v_pk_mul_f32 v[132:133], v[28:29], v[28:29]
	v_add_f32_e32 v130, v130, v131
	v_add_f32_e32 v128, v128, v129
	v_pk_mul_f32 v[136:137], v[16:17], v[16:17]
	v_pk_mul_f32 v[138:139], v[18:19], v[18:19]
	v_add_f32_e32 v128, v128, v130
	v_add_f32_e32 v129, v132, v133
	v_pk_mul_f32 v[140:141], v[20:21], v[20:21]
	v_add_f32_e32 v128, v129, v128
	v_add_f32_e32 v129, v138, v139
	v_add_f32_e32 v130, v136, v137
	v_pk_mul_f32 v[142:143], v[22:23], v[22:23]
	v_add_f32_e32 v129, v130, v129
	v_add_f32_e32 v130, v140, v141
	v_add_f32_e32 v129, v130, v129
	v_add_f32_e32 v130, v142, v143
	v_add_f32_e32 v129, v130, v129
	v_add_co_u32_e32 v130, vcc, s8, v212
	v_fmamk_f32 v136, v232, 0x3a800000, v221
	s_nop 0
	v_addc_co_u32_e32 v131, vcc, 0, v213, vcc
	v_add_co_u32_e32 v132, vcc, s8, v208
	v_mul_f32_e32 v137, 0x4b800000, v136
	s_nop 0
	v_addc_co_u32_e32 v133, vcc, 0, v209, vcc
	v_cmp_gt_f32_e32 vcc, s11, v136
	v_lshlrev_b32_e32 v140, 16, v172
	v_and_b32_e32 v141, 0xffff0000, v172
	v_cndmask_b32_e32 v136, v136, v137, vcc
	v_rsq_f32_e32 v136, v136
	v_lshlrev_b32_e32 v142, 16, v173
	v_and_b32_e32 v143, 0xffff0000, v173
	v_pk_mul_f32 v[134:135], v[30:31], v[30:31]
	v_mul_f32_e32 v137, 0x45800000, v136
	v_cndmask_b32_e32 v136, v136, v137, vcc
	v_pk_mul_f32 v[138:139], v[106:107], v[136:137] op_sel_hi:[1,0]
	v_pk_mul_f32 v[106:107], v[104:105], v[136:137] op_sel_hi:[1,0]
	v_pk_mul_f32 v[108:109], v[108:109], v[136:137] op_sel_hi:[1,0]
	v_mul_f32_e32 v105, 0xbfb8aa3b, v106
	v_exp_f32_e32 v105, v105
	v_mul_f32_e32 v104, 0xbfb8aa3b, v108
	v_exp_f32_e32 v104, v104
	v_mul_f32_e32 v107, 0xbfb8aa3b, v107
	v_add_f32_e32 v105, 1.0, v105
	v_rcp_f32_e32 v106, v105
	v_mul_f32_e32 v105, 0xbfb8aa3b, v109
	v_exp_f32_e32 v105, v105
	v_exp_f32_e32 v107, v107
	v_add_f32_e32 v104, 1.0, v104
	v_rcp_f32_e32 v104, v104
	v_add_f32_e32 v105, 1.0, v105
	v_rcp_f32_e32 v105, v105
	v_add_f32_e32 v107, 1.0, v107
	v_rcp_f32_e32 v107, v107
	v_lshlrev_b32_e32 v108, 16, v168
	v_and_b32_e32 v109, 0xffff0000, v168
	v_pk_fma_f32 v[104:105], v[104:105], v[108:109], v[140:141]
	v_lshlrev_b32_e32 v108, 16, v170
	v_and_b32_e32 v109, 0xffff0000, v170
	v_lshlrev_b32_e32 v140, 16, v174
	v_and_b32_e32 v141, 0xffff0000, v174
	v_pk_fma_f32 v[108:109], v[106:107], v[108:109], v[140:141]
	v_mul_f32_e32 v107, 0xbfb8aa3b, v138
	v_exp_f32_e32 v107, v107
	v_pk_mul_f32 v[110:111], v[110:111], v[136:137] op_sel_hi:[1,0]
	v_lshlrev_b32_e32 v138, 16, v171
	v_mul_f32_e32 v106, 0xbfb8aa3b, v110
	v_add_f32_e32 v107, 1.0, v107
	v_rcp_f32_e32 v110, v107
	v_mul_f32_e32 v107, 0xbfb8aa3b, v111
	v_mul_f32_e32 v111, 0xbfb8aa3b, v139
	v_and_b32_e32 v139, 0xffff0000, v171
	v_pk_mul_f32 v[170:171], v[122:123], v[136:137] op_sel_hi:[1,0]
	v_pk_mul_f32 v[122:123], v[120:121], v[136:137] op_sel_hi:[1,0]
	v_pk_mul_f32 v[124:125], v[124:125], v[136:137] op_sel_hi:[1,0]
	v_mul_f32_e32 v121, 0xbfb8aa3b, v122
	v_exp_f32_e32 v121, v121
	v_mul_f32_e32 v120, 0xbfb8aa3b, v124
	v_exp_f32_e32 v120, v120
	v_mul_f32_e32 v123, 0xbfb8aa3b, v123
	v_add_f32_e32 v121, 1.0, v121
	v_rcp_f32_e32 v122, v121
	v_mul_f32_e32 v121, 0xbfb8aa3b, v125
	v_exp_f32_e32 v121, v121
	v_exp_f32_e32 v123, v123
	v_add_f32_e32 v120, 1.0, v120
	v_rcp_f32_e32 v120, v120
	v_add_f32_e32 v121, 1.0, v121
	v_rcp_f32_e32 v121, v121
	v_add_f32_e32 v123, 1.0, v123
	v_rcp_f32_e32 v123, v123
	v_pk_mul_f32 v[126:127], v[126:127], v[136:137] op_sel_hi:[1,0]
	v_lshlrev_b32_e32 v124, 16, v156
	v_and_b32_e32 v125, 0xffff0000, v156
	v_lshlrev_b32_e32 v136, 16, v152
	v_and_b32_e32 v137, 0xffff0000, v152
	v_pk_fma_f32 v[120:121], v[120:121], v[124:125], v[136:137]
	v_lshlrev_b32_e32 v124, 16, v158
	v_and_b32_e32 v125, 0xffff0000, v158
	v_lshlrev_b32_e32 v136, 16, v154
	v_and_b32_e32 v137, 0xffff0000, v154
	v_pk_fma_f32 v[124:125], v[122:123], v[124:125], v[136:137]
	v_mul_f32_e32 v123, 0xbfb8aa3b, v170
	v_exp_f32_e32 v123, v123
	v_mul_f32_e32 v122, 0xbfb8aa3b, v126
	v_exp_f32_e32 v122, v122
	v_exp_f32_e32 v106, v106
	v_add_f32_e32 v123, 1.0, v123
	v_rcp_f32_e32 v126, v123
	v_mul_f32_e32 v123, 0xbfb8aa3b, v127
	v_exp_f32_e32 v123, v123
	v_mul_f32_e32 v127, 0xbfb8aa3b, v171
	v_exp_f32_e32 v127, v127
	v_exp_f32_e32 v107, v107
	v_exp_f32_e32 v111, v111
	v_add_f32_e32 v122, 1.0, v122
	v_add_f32_e32 v123, 1.0, v123
	v_rcp_f32_e32 v122, v122
	v_rcp_f32_e32 v123, v123
	v_add_f32_e32 v127, 1.0, v127
	v_add_f32_e32 v106, 1.0, v106
	v_add_f32_e32 v107, 1.0, v107
	v_rcp_f32_e32 v127, v127
	v_rcp_f32_e32 v106, v106
	v_rcp_f32_e32 v107, v107
	v_add_f32_e32 v111, 1.0, v111
	v_rcp_f32_e32 v111, v111
	v_lshlrev_b32_e32 v136, 16, v157
	v_and_b32_e32 v137, 0xffff0000, v157
	v_lshlrev_b32_e32 v152, 16, v153
	v_and_b32_e32 v153, 0xffff0000, v153
	v_pk_fma_f32 v[122:123], v[122:123], v[136:137], v[152:153]
	v_lshlrev_b32_e32 v136, 16, v159
	v_and_b32_e32 v137, 0xffff0000, v159
	v_lshlrev_b32_e32 v152, 16, v155
	v_and_b32_e32 v153, 0xffff0000, v155
	v_lshlrev_b32_e32 v140, 16, v169
; __device__ __forceinline__ float sigm(float x) { return __builtin_amdgcn_rcpf(1.0f + __builtin_amdgcn_exp2f(-1.4426950408889634f * x)); }
; __device__ __forceinline__ void unpack8(const u32x4& w, f32x4& v0, f32x4& v1) { v0[0] = bf_lo(w.x); v0[1] = bf_hi(w.x); v0[2] = bf_lo(w.y); v0[3] = bf_hi(w.y); v1[0] = bf_lo(w.z); v1[1] = bf_hi(w.z); v1[2] = bf_lo(w.w); v1[3] = bf_hi(w.w); }
; #define PG8_ELD(k) do { const size_t o_ = ob + (size_t)(((k) >> 2) * HALF + ((k) & 3) * 16) * 1024; eq[k][0] = *(const u32x4*)(e + o_); xq[k][0] = *(const u32x4*)(x2 + o_); eq[k][1] = *(const u32x4*)(e + o_ + 32); xq[k][1] = *(const u32x4*)(x2 + o_ + 32); } while (0)
;     __device__ __forceinline__ void run(f32x4 (&acc)[2][2][4][2], const Unit& u, int wr, int wc, int fr, int fq, PG8_LAS unsigned char* lds, int wid) const {
;     ...
;         for (int k = 0; k < 8; ++k) { const int ai = k >> 2, m = k & 3; float s = 0.f;
;             if (k + 2 < 8) PG8_ELD(k + 2);
;             const float rstd = rsqrtf(sq8[k] * (1.0f / 1024.0f) + 1e-6f);
; #pragma unroll
;             for (int bj = 0; bj < 2; ++bj) { f32x4 v0 = acc[ai][bj][m][0] * rstd, v1 = acc[ai][bj][m][1] * rstd, e0, e1, r0, r1; unpack8(eq[k][bj], e0, e1); unpack8(xq[k][bj], r0, r1);
; #pragma unroll
;                 for (int i = 0; i < 4; ++i) { v0[i] = r0[i] + sigm(v0[i]) * e0[i]; v1[i] = r1[i] + sigm(v1[i]) * e1[i]; }
;                 s += (v0[0] * v0[0] + v0[1] * v0[1]) + (v0[2] * v0[2] + v0[3] * v0[3]) + (v1[0] * v1[0] + v1[1] * v1[1]) + (v1[2] * v1[2] + v1[3] * v1[3]);
;                 acc[ai][bj][m][0] = v0; acc[ai][bj][m][1] = v1; }
;             s += __shfl_xor(s, 16); s += __shfl_xor(s, 32); sv[k] = s;
;             asm volatile("" : "+v"(acc[ai][0][m][0]), "+v"(acc[ai][0][m][1]), "+v"(acc[ai][1][m][0]), "+v"(acc[ai][1][m][1]), "+v"(sv[k]) :: "memory"); }
	v_and_b32_e32 v141, 0xffff0000, v169
	v_pk_fma_f32 v[126:127], v[126:127], v[136:137], v[152:153]
	v_pk_mul_f32 v[136:137], v[120:121], v[120:121]
	v_pk_mul_f32 v[152:153], v[122:123], v[122:123]
	v_pk_fma_f32 v[106:107], v[106:107], v[140:141], v[142:143]
	v_lshlrev_b32_e32 v140, 16, v175
	v_and_b32_e32 v141, 0xffff0000, v175
	v_pk_mul_f32 v[154:155], v[124:125], v[124:125]
	v_add_f32_e32 v152, v152, v153
	v_add_f32_e32 v136, v136, v137
	v_pk_fma_f32 v[110:111], v[110:111], v[138:139], v[140:141]
	v_pk_mul_f32 v[138:139], v[104:105], v[104:105]
	v_pk_mul_f32 v[140:141], v[106:107], v[106:107]
	v_add_f32_e32 v136, v136, v152
	v_add_f32_e32 v137, v154, v155
	v_pk_mul_f32 v[142:143], v[108:109], v[108:109]
	v_add_f32_e32 v136, v137, v136
	v_add_f32_e32 v137, v140, v141
	v_add_f32_e32 v138, v138, v139
	v_pk_mul_f32 v[168:169], v[110:111], v[110:111]
	v_add_f32_e32 v137, v138, v137
	v_add_f32_e32 v138, v142, v143
	v_add_f32_e32 v137, v138, v137
	v_add_f32_e32 v138, v168, v169
	v_add_f32_e32 v137, v138, v137
	v_add_co_u32_e32 v138, vcc, s9, v212
	v_fmamk_f32 v168, v234, 0x3a800000, v221
	s_nop 0
	v_addc_co_u32_e32 v139, vcc, 0, v213, vcc
	v_add_co_u32_e32 v140, vcc, s9, v208
	v_mul_f32_e32 v169, 0x4b800000, v168
	s_nop 0
	v_addc_co_u32_e32 v141, vcc, 0, v209, vcc
	v_cmp_gt_f32_e32 vcc, s11, v168
	v_add_f32_e32 v134, v134, v135
	v_add_f32_e32 v128, v134, v128
	v_cndmask_b32_e32 v168, v168, v169, vcc
	v_rsq_f32_e32 v168, v168
	v_add_f32_e32 v128, v129, v128
	v_mov_b32_e32 v129, v128
	s_nop 1
	v_permlane16_swap_b32_e32 v129, v128
	s_waitcnt vmcnt(2)
	v_lshlrev_b32_e32 v172, 16, v164
	v_mul_f32_e32 v169, 0x45800000, v168
	v_cndmask_b32_e32 v168, v168, v169, vcc
	v_pk_mul_f32 v[170:171], v[114:115], v[168:169] op_sel_hi:[1,0]
	v_pk_mul_f32 v[114:115], v[112:113], v[168:169] op_sel_hi:[1,0]
	s_waitcnt lgkmcnt(0)
	v_add_f32_e32 v128, v128, v129
	v_mul_f32_e32 v113, 0xbfb8aa3b, v114
	v_exp_f32_e32 v113, v113
	v_mov_b32_e32 v129, v128
	s_nop 1
	v_permlane32_swap_b32_e32 v129, v128
	v_pk_mul_f32 v[116:117], v[116:117], v[168:169] op_sel_hi:[1,0]
	v_mul_f32_e32 v115, 0xbfb8aa3b, v115
	v_add_f32_e32 v113, 1.0, v113
	v_mul_f32_e32 v112, 0xbfb8aa3b, v116
	v_rcp_f32_e32 v114, v113
	v_mul_f32_e32 v113, 0xbfb8aa3b, v117
	v_exp_f32_e32 v112, v112
	v_exp_f32_e32 v113, v113
	v_exp_f32_e32 v115, v115
	s_waitcnt lgkmcnt(0)
	v_add_f32_e32 v230, v128, v129
	v_add_f32_e32 v112, 1.0, v112
	v_add_f32_e32 v113, 1.0, v113
	global_load_dwordx4 v[176:179], v[130:131], off
	v_rcp_f32_e32 v112, v112
	v_rcp_f32_e32 v113, v113
	v_add_f32_e32 v115, 1.0, v115
	v_lshl_add_u64 v[128:129], v[212:213], 0, s[48:49]
	v_lshl_add_u64 v[130:131], v[208:209], 0, s[48:49]
	v_rcp_f32_e32 v115, v115
	global_load_dwordx4 v[180:183], v[132:133], off
	s_nop 0
	global_load_dwordx4 v[132:135], v[128:129], off offset:64
	s_nop 0
	global_load_dwordx4 v[128:131], v[130:131], off offset:64
	v_lshlrev_b32_e32 v116, 16, v160
	v_and_b32_e32 v117, 0xffff0000, v160
	v_and_b32_e32 v173, 0xffff0000, v164
	v_pk_fma_f32 v[112:113], v[112:113], v[116:117], v[172:173]
	v_lshlrev_b32_e32 v116, 16, v162
	v_and_b32_e32 v117, 0xffff0000, v162
	v_lshlrev_b32_e32 v172, 16, v166
	v_and_b32_e32 v173, 0xffff0000, v166
	v_pk_fma_f32 v[116:117], v[114:115], v[116:117], v[172:173]
	v_mul_f32_e32 v115, 0xbfb8aa3b, v170
	v_exp_f32_e32 v115, v115
	v_pk_mul_f32 v[118:119], v[118:119], v[168:169] op_sel_hi:[1,0]
	v_pk_mul_f32 v[100:101], v[100:101], v[168:169] op_sel_hi:[1,0]
	v_mul_f32_e32 v114, 0xbfb8aa3b, v118
	v_add_f32_e32 v115, 1.0, v115
	v_rcp_f32_e32 v118, v115
	v_mul_f32_e32 v115, 0xbfb8aa3b, v119
	v_mul_f32_e32 v119, 0xbfb8aa3b, v171
	v_pk_mul_f32 v[170:171], v[98:99], v[168:169] op_sel_hi:[1,0]
	v_pk_mul_f32 v[98:99], v[96:97], v[168:169] op_sel_hi:[1,0]
	v_mul_f32_e32 v96, 0xbfb8aa3b, v100
	v_mul_f32_e32 v97, 0xbfb8aa3b, v98
	v_exp_f32_e32 v97, v97
	v_exp_f32_e32 v96, v96
	v_mul_f32_e32 v99, 0xbfb8aa3b, v99
	v_exp_f32_e32 v99, v99
	v_add_f32_e32 v97, 1.0, v97
	v_rcp_f32_e32 v98, v97
	v_mul_f32_e32 v97, 0xbfb8aa3b, v101
	v_exp_f32_e32 v97, v97
	v_add_f32_e32 v96, 1.0, v96
	v_rcp_f32_e32 v96, v96
	v_add_f32_e32 v99, 1.0, v99
	v_add_f32_e32 v97, 1.0, v97
	v_rcp_f32_e32 v97, v97
	v_rcp_f32_e32 v99, v99
	v_pk_mul_f32 v[102:103], v[102:103], v[168:169] op_sel_hi:[1,0]
	s_waitcnt vmcnt(5)
	v_lshlrev_b32_e32 v100, 16, v148
	v_and_b32_e32 v101, 0xffff0000, v148
	s_waitcnt vmcnt(4)
; __device__ __forceinline__ float sigm(float x) { return __builtin_amdgcn_rcpf(1.0f + __builtin_amdgcn_exp2f(-1.4426950408889634f * x)); }
; __device__ __forceinline__ void unpack8(const u32x4& w, f32x4& v0, f32x4& v1) { v0[0] = bf_lo(w.x); v0[1] = bf_hi(w.x); v0[2] = bf_lo(w.y); v0[3] = bf_hi(w.y); v1[0] = bf_lo(w.z); v1[1] = bf_hi(w.z); v1[2] = bf_lo(w.w); v1[3] = bf_hi(w.w); }
; #define PG8_ELD(k) do { const size_t o_ = ob + (size_t)(((k) >> 2) * HALF + ((k) & 3) * 16) * 1024; eq[k][0] = *(const u32x4*)(e + o_); xq[k][0] = *(const u32x4*)(x2 + o_); eq[k][1] = *(const u32x4*)(e + o_ + 32); xq[k][1] = *(const u32x4*)(x2 + o_ + 32); } while (0)
;     __device__ __forceinline__ void run(f32x4 (&acc)[2][2][4][2], const Unit& u, int wr, int wc, int fr, int fq, PG8_LAS unsigned char* lds, int wid) const {
;     ...
;         for (int k = 0; k < 8; ++k) { const int ai = k >> 2, m = k & 3; float s = 0.f;
;             if (k + 2 < 8) PG8_ELD(k + 2);
;             const float rstd = rsqrtf(sq8[k] * (1.0f / 1024.0f) + 1e-6f);
; #pragma unroll
;             for (int bj = 0; bj < 2; ++bj) { f32x4 v0 = acc[ai][bj][m][0] * rstd, v1 = acc[ai][bj][m][1] * rstd, e0, e1, r0, r1; unpack8(eq[k][bj], e0, e1); unpack8(xq[k][bj], r0, r1);
; #pragma unroll
;                 for (int i = 0; i < 4; ++i) { v0[i] = r0[i] + sigm(v0[i]) * e0[i]; v1[i] = r1[i] + sigm(v1[i]) * e1[i]; }
;                 s += (v0[0] * v0[0] + v0[1] * v0[1]) + (v0[2] * v0[2] + v0[3] * v0[3]) + (v1[0] * v1[0] + v1[1] * v1[1]) + (v1[2] * v1[2] + v1[3] * v1[3]);
;                 acc[ai][bj][m][0] = v0; acc[ai][bj][m][1] = v1; }
;             s += __shfl_xor(s, 16); s += __shfl_xor(s, 32); sv[k] = s;
;             asm volatile("" : "+v"(acc[ai][0][m][0]), "+v"(acc[ai][0][m][1]), "+v"(acc[ai][1][m][0]), "+v"(acc[ai][1][m][1]), "+v"(sv[k]) :: "memory"); }
	v_lshlrev_b32_e32 v168, 16, v144
	v_and_b32_e32 v169, 0xffff0000, v144
	v_pk_fma_f32 v[96:97], v[96:97], v[100:101], v[168:169]
	v_lshlrev_b32_e32 v100, 16, v150
	v_and_b32_e32 v101, 0xffff0000, v150
	v_lshlrev_b32_e32 v168, 16, v146
	v_and_b32_e32 v169, 0xffff0000, v146
	v_pk_fma_f32 v[100:101], v[98:99], v[100:101], v[168:169]
	v_mul_f32_e32 v99, 0xbfb8aa3b, v170
	v_exp_f32_e32 v99, v99
	v_mul_f32_e32 v98, 0xbfb8aa3b, v102
	v_exp_f32_e32 v98, v98
	v_exp_f32_e32 v114, v114
	v_add_f32_e32 v99, 1.0, v99
	v_rcp_f32_e32 v102, v99
	v_mul_f32_e32 v99, 0xbfb8aa3b, v103
	v_exp_f32_e32 v99, v99
	v_mul_f32_e32 v103, 0xbfb8aa3b, v171
	v_exp_f32_e32 v103, v103
	v_exp_f32_e32 v115, v115
	v_exp_f32_e32 v119, v119
	v_add_f32_e32 v98, 1.0, v98
	v_add_f32_e32 v99, 1.0, v99
	v_rcp_f32_e32 v98, v98
	v_rcp_f32_e32 v99, v99
	v_add_f32_e32 v103, 1.0, v103
	v_add_f32_e32 v114, 1.0, v114
	v_add_f32_e32 v115, 1.0, v115
	v_rcp_f32_e32 v103, v103
	v_rcp_f32_e32 v114, v114
	v_rcp_f32_e32 v115, v115
	v_add_f32_e32 v119, 1.0, v119
	v_rcp_f32_e32 v119, v119
	v_lshlrev_b32_e32 v148, 16, v149
	v_and_b32_e32 v149, 0xffff0000, v149
	v_lshlrev_b32_e32 v144, 16, v145
	v_and_b32_e32 v145, 0xffff0000, v145
	v_pk_fma_f32 v[98:99], v[98:99], v[148:149], v[144:145]
	v_lshlrev_b32_e32 v144, 16, v151
	v_and_b32_e32 v145, 0xffff0000, v151
	v_lshlrev_b32_e32 v146, 16, v147
	v_and_b32_e32 v147, 0xffff0000, v147
	v_lshlrev_b32_e32 v160, 16, v161
	v_and_b32_e32 v161, 0xffff0000, v161
	v_lshlrev_b32_e32 v164, 16, v165
	v_and_b32_e32 v165, 0xffff0000, v165
	v_pk_fma_f32 v[102:103], v[102:103], v[144:145], v[146:147]
	v_pk_mul_f32 v[144:145], v[96:97], v[96:97]
	v_pk_mul_f32 v[146:147], v[98:99], v[98:99]
	v_pk_fma_f32 v[114:115], v[114:115], v[160:161], v[164:165]
	v_lshlrev_b32_e32 v160, 16, v163
	v_and_b32_e32 v161, 0xffff0000, v163
	v_lshlrev_b32_e32 v162, 16, v167
	v_and_b32_e32 v163, 0xffff0000, v167
	v_pk_mul_f32 v[148:149], v[100:101], v[100:101]
	v_add_f32_e32 v146, v146, v147
	v_add_f32_e32 v144, v144, v145
	v_pk_fma_f32 v[118:119], v[118:119], v[160:161], v[162:163]
	v_pk_mul_f32 v[160:161], v[112:113], v[112:113]
	v_pk_mul_f32 v[162:163], v[114:115], v[114:115]
	v_add_f32_e32 v144, v144, v146
	v_add_f32_e32 v145, v148, v149
	v_pk_mul_f32 v[164:165], v[116:117], v[116:117]
	v_add_f32_e32 v144, v145, v144
	v_add_f32_e32 v145, v162, v163
	v_add_f32_e32 v146, v160, v161
	v_pk_mul_f32 v[166:167], v[118:119], v[118:119]
	v_add_f32_e32 v145, v146, v145
	v_add_f32_e32 v146, v164, v165
	v_add_f32_e32 v145, v146, v145
	v_add_f32_e32 v146, v166, v167
	v_add_f32_e32 v145, v146, v145
	v_add_co_u32_e32 v146, vcc, s26, v212
	v_fmamk_f32 v168, v233, 0x3a800000, v221
	s_nop 0
	v_addc_co_u32_e32 v147, vcc, 0, v213, vcc
	v_add_co_u32_e32 v148, vcc, s26, v208
	v_mul_f32_e32 v169, 0x4b800000, v168
	s_nop 0
	v_addc_co_u32_e32 v149, vcc, 0, v209, vcc
	v_cmp_gt_f32_e32 vcc, s11, v168
	v_pk_mul_f32 v[156:157], v[126:127], v[126:127]
	s_waitcnt vmcnt(2)
	v_lshlrev_b32_e32 v172, 16, v180
	v_cndmask_b32_e32 v168, v168, v169, vcc
	v_rsq_f32_e32 v168, v168
	v_add_f32_e32 v156, v156, v157
	v_add_f32_e32 v136, v156, v136
	v_add_f32_e32 v136, v137, v136
	v_mul_f32_e32 v169, 0x45800000, v168
	v_cndmask_b32_e32 v168, v168, v169, vcc
	v_mov_b32_e32 v137, v136
	s_nop 1
	v_permlane16_swap_b32_e32 v137, v136
	v_pk_mul_f32 v[170:171], v[90:91], v[168:169] op_sel_hi:[1,0]
	v_pk_mul_f32 v[90:91], v[88:89], v[168:169] op_sel_hi:[1,0]
	v_pk_mul_f32 v[92:93], v[92:93], v[168:169] op_sel_hi:[1,0]
	v_mul_f32_e32 v89, 0xbfb8aa3b, v90
	v_exp_f32_e32 v89, v89
	s_waitcnt lgkmcnt(0)
	v_add_f32_e32 v136, v136, v137
	v_mov_b32_e32 v137, v136
	s_nop 1
	v_permlane32_swap_b32_e32 v137, v136
	v_mul_f32_e32 v88, 0xbfb8aa3b, v92
	v_add_f32_e32 v89, 1.0, v89
	v_rcp_f32_e32 v90, v89
	v_mul_f32_e32 v89, 0xbfb8aa3b, v93
	v_exp_f32_e32 v88, v88
	v_exp_f32_e32 v89, v89
	v_mul_f32_e32 v91, 0xbfb8aa3b, v91
	v_exp_f32_e32 v91, v91
	s_waitcnt lgkmcnt(0)
	v_add_f32_e32 v232, v136, v137
	v_add_f32_e32 v88, 1.0, v88
	v_add_f32_e32 v89, 1.0, v89
	global_load_dwordx4 v[152:155], v[138:139], off
	v_rcp_f32_e32 v88, v88
	v_rcp_f32_e32 v89, v89
	v_add_f32_e32 v91, 1.0, v91
	v_lshl_add_u64 v[136:137], v[212:213], 0, s[50:51]
	v_lshl_add_u64 v[138:139], v[208:209], 0, s[50:51]
	v_rcp_f32_e32 v91, v91
	global_load_dwordx4 v[156:159], v[140:141], off
	s_nop 0
	global_load_dwordx4 v[140:143], v[136:137], off offset:64
	s_nop 0
	global_load_dwordx4 v[136:139], v[138:139], off offset:64
	v_lshlrev_b32_e32 v92, 16, v176
	v_and_b32_e32 v93, 0xffff0000, v176
	v_and_b32_e32 v173, 0xffff0000, v180
	v_pk_fma_f32 v[88:89], v[88:89], v[92:93], v[172:173]
	v_lshlrev_b32_e32 v92, 16, v178
	v_and_b32_e32 v93, 0xffff0000, v178
	v_lshlrev_b32_e32 v172, 16, v182
	v_and_b32_e32 v173, 0xffff0000, v182
	v_pk_fma_f32 v[92:93], v[90:91], v[92:93], v[172:173]
	v_mul_f32_e32 v91, 0xbfb8aa3b, v170
	v_exp_f32_e32 v91, v91
	v_pk_mul_f32 v[94:95], v[94:95], v[168:169] op_sel_hi:[1,0]
	v_lshlrev_b32_e32 v170, 16, v179
	v_mul_f32_e32 v90, 0xbfb8aa3b, v94
	v_add_f32_e32 v91, 1.0, v91
	v_rcp_f32_e32 v94, v91
	v_mul_f32_e32 v91, 0xbfb8aa3b, v95
	v_mul_f32_e32 v95, 0xbfb8aa3b, v171
	v_and_b32_e32 v171, 0xffff0000, v179
	v_pk_mul_f32 v[178:179], v[82:83], v[168:169] op_sel_hi:[1,0]
	v_pk_mul_f32 v[82:83], v[80:81], v[168:169] op_sel_hi:[1,0]
	v_pk_mul_f32 v[84:85], v[84:85], v[168:169] op_sel_hi:[1,0]
	v_mul_f32_e32 v81, 0xbfb8aa3b, v82
	v_exp_f32_e32 v81, v81
	v_mul_f32_e32 v80, 0xbfb8aa3b, v84
	v_exp_f32_e32 v80, v80
	v_mul_f32_e32 v83, 0xbfb8aa3b, v83
	v_add_f32_e32 v81, 1.0, v81
	v_rcp_f32_e32 v82, v81
	v_mul_f32_e32 v81, 0xbfb8aa3b, v85
	v_exp_f32_e32 v81, v81
	v_exp_f32_e32 v83, v83
	v_add_f32_e32 v80, 1.0, v80
	v_rcp_f32_e32 v80, v80
	v_add_f32_e32 v81, 1.0, v81
	v_rcp_f32_e32 v81, v81
	v_add_f32_e32 v83, 1.0, v83
	v_rcp_f32_e32 v83, v83
	v_pk_mul_f32 v[86:87], v[86:87], v[168:169] op_sel_hi:[1,0]
	s_waitcnt vmcnt(5)
; __device__ __forceinline__ float sigm(float x) { return __builtin_amdgcn_rcpf(1.0f + __builtin_amdgcn_exp2f(-1.4426950408889634f * x)); }
; __device__ __forceinline__ void unpack8(const u32x4& w, f32x4& v0, f32x4& v1) { v0[0] = bf_lo(w.x); v0[1] = bf_hi(w.x); v0[2] = bf_lo(w.y); v0[3] = bf_hi(w.y); v1[0] = bf_lo(w.z); v1[1] = bf_hi(w.z); v1[2] = bf_lo(w.w); v1[3] = bf_hi(w.w); }
; #define PG8_ELD(k) do { const size_t o_ = ob + (size_t)(((k) >> 2) * HALF + ((k) & 3) * 16) * 1024; eq[k][0] = *(const u32x4*)(e + o_); xq[k][0] = *(const u32x4*)(x2 + o_); eq[k][1] = *(const u32x4*)(e + o_ + 32); xq[k][1] = *(const u32x4*)(x2 + o_ + 32); } while (0)
;     __device__ __forceinline__ void run(f32x4 (&acc)[2][2][4][2], const Unit& u, int wr, int wc, int fr, int fq, PG8_LAS unsigned char* lds, int wid) const {
;     ...
;         for (int k = 0; k < 8; ++k) { const int ai = k >> 2, m = k & 3; float s = 0.f;
;             if (k + 2 < 8) PG8_ELD(k + 2);
;             const float rstd = rsqrtf(sq8[k] * (1.0f / 1024.0f) + 1e-6f);
; #pragma unroll
;             for (int bj = 0; bj < 2; ++bj) { f32x4 v0 = acc[ai][bj][m][0] * rstd, v1 = acc[ai][bj][m][1] * rstd, e0, e1, r0, r1; unpack8(eq[k][bj], e0, e1); unpack8(xq[k][bj], r0, r1);
; #pragma unroll
;                 for (int i = 0; i < 4; ++i) { v0[i] = r0[i] + sigm(v0[i]) * e0[i]; v1[i] = r1[i] + sigm(v1[i]) * e1[i]; }
;                 s += (v0[0] * v0[0] + v0[1] * v0[1]) + (v0[2] * v0[2] + v0[3] * v0[3]) + (v1[0] * v1[0] + v1[1] * v1[1]) + (v1[2] * v1[2] + v1[3] * v1[3]);
;                 acc[ai][bj][m][0] = v0; acc[ai][bj][m][1] = v1; }
;             s += __shfl_xor(s, 16); s += __shfl_xor(s, 32); sv[k] = s;
;             asm volatile("" : "+v"(acc[ai][0][m][0]), "+v"(acc[ai][0][m][1]), "+v"(acc[ai][1][m][0]), "+v"(acc[ai][1][m][1]), "+v"(sv[k]) :: "memory"); }
	v_lshlrev_b32_e32 v84, 16, v132
	v_and_b32_e32 v85, 0xffff0000, v132
	s_waitcnt vmcnt(4)
	v_lshlrev_b32_e32 v168, 16, v128
	v_and_b32_e32 v169, 0xffff0000, v128
	v_pk_fma_f32 v[80:81], v[80:81], v[84:85], v[168:169]
	v_lshlrev_b32_e32 v84, 16, v134
	v_and_b32_e32 v85, 0xffff0000, v134
	v_lshlrev_b32_e32 v168, 16, v130
	v_and_b32_e32 v169, 0xffff0000, v130
	v_pk_fma_f32 v[84:85], v[82:83], v[84:85], v[168:169]
	v_mul_f32_e32 v83, 0xbfb8aa3b, v178
	v_exp_f32_e32 v83, v83
	v_mul_f32_e32 v82, 0xbfb8aa3b, v86
	v_exp_f32_e32 v82, v82
	v_exp_f32_e32 v90, v90
	v_add_f32_e32 v83, 1.0, v83
	v_rcp_f32_e32 v86, v83
	v_mul_f32_e32 v83, 0xbfb8aa3b, v87
	v_exp_f32_e32 v83, v83
	v_mul_f32_e32 v87, 0xbfb8aa3b, v179
	v_exp_f32_e32 v87, v87
	v_exp_f32_e32 v91, v91
	v_exp_f32_e32 v95, v95
	v_add_f32_e32 v82, 1.0, v82
	v_add_f32_e32 v83, 1.0, v83
	v_rcp_f32_e32 v82, v82
	v_rcp_f32_e32 v83, v83
	v_add_f32_e32 v87, 1.0, v87
	v_add_f32_e32 v90, 1.0, v90
	v_add_f32_e32 v91, 1.0, v91
	v_rcp_f32_e32 v87, v87
	v_rcp_f32_e32 v90, v90
	v_rcp_f32_e32 v91, v91
	v_add_f32_e32 v95, 1.0, v95
	v_rcp_f32_e32 v95, v95
	v_lshlrev_b32_e32 v132, 16, v133
	v_and_b32_e32 v133, 0xffff0000, v133
	v_lshlrev_b32_e32 v128, 16, v129
	v_and_b32_e32 v129, 0xffff0000, v129
	v_pk_fma_f32 v[82:83], v[82:83], v[132:133], v[128:129]
	v_lshlrev_b32_e32 v128, 16, v135
	v_and_b32_e32 v129, 0xffff0000, v135
	v_lshlrev_b32_e32 v130, 16, v131
	v_and_b32_e32 v131, 0xffff0000, v131
	v_lshlrev_b32_e32 v172, 16, v177
	v_and_b32_e32 v173, 0xffff0000, v177
	v_lshlrev_b32_e32 v174, 16, v181
	v_and_b32_e32 v175, 0xffff0000, v181
	v_pk_fma_f32 v[86:87], v[86:87], v[128:129], v[130:131]
	v_pk_mul_f32 v[128:129], v[80:81], v[80:81]
	v_pk_mul_f32 v[130:131], v[82:83], v[82:83]
	v_pk_fma_f32 v[90:91], v[90:91], v[172:173], v[174:175]
	v_lshlrev_b32_e32 v172, 16, v183
	v_and_b32_e32 v173, 0xffff0000, v183
	v_pk_mul_f32 v[132:133], v[84:85], v[84:85]
	v_add_f32_e32 v130, v130, v131
	v_add_f32_e32 v128, v128, v129
	v_pk_fma_f32 v[94:95], v[94:95], v[170:171], v[172:173]
	v_pk_mul_f32 v[170:171], v[88:89], v[88:89]
	v_pk_mul_f32 v[172:173], v[90:91], v[90:91]
	v_add_f32_e32 v128, v128, v130
	v_add_f32_e32 v129, v132, v133
	v_pk_mul_f32 v[174:175], v[92:93], v[92:93]
	v_add_f32_e32 v128, v129, v128
	v_add_f32_e32 v129, v172, v173
	v_add_f32_e32 v130, v170, v171
	v_pk_mul_f32 v[176:177], v[94:95], v[94:95]
	v_add_f32_e32 v129, v130, v129
	v_add_f32_e32 v130, v174, v175
	v_add_f32_e32 v129, v130, v129
	v_add_f32_e32 v130, v176, v177
	v_add_f32_e32 v129, v130, v129
	v_add_co_u32_e32 v130, vcc, s27, v212
	v_fmamk_f32 v177, v231, 0x3a800000, v221
	s_nop 0
	v_addc_co_u32_e32 v131, vcc, 0, v213, vcc
	v_add_co_u32_e32 v132, vcc, s27, v208
	v_mul_f32_e32 v178, 0x4b800000, v177
	s_nop 0
	v_addc_co_u32_e32 v133, vcc, 0, v209, vcc
	v_cmp_gt_f32_e32 vcc, s11, v177
	v_pk_mul_f32 v[150:151], v[102:103], v[102:103]
	s_waitcnt vmcnt(2)
	v_lshlrev_b32_e32 v182, 16, v156
	v_cndmask_b32_e32 v177, v177, v178, vcc
	v_rsq_f32_e32 v177, v177
	v_add_f32_e32 v150, v150, v151
	v_add_f32_e32 v144, v150, v144
	v_add_f32_e32 v144, v145, v144
	v_mul_f32_e32 v178, 0x45800000, v177
	v_cndmask_b32_e32 v178, v177, v178, vcc
	v_pk_mul_f32 v[180:181], v[74:75], v[178:179] op_sel_hi:[1,0]
	v_pk_mul_f32 v[74:75], v[72:73], v[178:179] op_sel_hi:[1,0]
	v_pk_mul_f32 v[76:77], v[76:77], v[178:179] op_sel_hi:[1,0]
	v_mul_f32_e32 v73, 0xbfb8aa3b, v74
	v_exp_f32_e32 v73, v73
	v_mul_f32_e32 v72, 0xbfb8aa3b, v76
	v_exp_f32_e32 v72, v72
	v_mul_f32_e32 v75, 0xbfb8aa3b, v75
	v_add_f32_e32 v73, 1.0, v73
	v_rcp_f32_e32 v74, v73
	v_mul_f32_e32 v73, 0xbfb8aa3b, v77
	v_exp_f32_e32 v73, v73
	v_mov_b32_e32 v145, v144
	s_nop 1
	v_permlane16_swap_b32_e32 v145, v144
	v_exp_f32_e32 v75, v75
	v_add_f32_e32 v72, 1.0, v72
	v_add_f32_e32 v73, 1.0, v73
	v_rcp_f32_e32 v72, v72
	v_rcp_f32_e32 v73, v73
	v_add_f32_e32 v75, 1.0, v75
	s_waitcnt lgkmcnt(0)
	v_add_f32_e32 v144, v144, v145
	v_rcp_f32_e32 v75, v75
	v_mov_b32_e32 v145, v144
	s_nop 1
	v_permlane32_swap_b32_e32 v145, v144
	v_lshlrev_b32_e32 v76, 16, v152
	v_and_b32_e32 v77, 0xffff0000, v152
	v_and_b32_e32 v183, 0xffff0000, v156
	v_pk_fma_f32 v[72:73], v[72:73], v[76:77], v[182:183]
	v_lshlrev_b32_e32 v76, 16, v154
	v_and_b32_e32 v77, 0xffff0000, v154
	v_lshlrev_b32_e32 v182, 16, v158
	v_and_b32_e32 v183, 0xffff0000, v158
	v_pk_fma_f32 v[76:77], v[74:75], v[76:77], v[182:183]
	v_mul_f32_e32 v75, 0xbfb8aa3b, v180
	v_exp_f32_e32 v75, v75
	s_waitcnt lgkmcnt(0)
	v_add_f32_e32 v234, v144, v145
	v_lshl_add_u64 v[144:145], v[212:213], 0, s[52:53]
	global_load_dwordx4 v[160:163], v[146:147], off
	v_lshl_add_u64 v[146:147], v[208:209], 0, s[52:53]
	global_load_dwordx4 v[164:167], v[148:149], off
	s_nop 0
	global_load_dwordx4 v[148:151], v[144:145], off offset:64
	s_nop 0
	global_load_dwordx4 v[144:147], v[146:147], off offset:64
	v_pk_mul_f32 v[78:79], v[78:79], v[178:179] op_sel_hi:[1,0]
	v_add_f32_e32 v75, 1.0, v75
	v_mul_f32_e32 v74, 0xbfb8aa3b, v78
	v_rcp_f32_e32 v78, v75
	v_mul_f32_e32 v75, 0xbfb8aa3b, v79
	v_mul_f32_e32 v79, 0xbfb8aa3b, v181
	v_pk_mul_f32 v[180:181], v[66:67], v[178:179] op_sel_hi:[1,0]
	v_pk_mul_f32 v[66:67], v[64:65], v[178:179] op_sel_hi:[1,0]
	v_pk_mul_f32 v[68:69], v[68:69], v[178:179] op_sel_hi:[1,0]
	v_mul_f32_e32 v65, 0xbfb8aa3b, v66
	v_exp_f32_e32 v65, v65
	v_mul_f32_e32 v64, 0xbfb8aa3b, v68
	v_exp_f32_e32 v64, v64
	v_mul_f32_e32 v67, 0xbfb8aa3b, v67
	v_add_f32_e32 v65, 1.0, v65
	v_rcp_f32_e32 v66, v65
	v_mul_f32_e32 v65, 0xbfb8aa3b, v69
	v_exp_f32_e32 v65, v65
	v_exp_f32_e32 v67, v67
	v_add_f32_e32 v64, 1.0, v64
	v_rcp_f32_e32 v64, v64
	v_add_f32_e32 v65, 1.0, v65
	v_rcp_f32_e32 v65, v65
	v_add_f32_e32 v67, 1.0, v67
	v_rcp_f32_e32 v67, v67
	v_pk_mul_f32 v[70:71], v[70:71], v[178:179] op_sel_hi:[1,0]
	s_waitcnt vmcnt(5)
; __device__ __forceinline__ float sigm(float x) { return __builtin_amdgcn_rcpf(1.0f + __builtin_amdgcn_exp2f(-1.4426950408889634f * x)); }
; __device__ __forceinline__ void unpack8(const u32x4& w, f32x4& v0, f32x4& v1) { v0[0] = bf_lo(w.x); v0[1] = bf_hi(w.x); v0[2] = bf_lo(w.y); v0[3] = bf_hi(w.y); v1[0] = bf_lo(w.z); v1[1] = bf_hi(w.z); v1[2] = bf_lo(w.w); v1[3] = bf_hi(w.w); }
; #define PG8_ELD(k) do { const size_t o_ = ob + (size_t)(((k) >> 2) * HALF + ((k) & 3) * 16) * 1024; eq[k][0] = *(const u32x4*)(e + o_); xq[k][0] = *(const u32x4*)(x2 + o_); eq[k][1] = *(const u32x4*)(e + o_ + 32); xq[k][1] = *(const u32x4*)(x2 + o_ + 32); } while (0)
;     __device__ __forceinline__ void run(f32x4 (&acc)[2][2][4][2], const Unit& u, int wr, int wc, int fr, int fq, PG8_LAS unsigned char* lds, int wid) const {
;     ...
;         for (int k = 0; k < 8; ++k) { const int ai = k >> 2, m = k & 3; float s = 0.f;
;             if (k + 2 < 8) PG8_ELD(k + 2);
;             const float rstd = rsqrtf(sq8[k] * (1.0f / 1024.0f) + 1e-6f);
; #pragma unroll
;             for (int bj = 0; bj < 2; ++bj) { f32x4 v0 = acc[ai][bj][m][0] * rstd, v1 = acc[ai][bj][m][1] * rstd, e0, e1, r0, r1; unpack8(eq[k][bj], e0, e1); unpack8(xq[k][bj], r0, r1);
; #pragma unroll
;                 for (int i = 0; i < 4; ++i) { v0[i] = r0[i] + sigm(v0[i]) * e0[i]; v1[i] = r1[i] + sigm(v1[i]) * e1[i]; }
;                 s += (v0[0] * v0[0] + v0[1] * v0[1]) + (v0[2] * v0[2] + v0[3] * v0[3]) + (v1[0] * v1[0] + v1[1] * v1[1]) + (v1[2] * v1[2] + v1[3] * v1[3]);
;                 acc[ai][bj][m][0] = v0; acc[ai][bj][m][1] = v1; }
;             s += __shfl_xor(s, 16); s += __shfl_xor(s, 32); sv[k] = s;
;             asm volatile("" : "+v"(acc[ai][0][m][0]), "+v"(acc[ai][0][m][1]), "+v"(acc[ai][1][m][0]), "+v"(acc[ai][1][m][1]), "+v"(sv[k]) :: "memory"); }
	v_lshlrev_b32_e32 v68, 16, v140
	v_and_b32_e32 v69, 0xffff0000, v140
	s_waitcnt vmcnt(4)
	v_lshlrev_b32_e32 v178, 16, v136
	v_and_b32_e32 v179, 0xffff0000, v136
	v_pk_fma_f32 v[64:65], v[64:65], v[68:69], v[178:179]
	v_lshlrev_b32_e32 v68, 16, v142
	v_and_b32_e32 v69, 0xffff0000, v142
	v_lshlrev_b32_e32 v178, 16, v138
	v_and_b32_e32 v179, 0xffff0000, v138
	v_pk_fma_f32 v[68:69], v[66:67], v[68:69], v[178:179]
	v_mul_f32_e32 v67, 0xbfb8aa3b, v180
	v_exp_f32_e32 v67, v67
	v_mul_f32_e32 v66, 0xbfb8aa3b, v70
	v_exp_f32_e32 v66, v66
	v_exp_f32_e32 v74, v74
	v_add_f32_e32 v67, 1.0, v67
	v_rcp_f32_e32 v70, v67
	v_mul_f32_e32 v67, 0xbfb8aa3b, v71
	v_exp_f32_e32 v67, v67
	v_mul_f32_e32 v71, 0xbfb8aa3b, v181
	v_exp_f32_e32 v71, v71
	v_exp_f32_e32 v75, v75
	v_exp_f32_e32 v79, v79
	v_add_f32_e32 v66, 1.0, v66
	v_add_f32_e32 v67, 1.0, v67
	v_rcp_f32_e32 v66, v66
	v_rcp_f32_e32 v67, v67
	v_add_f32_e32 v71, 1.0, v71
	v_add_f32_e32 v74, 1.0, v74
	v_add_f32_e32 v75, 1.0, v75
	v_rcp_f32_e32 v71, v71
	v_rcp_f32_e32 v74, v74
	v_rcp_f32_e32 v75, v75
	v_add_f32_e32 v79, 1.0, v79
	v_rcp_f32_e32 v79, v79
	v_lshlrev_b32_e32 v140, 16, v141
	v_and_b32_e32 v141, 0xffff0000, v141
	v_lshlrev_b32_e32 v136, 16, v137
	v_and_b32_e32 v137, 0xffff0000, v137
	v_pk_fma_f32 v[66:67], v[66:67], v[140:141], v[136:137]
	v_lshlrev_b32_e32 v136, 16, v143
	v_and_b32_e32 v137, 0xffff0000, v143
	v_lshlrev_b32_e32 v138, 16, v139
	v_and_b32_e32 v139, 0xffff0000, v139
	v_lshlrev_b32_e32 v152, 16, v153
	v_and_b32_e32 v153, 0xffff0000, v153
	v_lshlrev_b32_e32 v156, 16, v157
	v_and_b32_e32 v157, 0xffff0000, v157
	v_pk_fma_f32 v[70:71], v[70:71], v[136:137], v[138:139]
	v_pk_mul_f32 v[136:137], v[64:65], v[64:65]
	v_pk_mul_f32 v[138:139], v[66:67], v[66:67]
	v_pk_fma_f32 v[74:75], v[74:75], v[152:153], v[156:157]
	v_lshlrev_b32_e32 v152, 16, v155
	v_and_b32_e32 v153, 0xffff0000, v155
	v_lshlrev_b32_e32 v154, 16, v159
	v_and_b32_e32 v155, 0xffff0000, v159
	v_pk_mul_f32 v[140:141], v[68:69], v[68:69]
	v_add_f32_e32 v138, v138, v139
	v_add_f32_e32 v136, v136, v137
	v_pk_fma_f32 v[78:79], v[78:79], v[152:153], v[154:155]
	v_pk_mul_f32 v[152:153], v[72:73], v[72:73]
	v_pk_mul_f32 v[154:155], v[74:75], v[74:75]
	v_add_f32_e32 v136, v136, v138
	v_add_f32_e32 v137, v140, v141
	v_pk_mul_f32 v[156:157], v[76:77], v[76:77]
	v_add_f32_e32 v136, v137, v136
	v_add_f32_e32 v137, v154, v155
	v_add_f32_e32 v138, v152, v153
	v_pk_mul_f32 v[158:159], v[78:79], v[78:79]
	v_pk_mul_f32 v[142:143], v[70:71], v[70:71]
	v_add_f32_e32 v137, v138, v137
	v_add_f32_e32 v138, v156, v157
	v_add_f32_e32 v142, v142, v143
	v_add_f32_e32 v137, v138, v137
	v_add_f32_e32 v138, v158, v159
	v_add_f32_e32 v136, v142, v136
	v_add_f32_e32 v137, v138, v137
	v_add_f32_e32 v136, v137, v136
	v_mov_b32_e32 v137, v136
	s_nop 1
	v_permlane16_swap_b32_e32 v137, v136
	v_pk_mul_f32 v[134:135], v[86:87], v[86:87]
	s_waitcnt vmcnt(2)
	v_lshlrev_b32_e32 v142, 16, v164
	v_add_f32_e32 v134, v134, v135
	v_add_f32_e32 v128, v134, v128
	v_add_f32_e32 v128, v129, v128
	s_waitcnt lgkmcnt(0)
	v_add_f32_e32 v136, v136, v137
	v_mov_b32_e32 v129, v128
	s_nop 1
	v_permlane16_swap_b32_e32 v129, v128
	v_mov_b32_e32 v137, v136
	s_nop 1
	v_permlane32_swap_b32_e32 v137, v136
	v_and_b32_e32 v143, 0xffff0000, v164
	v_lshlrev_b32_e32 v152, 16, v165
	v_and_b32_e32 v153, 0xffff0000, v165
	s_waitcnt lgkmcnt(0)
	v_add_f32_e32 v128, v128, v129
	s_waitcnt lgkmcnt(0)
	v_add_f32_e32 v136, v136, v137
	v_fmamk_f32 v137, v229, 0x3a800000, v221
	v_mov_b32_e32 v129, v128
	s_nop 1
	v_permlane32_swap_b32_e32 v129, v128
	v_cmp_gt_f32_e32 vcc, s11, v137
	v_mul_f32_e32 v138, 0x4b800000, v137
	s_waitcnt lgkmcnt(0)
	v_add_f32_e32 v176, v128, v129
	v_cndmask_b32_e32 v137, v137, v138, vcc
	v_rsq_f32_e32 v137, v137
	v_lshl_add_u64 v[128:129], v[212:213], 0, s[54:55]
	global_load_dwordx4 v[168:171], v[130:131], off
	v_mul_f32_e32 v138, 0x45800000, v137
	v_lshl_add_u64 v[130:131], v[208:209], 0, s[54:55]
	v_cndmask_b32_e32 v138, v137, v138, vcc
	global_load_dwordx4 v[172:175], v[132:133], off
	s_nop 0
	global_load_dwordx4 v[132:135], v[128:129], off offset:64
	s_nop 0
	global_load_dwordx4 v[128:131], v[130:131], off offset:64
	v_pk_mul_f32 v[156:157], v[50:51], v[138:139] op_sel_hi:[1,0]
	v_pk_mul_f32 v[50:51], v[48:49], v[138:139] op_sel_hi:[1,0]
	v_pk_mul_f32 v[140:141], v[58:59], v[138:139] op_sel_hi:[1,0]
	v_mul_f32_e32 v49, 0xbfb8aa3b, v50
	v_exp_f32_e32 v49, v49
	v_pk_mul_f32 v[58:59], v[56:57], v[138:139] op_sel_hi:[1,0]
	v_pk_mul_f32 v[52:53], v[52:53], v[138:139] op_sel_hi:[1,0]
	v_mul_f32_e32 v57, 0xbfb8aa3b, v58
	v_exp_f32_e32 v57, v57
	v_add_f32_e32 v49, 1.0, v49
	v_mul_f32_e32 v48, 0xbfb8aa3b, v52
	v_rcp_f32_e32 v50, v49
	v_mul_f32_e32 v49, 0xbfb8aa3b, v53
	v_exp_f32_e32 v48, v48
	v_exp_f32_e32 v49, v49
	v_mul_f32_e32 v51, 0xbfb8aa3b, v51
	v_pk_mul_f32 v[60:61], v[60:61], v[138:139] op_sel_hi:[1,0]
	v_add_f32_e32 v57, 1.0, v57
	v_exp_f32_e32 v51, v51
	v_mul_f32_e32 v56, 0xbfb8aa3b, v60
	v_rcp_f32_e32 v58, v57
	v_mul_f32_e32 v57, 0xbfb8aa3b, v61
	v_exp_f32_e32 v56, v56
	v_exp_f32_e32 v57, v57
	v_mul_f32_e32 v59, 0xbfb8aa3b, v59
	v_exp_f32_e32 v59, v59
	v_add_f32_e32 v48, 1.0, v48
	v_add_f32_e32 v49, 1.0, v49
	v_rcp_f32_e32 v48, v48
	v_rcp_f32_e32 v49, v49
	v_add_f32_e32 v51, 1.0, v51
	v_rcp_f32_e32 v51, v51
	v_add_f32_e32 v56, 1.0, v56
	v_add_f32_e32 v57, 1.0, v57
	v_pk_mul_f32 v[62:63], v[62:63], v[138:139] op_sel_hi:[1,0]
	v_rcp_f32_e32 v56, v56
	v_rcp_f32_e32 v57, v57
	v_add_f32_e32 v59, 1.0, v59
	v_pk_mul_f32 v[54:55], v[54:55], v[138:139] op_sel_hi:[1,0]
	s_waitcnt vmcnt(5)
	v_lshlrev_b32_e32 v52, 16, v148
	v_and_b32_e32 v53, 0xffff0000, v148
	s_waitcnt vmcnt(4)
; __device__ __forceinline__ float sigm(float x) { return __builtin_amdgcn_rcpf(1.0f + __builtin_amdgcn_exp2f(-1.4426950408889634f * x)); }
; __device__ __forceinline__ void unpack8(const u32x4& w, f32x4& v0, f32x4& v1) { v0[0] = bf_lo(w.x); v0[1] = bf_hi(w.x); v0[2] = bf_lo(w.y); v0[3] = bf_hi(w.y); v1[0] = bf_lo(w.z); v1[1] = bf_hi(w.z); v1[2] = bf_lo(w.w); v1[3] = bf_hi(w.w); }
; #define PG8_ELD(k) do { const size_t o_ = ob + (size_t)(((k) >> 2) * HALF + ((k) & 3) * 16) * 1024; eq[k][0] = *(const u32x4*)(e + o_); xq[k][0] = *(const u32x4*)(x2 + o_); eq[k][1] = *(const u32x4*)(e + o_ + 32); xq[k][1] = *(const u32x4*)(x2 + o_ + 32); } while (0)
;     __device__ __forceinline__ void run(f32x4 (&acc)[2][2][4][2], const Unit& u, int wr, int wc, int fr, int fq, PG8_LAS unsigned char* lds, int wid) const {
;     ...
;         for (int k = 0; k < 8; ++k) { const int ai = k >> 2, m = k & 3; float s = 0.f;
;             if (k + 2 < 8) PG8_ELD(k + 2);
;             const float rstd = rsqrtf(sq8[k] * (1.0f / 1024.0f) + 1e-6f);
; #pragma unroll
;             for (int bj = 0; bj < 2; ++bj) { f32x4 v0 = acc[ai][bj][m][0] * rstd, v1 = acc[ai][bj][m][1] * rstd, e0, e1, r0, r1; unpack8(eq[k][bj], e0, e1); unpack8(xq[k][bj], r0, r1);
; #pragma unroll
;                 for (int i = 0; i < 4; ++i) { v0[i] = r0[i] + sigm(v0[i]) * e0[i]; v1[i] = r1[i] + sigm(v1[i]) * e1[i]; }
;                 s += (v0[0] * v0[0] + v0[1] * v0[1]) + (v0[2] * v0[2] + v0[3] * v0[3]) + (v1[0] * v1[0] + v1[1] * v1[1]) + (v1[2] * v1[2] + v1[3] * v1[3]);
;                 acc[ai][bj][m][0] = v0; acc[ai][bj][m][1] = v1; }
;             s += __shfl_xor(s, 16); s += __shfl_xor(s, 32); sv[k] = s;
;             asm volatile("" : "+v"(acc[ai][0][m][0]), "+v"(acc[ai][0][m][1]), "+v"(acc[ai][1][m][0]), "+v"(acc[ai][1][m][1]), "+v"(sv[k]) :: "memory"); }
	v_lshlrev_b32_e32 v138, 16, v144
	v_and_b32_e32 v139, 0xffff0000, v144
	v_rcp_f32_e32 v59, v59
	v_pk_fma_f32 v[48:49], v[48:49], v[52:53], v[138:139]
	v_lshlrev_b32_e32 v52, 16, v150
	v_and_b32_e32 v53, 0xffff0000, v150
	v_lshlrev_b32_e32 v138, 16, v146
	v_and_b32_e32 v139, 0xffff0000, v146
	v_pk_fma_f32 v[52:53], v[50:51], v[52:53], v[138:139]
	v_mul_f32_e32 v51, 0xbfb8aa3b, v156
	v_lshlrev_b32_e32 v60, 16, v160
	v_and_b32_e32 v61, 0xffff0000, v160
	v_exp_f32_e32 v51, v51
	v_pk_fma_f32 v[56:57], v[56:57], v[60:61], v[142:143]
	v_lshlrev_b32_e32 v60, 16, v162
	v_and_b32_e32 v61, 0xffff0000, v162
	v_lshlrev_b32_e32 v142, 16, v166
	v_and_b32_e32 v143, 0xffff0000, v166
	v_pk_fma_f32 v[60:61], v[58:59], v[60:61], v[142:143]
	v_mul_f32_e32 v59, 0xbfb8aa3b, v140
	v_exp_f32_e32 v59, v59
	v_add_f32_e32 v51, 1.0, v51
	v_mul_f32_e32 v50, 0xbfb8aa3b, v54
	v_rcp_f32_e32 v54, v51
	v_mul_f32_e32 v51, 0xbfb8aa3b, v55
	v_exp_f32_e32 v50, v50
	v_exp_f32_e32 v51, v51
	v_mul_f32_e32 v55, 0xbfb8aa3b, v157
	v_add_f32_e32 v59, 1.0, v59
	v_exp_f32_e32 v55, v55
	v_mul_f32_e32 v58, 0xbfb8aa3b, v62
	v_rcp_f32_e32 v62, v59
	v_mul_f32_e32 v59, 0xbfb8aa3b, v63
	v_exp_f32_e32 v58, v58
	v_exp_f32_e32 v59, v59
	v_mul_f32_e32 v63, 0xbfb8aa3b, v141
	v_exp_f32_e32 v63, v63
	v_add_f32_e32 v50, 1.0, v50
	v_add_f32_e32 v51, 1.0, v51
	v_rcp_f32_e32 v50, v50
	v_rcp_f32_e32 v51, v51
	v_add_f32_e32 v55, 1.0, v55
	v_rcp_f32_e32 v55, v55
	v_add_f32_e32 v58, 1.0, v58
	v_add_f32_e32 v59, 1.0, v59
	v_rcp_f32_e32 v58, v58
	v_rcp_f32_e32 v59, v59
	v_add_f32_e32 v63, 1.0, v63
	v_lshlrev_b32_e32 v138, 16, v149
	v_and_b32_e32 v139, 0xffff0000, v149
	v_lshlrev_b32_e32 v144, 16, v145
	v_and_b32_e32 v145, 0xffff0000, v145
	v_rcp_f32_e32 v63, v63
	v_pk_fma_f32 v[50:51], v[50:51], v[138:139], v[144:145]
	v_lshlrev_b32_e32 v138, 16, v151
	v_and_b32_e32 v139, 0xffff0000, v151
	v_lshlrev_b32_e32 v144, 16, v147
	v_and_b32_e32 v145, 0xffff0000, v147
	v_pk_fma_f32 v[54:55], v[54:55], v[138:139], v[144:145]
	v_pk_mul_f32 v[138:139], v[48:49], v[48:49]
	v_pk_mul_f32 v[144:145], v[50:51], v[50:51]
	v_lshlrev_b32_e32 v142, 16, v161
	v_and_b32_e32 v143, 0xffff0000, v161
	v_pk_mul_f32 v[146:147], v[52:53], v[52:53]
	v_add_f32_e32 v144, v144, v145
	v_add_f32_e32 v138, v138, v139
	v_pk_fma_f32 v[58:59], v[58:59], v[142:143], v[152:153]
	v_lshlrev_b32_e32 v140, 16, v163
	v_and_b32_e32 v141, 0xffff0000, v163
	v_lshlrev_b32_e32 v142, 16, v167
	v_and_b32_e32 v143, 0xffff0000, v167
	v_pk_mul_f32 v[148:149], v[54:55], v[54:55]
	v_add_f32_e32 v138, v138, v144
	v_add_f32_e32 v139, v146, v147
	v_pk_fma_f32 v[62:63], v[62:63], v[140:141], v[142:143]
	v_pk_mul_f32 v[140:141], v[56:57], v[56:57]
	v_pk_mul_f32 v[142:143], v[58:59], v[58:59]
	v_add_f32_e32 v137, v148, v149
	v_add_f32_e32 v138, v139, v138
	v_pk_mul_f32 v[152:153], v[60:61], v[60:61]
	v_add_f32_e32 v137, v137, v138
	v_add_f32_e32 v138, v142, v143
	v_add_f32_e32 v139, v140, v141
	v_pk_mul_f32 v[154:155], v[62:63], v[62:63]
	v_add_f32_e32 v138, v139, v138
	v_add_f32_e32 v139, v152, v153
	v_add_f32_e32 v138, v139, v138
	v_add_f32_e32 v139, v154, v155
	v_add_f32_e32 v138, v139, v138
	v_add_f32_e32 v137, v138, v137
	v_mov_b32_e32 v138, v137
	s_nop 1
	v_permlane16_swap_b32_e32 v138, v137
	s_waitcnt vmcnt(2)
	v_lshlrev_b32_e32 v142, 16, v172
	v_and_b32_e32 v143, 0xffff0000, v172
	v_lshlrev_b32_e32 v144, 16, v173
	v_and_b32_e32 v145, 0xffff0000, v173
	s_waitcnt lgkmcnt(0)
	v_add_f32_e32 v137, v137, v138
	v_mov_b32_e32 v138, v137
	s_nop 1
	v_permlane32_swap_b32_e32 v138, v137
	s_waitcnt lgkmcnt(0)
	v_add_f32_e32 v137, v137, v138
	v_fmamk_f32 v138, v227, 0x3a800000, v221
	v_cmp_gt_f32_e32 vcc, s11, v138
	v_mul_f32_e32 v139, 0x4b800000, v138
	s_nop 0
	v_cndmask_b32_e32 v138, v138, v139, vcc
	v_rsq_f32_e32 v138, v138
	s_nop 0
	v_mul_f32_e32 v139, 0x45800000, v138
	v_cndmask_b32_e32 v138, v138, v139, vcc
	v_pk_mul_f32 v[148:149], v[34:35], v[138:139] op_sel_hi:[1,0]
	v_pk_mul_f32 v[34:35], v[32:33], v[138:139] op_sel_hi:[1,0]
	v_pk_mul_f32 v[140:141], v[42:43], v[138:139] op_sel_hi:[1,0]
	v_mul_f32_e32 v33, 0xbfb8aa3b, v34
	v_pk_mul_f32 v[42:43], v[40:41], v[138:139] op_sel_hi:[1,0]
	v_exp_f32_e32 v33, v33
	v_mul_f32_e32 v41, 0xbfb8aa3b, v42
	v_exp_f32_e32 v41, v41
	v_pk_mul_f32 v[36:37], v[36:37], v[138:139] op_sel_hi:[1,0]
	v_add_f32_e32 v33, 1.0, v33
	v_mul_f32_e32 v32, 0xbfb8aa3b, v36
	v_rcp_f32_e32 v34, v33
	v_mul_f32_e32 v33, 0xbfb8aa3b, v37
	v_pk_mul_f32 v[44:45], v[44:45], v[138:139] op_sel_hi:[1,0]
	v_add_f32_e32 v41, 1.0, v41
	v_exp_f32_e32 v32, v32
	v_exp_f32_e32 v33, v33
	v_mul_f32_e32 v35, 0xbfb8aa3b, v35
	v_mul_f32_e32 v40, 0xbfb8aa3b, v44
	v_rcp_f32_e32 v42, v41
	v_mul_f32_e32 v41, 0xbfb8aa3b, v45
	v_exp_f32_e32 v35, v35
	v_exp_f32_e32 v40, v40
	v_exp_f32_e32 v41, v41
	v_mul_f32_e32 v43, 0xbfb8aa3b, v43
	v_exp_f32_e32 v43, v43
	v_add_f32_e32 v32, 1.0, v32
	v_add_f32_e32 v33, 1.0, v33
	v_rcp_f32_e32 v32, v32
	v_rcp_f32_e32 v33, v33
	v_add_f32_e32 v35, 1.0, v35
	v_add_f32_e32 v40, 1.0, v40
	v_add_f32_e32 v41, 1.0, v41
	v_rcp_f32_e32 v35, v35
	v_rcp_f32_e32 v40, v40
	v_rcp_f32_e32 v41, v41
	v_add_f32_e32 v43, 1.0, v43
	v_pk_mul_f32 v[46:47], v[46:47], v[138:139] op_sel_hi:[1,0]
	v_rcp_f32_e32 v43, v43
	v_pk_mul_f32 v[38:39], v[38:39], v[138:139] op_sel_hi:[1,0]
	s_waitcnt vmcnt(1)
; __device__ __forceinline__ float sigm(float x) { return __builtin_amdgcn_rcpf(1.0f + __builtin_amdgcn_exp2f(-1.4426950408889634f * x)); }
; __device__ __forceinline__ void unpack8(const u32x4& w, f32x4& v0, f32x4& v1) { v0[0] = bf_lo(w.x); v0[1] = bf_hi(w.x); v0[2] = bf_lo(w.y); v0[3] = bf_hi(w.y); v1[0] = bf_lo(w.z); v1[1] = bf_hi(w.z); v1[2] = bf_lo(w.w); v1[3] = bf_hi(w.w); }
; #define PG8_ELD(k) do { const size_t o_ = ob + (size_t)(((k) >> 2) * HALF + ((k) & 3) * 16) * 1024; eq[k][0] = *(const u32x4*)(e + o_); xq[k][0] = *(const u32x4*)(x2 + o_); eq[k][1] = *(const u32x4*)(e + o_ + 32); xq[k][1] = *(const u32x4*)(x2 + o_ + 32); } while (0)
;     __device__ __forceinline__ void run(f32x4 (&acc)[2][2][4][2], const Unit& u, int wr, int wc, int fr, int fq, PG8_LAS unsigned char* lds, int wid) const {
;     ...
;         for (int k = 0; k < 8; ++k) { const int ai = k >> 2, m = k & 3; float s = 0.f;
;             if (k + 2 < 8) PG8_ELD(k + 2);
;             const float rstd = rsqrtf(sq8[k] * (1.0f / 1024.0f) + 1e-6f);
; #pragma unroll
;             for (int bj = 0; bj < 2; ++bj) { f32x4 v0 = acc[ai][bj][m][0] * rstd, v1 = acc[ai][bj][m][1] * rstd, e0, e1, r0, r1; unpack8(eq[k][bj], e0, e1); unpack8(xq[k][bj], r0, r1);
; #pragma unroll
;                 for (int i = 0; i < 4; ++i) { v0[i] = r0[i] + sigm(v0[i]) * e0[i]; v1[i] = r1[i] + sigm(v1[i]) * e1[i]; }
;                 s += (v0[0] * v0[0] + v0[1] * v0[1]) + (v0[2] * v0[2] + v0[3] * v0[3]) + (v1[0] * v1[0] + v1[1] * v1[1]) + (v1[2] * v1[2] + v1[3] * v1[3]);
;                 acc[ai][bj][m][0] = v0; acc[ai][bj][m][1] = v1; }
;             s += __shfl_xor(s, 16); s += __shfl_xor(s, 32); sv[k] = s;
;             asm volatile("" : "+v"(acc[ai][0][m][0]), "+v"(acc[ai][0][m][1]), "+v"(acc[ai][1][m][0]), "+v"(acc[ai][1][m][1]), "+v"(sv[k]) :: "memory"); }
;     ...
;         if (fq == 0) {
; #pragma unroll
;             for (int k = 0; k < 8; ++k) atomicAdd(ssq3 + row0 + (k >> 2) * HALF + (k & 3) * 16, sv[k]); }
	v_lshlrev_b32_e32 v36, 16, v132
	v_and_b32_e32 v37, 0xffff0000, v132
	s_waitcnt vmcnt(0)
	v_lshlrev_b32_e32 v138, 16, v128
	v_and_b32_e32 v139, 0xffff0000, v128
	v_pk_fma_f32 v[32:33], v[32:33], v[36:37], v[138:139]
	v_lshlrev_b32_e32 v36, 16, v134
	v_and_b32_e32 v37, 0xffff0000, v134
	v_lshlrev_b32_e32 v138, 16, v130
	v_and_b32_e32 v139, 0xffff0000, v130
	v_lshlrev_b32_e32 v44, 16, v168
	v_and_b32_e32 v45, 0xffff0000, v168
	v_pk_fma_f32 v[36:37], v[34:35], v[36:37], v[138:139]
	v_mul_f32_e32 v35, 0xbfb8aa3b, v148
	v_pk_fma_f32 v[40:41], v[40:41], v[44:45], v[142:143]
	v_lshlrev_b32_e32 v44, 16, v170
	v_and_b32_e32 v45, 0xffff0000, v170
	v_lshlrev_b32_e32 v142, 16, v174
	v_and_b32_e32 v143, 0xffff0000, v174
	v_exp_f32_e32 v35, v35
	v_pk_fma_f32 v[44:45], v[42:43], v[44:45], v[142:143]
	v_mul_f32_e32 v43, 0xbfb8aa3b, v140
	v_exp_f32_e32 v43, v43
	v_add_f32_e32 v35, 1.0, v35
	v_mul_f32_e32 v34, 0xbfb8aa3b, v38
	v_rcp_f32_e32 v38, v35
	v_mul_f32_e32 v35, 0xbfb8aa3b, v39
	v_add_f32_e32 v43, 1.0, v43
	v_exp_f32_e32 v34, v34
	v_exp_f32_e32 v35, v35
	v_mul_f32_e32 v39, 0xbfb8aa3b, v149
	v_mul_f32_e32 v42, 0xbfb8aa3b, v46
	v_rcp_f32_e32 v46, v43
	v_mul_f32_e32 v43, 0xbfb8aa3b, v47
	v_exp_f32_e32 v39, v39
	v_exp_f32_e32 v42, v42
	v_exp_f32_e32 v43, v43
	v_mul_f32_e32 v47, 0xbfb8aa3b, v141
	v_exp_f32_e32 v47, v47
	v_add_f32_e32 v34, 1.0, v34
	v_add_f32_e32 v35, 1.0, v35
	v_rcp_f32_e32 v34, v34
	v_rcp_f32_e32 v35, v35
	v_add_f32_e32 v39, 1.0, v39
	v_add_f32_e32 v42, 1.0, v42
	v_add_f32_e32 v43, 1.0, v43
	v_rcp_f32_e32 v39, v39
	v_rcp_f32_e32 v42, v42
	v_rcp_f32_e32 v43, v43
	v_add_f32_e32 v47, 1.0, v47
	v_rcp_f32_e32 v47, v47
	v_lshlrev_b32_e32 v132, 16, v133
	v_and_b32_e32 v133, 0xffff0000, v133
	v_lshlrev_b32_e32 v128, 16, v129
	v_and_b32_e32 v129, 0xffff0000, v129
	v_pk_fma_f32 v[34:35], v[34:35], v[132:133], v[128:129]
	v_lshlrev_b32_e32 v128, 16, v135
	v_and_b32_e32 v129, 0xffff0000, v135
	v_lshlrev_b32_e32 v130, 16, v131
	v_and_b32_e32 v131, 0xffff0000, v131
	v_lshlrev_b32_e32 v142, 16, v169
	v_and_b32_e32 v143, 0xffff0000, v169
	v_pk_fma_f32 v[38:39], v[38:39], v[128:129], v[130:131]
	v_pk_mul_f32 v[128:129], v[32:33], v[32:33]
	v_pk_mul_f32 v[130:131], v[34:35], v[34:35]
	v_pk_fma_f32 v[42:43], v[42:43], v[142:143], v[144:145]
	v_lshlrev_b32_e32 v140, 16, v171
	v_and_b32_e32 v141, 0xffff0000, v171
	v_lshlrev_b32_e32 v142, 16, v175
	v_and_b32_e32 v143, 0xffff0000, v175
	v_pk_mul_f32 v[132:133], v[36:37], v[36:37]
	v_add_f32_e32 v130, v130, v131
	v_add_f32_e32 v128, v128, v129
	v_pk_fma_f32 v[46:47], v[46:47], v[140:141], v[142:143]
	v_pk_mul_f32 v[140:141], v[40:41], v[40:41]
	v_pk_mul_f32 v[142:143], v[42:43], v[42:43]
	v_add_f32_e32 v128, v128, v130
	v_add_f32_e32 v129, v132, v133
	v_pk_mul_f32 v[144:145], v[44:45], v[44:45]
	v_add_f32_e32 v128, v129, v128
	v_add_f32_e32 v129, v142, v143
	v_add_f32_e32 v130, v140, v141
	v_pk_mul_f32 v[146:147], v[46:47], v[46:47]
	v_pk_mul_f32 v[134:135], v[38:39], v[38:39]
	v_add_f32_e32 v129, v130, v129
	v_add_f32_e32 v130, v144, v145
	v_add_f32_e32 v134, v134, v135
	v_add_f32_e32 v129, v130, v129
	v_add_f32_e32 v130, v146, v147
	v_add_f32_e32 v128, v134, v128
	v_add_f32_e32 v129, v130, v129
	v_add_f32_e32 v128, v129, v128
	v_mov_b32_e32 v129, v128
	s_nop 1
	v_permlane16_swap_b32_e32 v129, v128
	v_lshl_add_u64 v[142:143], v[206:207], 2, s[34:35]
	s_waitcnt lgkmcnt(0)
	v_add_f32_e32 v128, v128, v129
	v_mov_b32_e32 v129, v128
	s_nop 1
	v_permlane32_swap_b32_e32 v129, v128
	s_waitcnt lgkmcnt(0)
	v_add_f32_e32 v128, v128, v129
	s_and_saveexec_b64 s[78:79], s[4:5]
	s_cbranch_execz .LBB0_1663
	global_atomic_add_f32 v[142:143], v228, off
	global_atomic_add_f32 v[142:143], v230, off offset:64
	global_atomic_add_f32 v[142:143], v232, off offset:128
	global_atomic_add_f32 v[142:143], v234, off offset:192
	global_atomic_add_f32 v[142:143], v176, off offset:512
	global_atomic_add_f32 v[142:143], v136, off offset:576
	global_atomic_add_f32 v[142:143], v137, off offset:640
	global_atomic_add_f32 v[142:143], v128, off offset:704

; __device__ __forceinline__ void unpk8(const v4u w, float* f) { f[0] = bf_lo(w.x); f[1] = bf_hi(w.x); f[2] = bf_lo(w.y); f[3] = bf_hi(w.y); f[4] = bf_lo(w.z); f[5] = bf_hi(w.z); f[6] = bf_lo(w.w); f[7] = bf_hi(w.w); }
; __device__ __forceinline__ float wave_sum(float v) {
; #pragma unroll
;     for (int o = 1; o < 64; o <<= 1) v += __shfl_xor(v, o);
;     return v;
; }
; __global__ void __launch_bounds__(512, 2) mk_fwd(Params P) {
;     ...
;         for (int m = gw; m < NTOK; m += NGW) {
;             const bf16* xr = (const bf16*)(ws + WS_X3B) + (size_t)m * 1024; float v[16]; float s = 0.f;
;             unpk8(((const v4u*)xr)[2 * lane], v); unpk8(((const v4u*)xr)[2 * lane + 1], v + 8);
; #pragma unroll
;             for (int i = 0; i < 16; ++i) s += v[i] * v[i];
;             const float rstd = rsqrtf(wave_sum(s) * (1.f / 1024.f) + EPS);
;             float* orow = P.out + (size_t)m * 1024 + 16 * lane;
; #pragma unroll
;             for (int j = 0; j < 4; ++j) { const f32x4 g = ((const f32x4*)(gf + 16 * lane))[j]; f32x4 o; o[0] = v[4 * j] * rstd * g[0]; o[1] = v[4 * j + 1] * rstd * g[1]; o[2] = v[4 * j + 2] * rstd * g[2]; o[3] = v[4 * j + 3] * rstd * g[3]; ((f32x4*)orow)[j] = o; }
.LBB0_1738:
	global_load_dwordx4 v[14:17], v[2:3], off
	global_load_dwordx4 v[18:21], v[2:3], off offset:16
	global_load_dwordx4 v[22:25], v[0:1], off
	s_add_i32 s60, s60, s62
	v_lshl_add_u64 v[2:3], v[2:3], 0, s[0:1]
	s_cmp_lt_i32 s60, 0x8000
	s_waitcnt vmcnt(2)
	v_lshlrev_b32_e32 v26, 16, v14
	v_and_b32_e32 v27, 0xffff0000, v14
	v_lshlrev_b32_e32 v14, 16, v15
	v_and_b32_e32 v15, 0xffff0000, v15
	v_lshlrev_b32_e32 v28, 16, v16
	v_and_b32_e32 v29, 0xffff0000, v16
	v_lshlrev_b32_e32 v30, 16, v17
	v_and_b32_e32 v31, 0xffff0000, v17
	v_pk_mul_f32 v[16:17], v[26:27], v[26:27]
	v_pk_mul_f32 v[36:37], v[14:15], v[14:15]
	v_add_f32_e32 v13, v16, v17
	v_add_f32_e32 v13, v13, v36
	v_pk_mul_f32 v[38:39], v[28:29], v[28:29]
	v_add_f32_e32 v13, v13, v37
	v_add_f32_e32 v13, v13, v38
	v_pk_mul_f32 v[40:41], v[30:31], v[30:31]
	v_add_f32_e32 v13, v13, v39
	s_waitcnt vmcnt(1)
	v_lshlrev_b32_e32 v32, 16, v18
	v_and_b32_e32 v33, 0xffff0000, v18
	v_add_f32_e32 v13, v13, v40
	v_pk_mul_f32 v[42:43], v[32:33], v[32:33]
	v_add_f32_e32 v13, v13, v41
	v_lshlrev_b32_e32 v18, 16, v19
	v_and_b32_e32 v19, 0xffff0000, v19
	v_add_f32_e32 v13, v13, v42
	v_pk_mul_f32 v[44:45], v[18:19], v[18:19]
	v_add_f32_e32 v13, v13, v43
	v_lshlrev_b32_e32 v34, 16, v20
	v_and_b32_e32 v35, 0xffff0000, v20
	v_add_f32_e32 v13, v13, v44
	v_pk_mul_f32 v[46:47], v[34:35], v[34:35]
	v_add_f32_e32 v13, v13, v45
	v_lshlrev_b32_e32 v20, 16, v21
	v_and_b32_e32 v21, 0xffff0000, v21
	v_add_f32_e32 v13, v13, v46
	v_pk_mul_f32 v[48:49], v[20:21], v[20:21]
	v_add_f32_e32 v13, v13, v47
	v_add_f32_e32 v13, v13, v48
	v_add_f32_e32 v13, v13, v49
	ds_bpermute_b32 v16, v6, v13
	s_waitcnt lgkmcnt(0)
	v_add_f32_e32 v13, v13, v16
	ds_bpermute_b32 v16, v7, v13
	s_waitcnt lgkmcnt(0)
	v_add_f32_e32 v13, v13, v16
	ds_bpermute_b32 v16, v8, v13
	s_waitcnt lgkmcnt(0)
	v_add_f32_e32 v13, v13, v16
	ds_bpermute_b32 v16, v9, v13
	s_waitcnt lgkmcnt(0)
	v_add_f32_e32 v13, v13, v16
	v_mov_b32_e32 v16, v13
	s_nop 1
	v_permlane16_swap_b32_e32 v16, v13
	s_waitcnt lgkmcnt(0)
	v_add_f32_e32 v13, v13, v16
	v_mov_b32_e32 v16, v13
	s_nop 1
	v_permlane32_swap_b32_e32 v16, v13
	s_waitcnt lgkmcnt(0)
	v_add_f32_e32 v13, v13, v16
	v_fmamk_f32 v13, v13, 0x3a800000, v12
	v_mul_f32_e32 v16, 0x4b800000, v13
	v_cmp_gt_f32_e32 vcc, s4, v13
	s_nop 1
	v_cndmask_b32_e32 v13, v13, v16, vcc
	v_rsq_f32_e32 v13, v13
	s_nop 0
	v_mul_f32_e32 v16, 0x45800000, v13
	v_cndmask_b32_e32 v36, v13, v16, vcc
	v_pk_mul_f32 v[26:27], v[36:37], v[26:27] op_sel_hi:[0,1]
	v_pk_mul_f32 v[14:15], v[36:37], v[14:15] op_sel_hi:[0,1]
	s_waitcnt vmcnt(0)
	v_pk_mul_f32 v[16:17], v[14:15], v[24:25]
	v_pk_mul_f32 v[14:15], v[26:27], v[22:23]
	global_store_dwordx4 v[4:5], v[14:17], off
	global_load_dwordx4 v[14:17], v[0:1], off offset:16
	v_pk_mul_f32 v[22:23], v[36:37], v[30:31] op_sel_hi:[0,1]
	v_pk_mul_f32 v[24:25], v[36:37], v[28:29] op_sel_hi:[0,1]
	v_pk_mul_f32 v[18:19], v[36:37], v[18:19] op_sel_hi:[0,1]
	s_waitcnt vmcnt(0)
	v_pk_mul_f32 v[14:15], v[24:25], v[14:15]
	v_pk_mul_f32 v[16:17], v[22:23], v[16:17]
	global_store_dwordx4 v[4:5], v[14:17], off offset:16
	global_load_dwordx4 v[14:17], v[0:1], off offset:32
	v_pk_mul_f32 v[22:23], v[36:37], v[32:33] op_sel_hi:[0,1]
	s_waitcnt vmcnt(0)
	v_pk_mul_f32 v[14:15], v[22:23], v[14:15]
	v_pk_mul_f32 v[16:17], v[18:19], v[16:17]
	global_store_dwordx4 v[4:5], v[14:17], off offset:32
	global_load_dwordx4 v[14:17], v[0:1], off offset:48
	v_pk_mul_f32 v[18:19], v[36:37], v[20:21] op_sel_hi:[0,1]
	v_pk_mul_f32 v[20:21], v[36:37], v[34:35] op_sel_hi:[0,1]
	s_waitcnt vmcnt(0)
	v_pk_mul_f32 v[14:15], v[20:21], v[14:15]
	v_pk_mul_f32 v[16:17], v[18:19], v[16:17]
	global_store_dwordx4 v[4:5], v[14:17], off offset:48
	v_lshl_add_u64 v[4:5], v[4:5], 0, s[2:3]
	s_cbranch_scc1 .LBB0_1738
